# no-op lgkmcnt waits inside MFMA clusters removed (setprio left behind the barrier), ragged-tile test in front of the barrier
# speedup vs baseline: 1.0014x; 1.0008x over previous
.Lz1_a:
	s_waitcnt vmcnt(8)
	s_waitcnt lgkmcnt(0)
	s_barrier
	s_setprio 1
	v_mfma_scale_f32_16x16x128_f8f6f4 v[124:127], v[146:153], v[178:185], v[124:127], v143, v143 op_sel_hi:[0,0,0]
	v_mfma_scale_f32_16x16x128_f8f6f4 v[120:123], v[154:161], v[178:185], v[120:123], v143, v143 op_sel_hi:[0,0,0]
	v_mfma_scale_f32_16x16x128_f8f6f4 v[108:111], v[146:153], v[186:193], v[108:111], v143, v143 op_sel_hi:[0,0,0]
	v_mfma_scale_f32_16x16x128_f8f6f4 v[104:107], v[154:161], v[186:193], v[104:107], v143, v143 op_sel_hi:[0,0,0]
	v_mfma_scale_f32_16x16x128_f8f6f4 v[130:133], v[146:153], v[194:201], v[92:95], v143, v143 op_sel_hi:[0,0,0]
	v_mfma_scale_f32_16x16x128_f8f6f4 v[210:213], v[154:161], v[194:201], v[88:91], v143, v143 op_sel_hi:[0,0,0]
	v_mfma_scale_f32_16x16x128_f8f6f4 v[214:217], v[146:153], v[202:209], v[76:79], v143, v143 op_sel_hi:[0,0,0]
	v_mfma_scale_f32_16x16x128_f8f6f4 v[218:221], v[154:161], v[202:209], v[72:75], v143, v143 op_sel_hi:[0,0,0]
	s_setprio 0
	s_setprio 1
	v_mfma_scale_f32_16x16x128_f8f6f4 v[116:119], v[162:169], v[178:185], v[116:119], v143, v143 op_sel_hi:[0,0,0]
	v_mfma_scale_f32_16x16x128_f8f6f4 v[112:115], v[170:177], v[178:185], v[112:115], v143, v143 op_sel_hi:[0,0,0]
	v_mfma_scale_f32_16x16x128_f8f6f4 v[100:103], v[162:169], v[186:193], v[100:103], v143, v143 op_sel_hi:[0,0,0]
	v_mfma_scale_f32_16x16x128_f8f6f4 v[96:99], v[170:177], v[186:193], v[96:99], v143, v143 op_sel_hi:[0,0,0]
	v_mfma_scale_f32_16x16x128_f8f6f4 v[178:181], v[162:169], v[194:201], v[84:87], v143, v143 op_sel_hi:[0,0,0]
	v_mfma_scale_f32_16x16x128_f8f6f4 v[182:185], v[170:177], v[194:201], v[80:83], v143, v143 op_sel_hi:[0,0,0]
	v_mfma_scale_f32_16x16x128_f8f6f4 v[186:189], v[162:169], v[202:209], v[68:71], v143, v143 op_sel_hi:[0,0,0]
	v_mfma_scale_f32_16x16x128_f8f6f4 v[190:193], v[170:177], v[202:209], v[64:67], v143, v143 op_sel_hi:[0,0,0]
	s_setprio 0
	s_barrier
	s_nop 4
	ds_read_b128 v[64:67], v142 offset:16384
	ds_read_b128 v[68:71], v142 offset:17408
	ds_read_b128 v[72:75], v142 offset:18432
	ds_read_b128 v[76:79], v142 offset:19456
	ds_read_b128 v[80:83], v142 offset:20480
	ds_read_b128 v[84:87], v142 offset:21504
	ds_read_b128 v[88:91], v142 offset:22528
	ds_read_b128 v[92:95], v142 offset:23552
	s_mov_b32 s0, m0
	s_mov_b32 m0, s19
	s_nop 2
	global_load_lds_dwordx4 v136, s[84:85]
	s_mov_b32 m0, s0
	s_nop 0
	s_mov_b32 s0, m0
	s_mov_b32 m0, s40
	s_nop 2
	global_load_lds_dwordx4 v137, s[84:85]
	s_mov_b32 m0, s0
	s_nop 0
	s_mov_b32 s0, m0
	s_mov_b32 m0, s41
	s_nop 2
	global_load_lds_dwordx4 v136, s[62:63]
	s_mov_b32 m0, s0
	s_nop 0
	s_mov_b32 s0, m0
	s_mov_b32 m0, s42
	s_nop 2
	global_load_lds_dwordx4 v137, s[62:63]
	s_mov_b32 m0, s0
	s_nop 0
	s_mov_b32 s0, m0
	s_mov_b32 m0, s97
	s_nop 2
	global_load_lds_dwordx4 v138, s[80:81]
	s_mov_b32 m0, s0
	s_nop 0
	s_mov_b32 s0, m0
	s_mov_b32 m0, s43
	s_nop 2
	global_load_lds_dwordx4 v139, s[80:81]
	s_mov_b32 m0, s0
	s_cmp_lg_u32 s9, -2
	s_cbranch_scc1 .Lz1_b
	v_mov_b32_e32 v60, 0
	v_mov_b32_e32 v61, 0
	v_pk_mov_b32 v[62:63], v[60:61], v[60:61]
	v_pk_mov_b32 v[56:57], v[60:61], v[60:61]
	v_pk_mov_b32 v[58:59], v[60:61], v[60:61]
	v_pk_mov_b32 v[44:45], v[60:61], v[60:61]
	v_pk_mov_b32 v[46:47], v[60:61], v[60:61]
	v_pk_mov_b32 v[40:41], v[60:61], v[60:61]
	v_pk_mov_b32 v[42:43], v[60:61], v[60:61]
	v_pk_mov_b32 v[28:29], v[60:61], v[60:61]
	v_pk_mov_b32 v[30:31], v[60:61], v[60:61]
	v_pk_mov_b32 v[24:25], v[60:61], v[60:61]
	v_pk_mov_b32 v[26:27], v[60:61], v[60:61]
	v_pk_mov_b32 v[12:13], v[60:61], v[60:61]
	v_pk_mov_b32 v[14:15], v[60:61], v[60:61]
	v_pk_mov_b32 v[0:1], v[60:61], v[60:61]
	v_pk_mov_b32 v[2:3], v[60:61], v[60:61]
	v_pk_mov_b32 v[52:53], v[60:61], v[60:61]
	v_pk_mov_b32 v[54:55], v[60:61], v[60:61]
	v_pk_mov_b32 v[48:49], v[60:61], v[60:61]
	v_pk_mov_b32 v[50:51], v[60:61], v[60:61]
	v_pk_mov_b32 v[36:37], v[60:61], v[60:61]
	v_pk_mov_b32 v[38:39], v[60:61], v[60:61]
	v_pk_mov_b32 v[32:33], v[60:61], v[60:61]
	v_pk_mov_b32 v[34:35], v[60:61], v[60:61]
	v_pk_mov_b32 v[20:21], v[60:61], v[60:61]
	v_pk_mov_b32 v[22:23], v[60:61], v[60:61]
	v_pk_mov_b32 v[16:17], v[60:61], v[60:61]
	v_pk_mov_b32 v[18:19], v[60:61], v[60:61]
	v_pk_mov_b32 v[8:9], v[60:61], v[60:61]
	v_pk_mov_b32 v[10:11], v[60:61], v[60:61]
	v_pk_mov_b32 v[4:5], v[60:61], v[60:61]
	v_pk_mov_b32 v[6:7], v[60:61], v[60:61]
.Lz1_b:
	s_waitcnt vmcnt(8)
	s_waitcnt lgkmcnt(0)
	s_barrier
	s_setprio 1
	v_mfma_scale_f32_16x16x128_f8f6f4 v[60:63], v[146:153], v[64:71], v[60:63], v143, v143 op_sel_hi:[0,0,0]
	v_mfma_scale_f32_16x16x128_f8f6f4 v[56:59], v[154:161], v[64:71], v[56:59], v143, v143 op_sel_hi:[0,0,0]
	v_mfma_scale_f32_16x16x128_f8f6f4 v[194:197], v[146:153], v[72:79], v[44:47], v143, v143 op_sel_hi:[0,0,0]
	v_mfma_scale_f32_16x16x128_f8f6f4 v[198:201], v[154:161], v[72:79], v[40:43], v143, v143 op_sel_hi:[0,0,0]
	v_mfma_scale_f32_16x16x128_f8f6f4 v[202:205], v[146:153], v[80:87], v[28:31], v143, v143 op_sel_hi:[0,0,0]
	v_mfma_scale_f32_16x16x128_f8f6f4 v[206:209], v[154:161], v[80:87], v[24:27], v143, v143 op_sel_hi:[0,0,0]
	v_mfma_scale_f32_16x16x128_f8f6f4 v[222:225], v[146:153], v[88:95], v[12:15], v143, v143 op_sel_hi:[0,0,0]
	v_mfma_scale_f32_16x16x128_f8f6f4 v[226:229], v[154:161], v[88:95], v[0:3], v143, v143 op_sel_hi:[0,0,0]
	s_setprio 0
	s_setprio 1
	v_mfma_scale_f32_16x16x128_f8f6f4 v[52:55], v[162:169], v[64:71], v[52:55], v143, v143 op_sel_hi:[0,0,0]
	v_mfma_scale_f32_16x16x128_f8f6f4 v[48:51], v[170:177], v[64:71], v[48:51], v143, v143 op_sel_hi:[0,0,0]
	v_mfma_scale_f32_16x16x128_f8f6f4 v[230:233], v[162:169], v[72:79], v[36:39], v143, v143 op_sel_hi:[0,0,0]
	v_mfma_scale_f32_16x16x128_f8f6f4 v[234:237], v[170:177], v[72:79], v[32:35], v143, v143 op_sel_hi:[0,0,0]
	v_mfma_scale_f32_16x16x128_f8f6f4 v[238:241], v[162:169], v[80:87], v[20:23], v143, v143 op_sel_hi:[0,0,0]
	v_mfma_scale_f32_16x16x128_f8f6f4 v[242:245], v[170:177], v[80:87], v[16:19], v143, v143 op_sel_hi:[0,0,0]
	v_mfma_scale_f32_16x16x128_f8f6f4 v[246:249], v[162:169], v[88:95], v[8:11], v143, v143 op_sel_hi:[0,0,0]
	v_mfma_scale_f32_16x16x128_f8f6f4 v[250:253], v[170:177], v[88:95], v[4:7], v143, v143 op_sel_hi:[0,0,0]
	s_setprio 0
	s_barrier
	ds_read_b128 v[0:3], v144
	s_nop 3
	ds_read_b128 v[4:7], v144 offset:1024
	ds_read_b128 v[16:19], v144 offset:2048
	ds_read_b128 v[20:23], v144 offset:3072
	ds_read_b128 v[146:149], v145
	ds_read_b128 v[150:153], v145 offset:1024
	ds_read_b128 v[154:157], v145 offset:2048
	ds_read_b128 v[158:161], v145 offset:3072
	ds_read_b128 v[8:11], v142 offset:32768
	ds_read_b128 v[12:15], v142 offset:33792
	ds_read_b128 v[24:27], v142 offset:34816
	ds_read_b128 v[28:31], v142 offset:35840
	ds_read_b128 v[32:35], v142 offset:36864
	ds_read_b128 v[36:39], v142 offset:37888
	ds_read_b128 v[40:43], v142 offset:38912
	ds_read_b128 v[44:47], v142 offset:39936
	s_add_u32 s34, s80, 0x40000
	s_addc_u32 s35, s81, 0
	s_mov_b32 s0, m0
	s_mov_b32 m0, s44
	s_nop 2
	global_load_lds_dwordx4 v138, s[34:35]
	s_mov_b32 m0, s0
	s_nop 0
	s_mov_b32 s0, m0
	s_mov_b32 m0, s45
	s_nop 2
	global_load_lds_dwordx4 v139, s[34:35]
	s_mov_b32 m0, s0
	s_waitcnt vmcnt(8)
	s_waitcnt lgkmcnt(0)
	s_barrier
	s_setprio 1
	v_mfma_scale_f32_16x16x128_f8f6f4 v[124:127], v[0:7], v[8:15], v[124:127], v143, v143 op_sel_hi:[0,0,0]
	v_mfma_scale_f32_16x16x128_f8f6f4 v[120:123], v[16:23], v[8:15], v[120:123], v143, v143 op_sel_hi:[0,0,0]
	v_mfma_scale_f32_16x16x128_f8f6f4 v[108:111], v[0:7], v[24:31], v[108:111], v143, v143 op_sel_hi:[0,0,0]
	v_mfma_scale_f32_16x16x128_f8f6f4 v[104:107], v[16:23], v[24:31], v[104:107], v143, v143 op_sel_hi:[0,0,0]
	v_mfma_scale_f32_16x16x128_f8f6f4 v[92:95], v[0:7], v[32:39], v[130:133], v143, v143 op_sel_hi:[0,0,0]
	v_mfma_scale_f32_16x16x128_f8f6f4 v[88:91], v[16:23], v[32:39], v[210:213], v143, v143 op_sel_hi:[0,0,0]
	v_mfma_scale_f32_16x16x128_f8f6f4 v[76:79], v[0:7], v[40:47], v[214:217], v143, v143 op_sel_hi:[0,0,0]
	v_mfma_scale_f32_16x16x128_f8f6f4 v[72:75], v[16:23], v[40:47], v[218:221], v143, v143 op_sel_hi:[0,0,0]
	s_setprio 0
	s_setprio 1
	v_mfma_scale_f32_16x16x128_f8f6f4 v[116:119], v[146:153], v[8:15], v[116:119], v143, v143 op_sel_hi:[0,0,0]
	v_mfma_scale_f32_16x16x128_f8f6f4 v[112:115], v[154:161], v[8:15], v[112:115], v143, v143 op_sel_hi:[0,0,0]
	v_mfma_scale_f32_16x16x128_f8f6f4 v[100:103], v[146:153], v[24:31], v[100:103], v143, v143 op_sel_hi:[0,0,0]
	v_mfma_scale_f32_16x16x128_f8f6f4 v[96:99], v[154:161], v[24:31], v[96:99], v143, v143 op_sel_hi:[0,0,0]
	v_mfma_scale_f32_16x16x128_f8f6f4 v[84:87], v[146:153], v[32:39], v[178:181], v143, v143 op_sel_hi:[0,0,0]
	v_mfma_scale_f32_16x16x128_f8f6f4 v[80:83], v[154:161], v[32:39], v[182:185], v143, v143 op_sel_hi:[0,0,0]
	v_mfma_scale_f32_16x16x128_f8f6f4 v[68:71], v[146:153], v[40:47], v[186:189], v143, v143 op_sel_hi:[0,0,0]
	v_mfma_scale_f32_16x16x128_f8f6f4 v[64:67], v[154:161], v[40:47], v[190:193], v143, v143 op_sel_hi:[0,0,0]
	s_setprio 0
	s_barrier
	ds_read_b128 v[32:35], v142 offset:49152
	ds_read_b128 v[36:39], v142 offset:50176
	ds_read_b128 v[162:165], v142 offset:51200
	ds_read_b128 v[166:169], v142 offset:52224
	ds_read_b128 v[170:173], v142 offset:53248
	ds_read_b128 v[174:177], v142 offset:54272
	ds_read_b128 v[178:181], v142 offset:55296
	ds_read_b128 v[182:185], v142 offset:56320
	s_mov_b32 s0, m0
	s_mov_b32 m0, s46
	s_nop 2
	global_load_lds_dwordx4 v136, s[78:79]
	s_mov_b32 m0, s0
	s_add_u32 s34, s62, 0x80
	s_mov_b32 s0, m0
	s_mov_b32 m0, s48
	s_nop 2
	global_load_lds_dwordx4 v137, s[78:79]
	s_mov_b32 m0, s0
	s_addc_u32 s35, s63, 0
	s_mov_b32 s0, m0
	s_mov_b32 m0, s51
	s_nop 2
	global_load_lds_dwordx4 v136, s[34:35]
	s_mov_b32 m0, s0
	s_nop 0
	s_mov_b32 s0, m0
	s_mov_b32 m0, s52
	s_nop 2
	global_load_lds_dwordx4 v137, s[34:35]
	s_mov_b32 m0, s0
	s_nop 0
	s_mov_b32 s0, m0
	s_mov_b32 m0, s49
	s_nop 2
	global_load_lds_dwordx4 v138, s[76:77]
	s_mov_b32 m0, s0
	s_nop 0
	s_mov_b32 s0, m0
	s_mov_b32 m0, s50
	s_nop 2
	global_load_lds_dwordx4 v139, s[76:77]
	s_mov_b32 m0, s0
	s_waitcnt vmcnt(8)
	s_waitcnt lgkmcnt(0)
	s_barrier
	s_setprio 1
	v_mfma_scale_f32_16x16x128_f8f6f4 v[60:63], v[0:7], v[32:39], v[60:63], v143, v143 op_sel_hi:[0,0,0]
	v_mfma_scale_f32_16x16x128_f8f6f4 v[56:59], v[16:23], v[32:39], v[56:59], v143, v143 op_sel_hi:[0,0,0]
	v_mfma_scale_f32_16x16x128_f8f6f4 v[44:47], v[0:7], v[162:169], v[194:197], v143, v143 op_sel_hi:[0,0,0]
	v_mfma_scale_f32_16x16x128_f8f6f4 v[40:43], v[16:23], v[162:169], v[198:201], v143, v143 op_sel_hi:[0,0,0]
	v_mfma_scale_f32_16x16x128_f8f6f4 v[28:31], v[0:7], v[170:177], v[202:205], v143, v143 op_sel_hi:[0,0,0]
	v_mfma_scale_f32_16x16x128_f8f6f4 v[24:27], v[16:23], v[170:177], v[206:209], v143, v143 op_sel_hi:[0,0,0]
	v_mfma_scale_f32_16x16x128_f8f6f4 v[12:15], v[0:7], v[178:185], v[222:225], v143, v143 op_sel_hi:[0,0,0]
	v_mfma_scale_f32_16x16x128_f8f6f4 v[0:3], v[16:23], v[178:185], v[226:229], v143, v143 op_sel_hi:[0,0,0]
	s_setprio 0
	s_setprio 1
	v_mfma_scale_f32_16x16x128_f8f6f4 v[52:55], v[146:153], v[32:39], v[52:55], v143, v143 op_sel_hi:[0,0,0]
	v_mfma_scale_f32_16x16x128_f8f6f4 v[48:51], v[154:161], v[32:39], v[48:51], v143, v143 op_sel_hi:[0,0,0]
	v_mfma_scale_f32_16x16x128_f8f6f4 v[36:39], v[146:153], v[162:169], v[230:233], v143, v143 op_sel_hi:[0,0,0]
	v_mfma_scale_f32_16x16x128_f8f6f4 v[32:35], v[154:161], v[162:169], v[234:237], v143, v143 op_sel_hi:[0,0,0]
	v_mfma_scale_f32_16x16x128_f8f6f4 v[20:23], v[146:153], v[170:177], v[238:241], v143, v143 op_sel_hi:[0,0,0]
	v_mfma_scale_f32_16x16x128_f8f6f4 v[16:19], v[154:161], v[170:177], v[242:245], v143, v143 op_sel_hi:[0,0,0]
	v_mfma_scale_f32_16x16x128_f8f6f4 v[8:11], v[146:153], v[178:185], v[246:249], v143, v143 op_sel_hi:[0,0,0]
	v_mfma_scale_f32_16x16x128_f8f6f4 v[4:7], v[154:161], v[178:185], v[250:253], v143, v143 op_sel_hi:[0,0,0]
	s_setprio 0
	s_barrier
	s_add_i32 s9, s9, 2
	s_add_u32 s8, s8, 0x100
	s_addc_u32 s6, s6, 0
	s_add_u32 s7, s7, 0x100
	s_addc_u32 s33, s33, 0
	s_cmp_gt_u32 s9, 13
	s_mov_b64 s[34:35], s[36:37]
	s_cbranch_scc0 .LBB0_198
	s_and_b64 vcc, exec, s[16:17]
	s_cbranch_vccz .LBB0_201
	s_barrier

.LBB0_290:
	ds_read_b128 v[0:3], v134
	ds_read_b128 v[4:7], v134 offset:1024
	ds_read_b128 v[8:11], v134 offset:2048
	ds_read_b128 v[12:15], v134 offset:3072
	ds_read_b128 v[16:19], v135
	ds_read_b128 v[20:23], v135 offset:1024
	ds_read_b128 v[24:27], v135 offset:2048
	ds_read_b128 v[28:31], v135 offset:3072
	s_and_b64 s[34:35], s[26:27], exec
	s_cselect_b32 s37, s19, s29
	s_cselect_b32 s36, s18, s28
	s_cselect_b32 s63, s21, s57
	s_cselect_b32 s62, s20, s56
	s_cselect_b32 s35, s23, s31
	s_cselect_b32 s34, s22, s30
	s_add_u32 s78, s28, 0x100
	s_addc_u32 s79, s29, 0
	s_add_u32 s84, s56, 0x100
	s_addc_u32 s85, s57, 0
	s_add_u32 s80, s30, 0x100
	s_addc_u32 s81, s31, 0
	s_add_u32 s76, s56, 0x180
	s_addc_u32 s77, s57, 0
	s_add_u32 s56, s28, 0x180
	s_addc_u32 s57, s29, 0
	ds_read_b128 v[32:35], v136
	ds_read_b128 v[36:39], v136 offset:1024
	ds_read_b128 v[40:43], v136 offset:2048
	ds_read_b128 v[44:47], v136 offset:3072
	ds_read_b128 v[48:51], v136 offset:4096
	ds_read_b128 v[52:55], v136 offset:5120
	ds_read_b128 v[56:59], v136 offset:6144
	ds_read_b128 v[60:63], v136 offset:7168
	s_add_u32 s86, s28, 0x40080
	s_addc_u32 s87, s29, 0
	s_mov_b32 s7, m0
	s_mov_b32 m0, s54
	s_nop 2
	global_load_lds_dwordx4 v132, s[86:87]
	s_mov_b32 m0, s7
	s_nop 0
	s_mov_b32 s7, m0
	s_mov_b32 m0, s55
	s_nop 2
	global_load_lds_dwordx4 v133, s[86:87]
	s_mov_b32 m0, s7
	s_waitcnt vmcnt(8)
	s_waitcnt lgkmcnt(0)
	s_barrier
	s_setprio 1
	v_mfma_f32_16x16x32_bf16 v[64:67], v[0:3], v[32:35], 0
	v_mfma_f32_16x16x32_bf16 v[68:71], v[8:11], v[32:35], 0
	v_mfma_f32_16x16x32_bf16 v[72:75], v[0:3], v[40:43], 0
	v_mfma_f32_16x16x32_bf16 v[76:79], v[8:11], v[40:43], 0
	v_mfma_f32_16x16x32_bf16 v[80:83], v[0:3], v[48:51], 0
	v_mfma_f32_16x16x32_bf16 v[84:87], v[8:11], v[48:51], 0
	v_mfma_f32_16x16x32_bf16 v[88:91], v[0:3], v[56:59], 0
	v_mfma_f32_16x16x32_bf16 v[92:95], v[8:11], v[56:59], 0
	v_mfma_f32_16x16x32_bf16 v[64:67], v[4:7], v[36:39], v[64:67]
	v_mfma_f32_16x16x32_bf16 v[68:71], v[12:15], v[36:39], v[68:71]
	v_mfma_f32_16x16x32_bf16 v[72:75], v[4:7], v[44:47], v[72:75]
	v_mfma_f32_16x16x32_bf16 v[76:79], v[12:15], v[44:47], v[76:79]
	v_mfma_f32_16x16x32_bf16 v[80:83], v[4:7], v[52:55], v[80:83]
	v_mfma_f32_16x16x32_bf16 v[84:87], v[12:15], v[52:55], v[84:87]
	v_mfma_f32_16x16x32_bf16 v[88:91], v[4:7], v[60:63], v[88:91]
	v_mfma_f32_16x16x32_bf16 v[92:95], v[12:15], v[60:63], v[92:95]
	s_setprio 0
	s_setprio 1
	v_mfma_f32_16x16x32_bf16 v[96:99], v[16:19], v[32:35], 0
	v_mfma_f32_16x16x32_bf16 v[32:35], v[24:27], v[32:35], 0
	v_mfma_f32_16x16x32_bf16 v[96:99], v[20:23], v[36:39], v[96:99]
	v_mfma_f32_16x16x32_bf16 v[32:35], v[28:31], v[36:39], v[32:35]
	v_mfma_f32_16x16x32_bf16 v[36:39], v[16:19], v[40:43], 0
	v_mfma_f32_16x16x32_bf16 v[40:43], v[24:27], v[40:43], 0
	v_mfma_f32_16x16x32_bf16 v[36:39], v[20:23], v[44:47], v[36:39]
	v_mfma_f32_16x16x32_bf16 v[40:43], v[28:31], v[44:47], v[40:43]
	v_mfma_f32_16x16x32_bf16 v[44:47], v[16:19], v[48:51], 0
	v_mfma_f32_16x16x32_bf16 v[48:51], v[24:27], v[48:51], 0
	v_mfma_f32_16x16x32_bf16 v[44:47], v[20:23], v[52:55], v[44:47]
	v_mfma_f32_16x16x32_bf16 v[48:51], v[28:31], v[52:55], v[48:51]
	v_mfma_f32_16x16x32_bf16 v[52:55], v[16:19], v[56:59], 0
	v_mfma_f32_16x16x32_bf16 v[56:59], v[24:27], v[56:59], 0
	v_mfma_f32_16x16x32_bf16 v[52:55], v[20:23], v[60:63], v[52:55]
	v_mfma_f32_16x16x32_bf16 v[56:59], v[28:31], v[60:63], v[56:59]
	s_setprio 0
	s_barrier
	ds_read_b128 v[60:63], v136 offset:16384
	ds_read_b128 v[100:103], v136 offset:17408
	ds_read_b128 v[104:107], v136 offset:18432
	ds_read_b128 v[108:111], v136 offset:19456
	ds_read_b128 v[112:115], v136 offset:20480
	ds_read_b128 v[116:119], v136 offset:21504
	ds_read_b128 v[120:123], v136 offset:22528
	ds_read_b128 v[124:127], v136 offset:23552
	s_mov_b32 s7, m0
	s_mov_b32 m0, s40
	s_nop 2
	global_load_lds_dwordx4 v130, s[84:85]
	s_mov_b32 m0, s7
	s_nop 0
	s_mov_b32 s7, m0
	s_mov_b32 m0, s41
	s_nop 2
	global_load_lds_dwordx4 v131, s[84:85]
	s_mov_b32 m0, s7
	s_nop 0
	s_mov_b32 s7, m0
	s_mov_b32 m0, s42
	s_nop 2
	global_load_lds_dwordx4 v130, s[80:81]
	s_mov_b32 m0, s7
	s_nop 0
	s_mov_b32 s7, m0
	s_mov_b32 m0, s43
	s_nop 2
	global_load_lds_dwordx4 v131, s[80:81]
	s_mov_b32 m0, s7
	s_nop 0
	s_mov_b32 s7, m0
	s_mov_b32 m0, s97
	s_nop 2
	global_load_lds_dwordx4 v132, s[78:79]
	s_mov_b32 m0, s7
	s_nop 0
	s_mov_b32 s7, m0
	s_mov_b32 m0, s44
	s_nop 2
	global_load_lds_dwordx4 v133, s[78:79]
	s_mov_b32 m0, s7
	s_waitcnt vmcnt(8)
	s_waitcnt lgkmcnt(0)
	s_barrier
	s_setprio 1
	v_mfma_f32_16x16x32_bf16 v[140:143], v[0:3], v[60:63], 0
	v_mfma_f32_16x16x32_bf16 v[148:151], v[0:3], v[104:107], 0
	v_mfma_f32_16x16x32_bf16 v[156:159], v[0:3], v[112:115], 0
	v_mfma_f32_16x16x32_bf16 v[0:3], v[0:3], v[120:123], 0
	v_mfma_f32_16x16x32_bf16 v[140:143], v[4:7], v[100:103], v[140:143]
	v_mfma_f32_16x16x32_bf16 v[148:151], v[4:7], v[108:111], v[148:151]
	v_mfma_f32_16x16x32_bf16 v[156:159], v[4:7], v[116:119], v[156:159]
	v_mfma_f32_16x16x32_bf16 v[0:3], v[4:7], v[124:127], v[0:3]
	v_mfma_f32_16x16x32_bf16 v[4:7], v[8:11], v[120:123], 0
	v_mfma_f32_16x16x32_bf16 v[144:147], v[8:11], v[60:63], 0
	v_mfma_f32_16x16x32_bf16 v[152:155], v[8:11], v[104:107], 0
	v_mfma_f32_16x16x32_bf16 v[160:163], v[8:11], v[112:115], 0
	v_mfma_f32_16x16x32_bf16 v[4:7], v[12:15], v[124:127], v[4:7]
	v_mfma_f32_16x16x32_bf16 v[144:147], v[12:15], v[100:103], v[144:147]
	v_mfma_f32_16x16x32_bf16 v[152:155], v[12:15], v[108:111], v[152:155]
	v_mfma_f32_16x16x32_bf16 v[160:163], v[12:15], v[116:119], v[160:163]
	s_setprio 0
	s_setprio 1
	v_mfma_f32_16x16x32_bf16 v[8:11], v[16:19], v[60:63], 0
	v_mfma_f32_16x16x32_bf16 v[12:15], v[24:27], v[60:63], 0
	v_mfma_f32_16x16x32_bf16 v[8:11], v[20:23], v[100:103], v[8:11]
	v_mfma_f32_16x16x32_bf16 v[12:15], v[28:31], v[100:103], v[12:15]
	v_mfma_f32_16x16x32_bf16 v[60:63], v[16:19], v[104:107], 0
	v_mfma_f32_16x16x32_bf16 v[100:103], v[24:27], v[104:107], 0
	v_mfma_f32_16x16x32_bf16 v[104:107], v[16:19], v[112:115], 0
	v_mfma_f32_16x16x32_bf16 v[16:19], v[16:19], v[120:123], 0
	v_mfma_f32_16x16x32_bf16 v[60:63], v[20:23], v[108:111], v[60:63]
	v_mfma_f32_16x16x32_bf16 v[100:103], v[28:31], v[108:111], v[100:103]
	v_mfma_f32_16x16x32_bf16 v[104:107], v[20:23], v[116:119], v[104:107]
	v_mfma_f32_16x16x32_bf16 v[108:111], v[24:27], v[112:115], 0
	v_mfma_f32_16x16x32_bf16 v[16:19], v[20:23], v[124:127], v[16:19]
	v_mfma_f32_16x16x32_bf16 v[20:23], v[24:27], v[120:123], 0
	v_mfma_f32_16x16x32_bf16 v[108:111], v[28:31], v[116:119], v[108:111]
	v_mfma_f32_16x16x32_bf16 v[20:23], v[28:31], v[124:127], v[20:23]
	s_setprio 0
	s_barrier
	ds_read_b128 v[24:27], v137
	ds_read_b128 v[28:31], v137 offset:1024
	ds_read_b128 v[112:115], v137 offset:2048
	ds_read_b128 v[116:119], v137 offset:3072
	ds_read_b128 v[120:123], v138
	ds_read_b128 v[124:127], v138 offset:1024
	ds_read_b128 v[164:167], v138 offset:2048
	ds_read_b128 v[168:171], v138 offset:3072
	ds_read_b128 v[172:175], v136 offset:32768
	ds_read_b128 v[176:179], v136 offset:33792
	ds_read_b128 v[180:183], v136 offset:34816
	ds_read_b128 v[184:187], v136 offset:35840
	ds_read_b128 v[188:191], v136 offset:36864
	ds_read_b128 v[192:195], v136 offset:37888
	ds_read_b128 v[196:199], v136 offset:38912
	ds_read_b128 v[200:203], v136 offset:39936
	s_add_u32 s78, s28, 0x40100
	s_addc_u32 s79, s29, 0
	s_mov_b32 s7, m0
	s_mov_b32 m0, s45
	s_nop 2
	global_load_lds_dwordx4 v132, s[78:79]
	s_mov_b32 m0, s7
	s_nop 0
	s_mov_b32 s7, m0
	s_mov_b32 m0, s46
	s_nop 2
	global_load_lds_dwordx4 v133, s[78:79]
	s_mov_b32 m0, s7
	s_waitcnt vmcnt(8)
	s_waitcnt lgkmcnt(0)
	s_barrier
	s_setprio 1
	v_mfma_f32_16x16x32_bf16 v[64:67], v[24:27], v[172:175], v[64:67]
	v_mfma_f32_16x16x32_bf16 v[68:71], v[112:115], v[172:175], v[68:71]
	v_mfma_f32_16x16x32_bf16 v[72:75], v[24:27], v[180:183], v[72:75]
	v_mfma_f32_16x16x32_bf16 v[76:79], v[112:115], v[180:183], v[76:79]
	v_mfma_f32_16x16x32_bf16 v[80:83], v[24:27], v[188:191], v[80:83]
	v_mfma_f32_16x16x32_bf16 v[84:87], v[112:115], v[188:191], v[84:87]
	v_mfma_f32_16x16x32_bf16 v[88:91], v[24:27], v[196:199], v[88:91]
	v_mfma_f32_16x16x32_bf16 v[92:95], v[112:115], v[196:199], v[92:95]
	v_mfma_f32_16x16x32_bf16 v[64:67], v[28:31], v[176:179], v[64:67]
	v_mfma_f32_16x16x32_bf16 v[68:71], v[116:119], v[176:179], v[68:71]
	v_mfma_f32_16x16x32_bf16 v[72:75], v[28:31], v[184:187], v[72:75]
	v_mfma_f32_16x16x32_bf16 v[76:79], v[116:119], v[184:187], v[76:79]
	v_mfma_f32_16x16x32_bf16 v[80:83], v[28:31], v[192:195], v[80:83]
	v_mfma_f32_16x16x32_bf16 v[84:87], v[116:119], v[192:195], v[84:87]
	v_mfma_f32_16x16x32_bf16 v[88:91], v[28:31], v[200:203], v[88:91]
	v_mfma_f32_16x16x32_bf16 v[92:95], v[116:119], v[200:203], v[92:95]
	s_setprio 0
	s_setprio 1
	v_mfma_f32_16x16x32_bf16 v[96:99], v[120:123], v[172:175], v[96:99]
	v_mfma_f32_16x16x32_bf16 v[32:35], v[164:167], v[172:175], v[32:35]
	v_mfma_f32_16x16x32_bf16 v[36:39], v[120:123], v[180:183], v[36:39]
	v_mfma_f32_16x16x32_bf16 v[40:43], v[164:167], v[180:183], v[40:43]
	v_mfma_f32_16x16x32_bf16 v[44:47], v[120:123], v[188:191], v[44:47]
	v_mfma_f32_16x16x32_bf16 v[48:51], v[164:167], v[188:191], v[48:51]
	v_mfma_f32_16x16x32_bf16 v[52:55], v[120:123], v[196:199], v[52:55]
	v_mfma_f32_16x16x32_bf16 v[56:59], v[164:167], v[196:199], v[56:59]
	v_mfma_f32_16x16x32_bf16 v[96:99], v[124:127], v[176:179], v[96:99]
	v_mfma_f32_16x16x32_bf16 v[32:35], v[168:171], v[176:179], v[32:35]
	v_mfma_f32_16x16x32_bf16 v[36:39], v[124:127], v[184:187], v[36:39]
	v_mfma_f32_16x16x32_bf16 v[40:43], v[168:171], v[184:187], v[40:43]
	v_mfma_f32_16x16x32_bf16 v[44:47], v[124:127], v[192:195], v[44:47]
	v_mfma_f32_16x16x32_bf16 v[48:51], v[168:171], v[192:195], v[48:51]
	v_mfma_f32_16x16x32_bf16 v[52:55], v[124:127], v[200:203], v[52:55]
	v_mfma_f32_16x16x32_bf16 v[56:59], v[168:171], v[200:203], v[56:59]
	s_setprio 0
	s_barrier
	ds_read_b128 v[172:175], v136 offset:49152
	ds_read_b128 v[176:179], v136 offset:50176
	ds_read_b128 v[180:183], v136 offset:51200
	ds_read_b128 v[184:187], v136 offset:52224
	ds_read_b128 v[188:191], v136 offset:53248
	ds_read_b128 v[192:195], v136 offset:54272
	ds_read_b128 v[196:199], v136 offset:55296
	ds_read_b128 v[200:203], v136 offset:56320
	s_mov_b32 s7, m0
	s_mov_b32 m0, s48
	s_nop 2
	global_load_lds_dwordx4 v130, s[76:77]
	s_mov_b32 m0, s7
	s_add_u32 s30, s30, 0x180
	s_mov_b32 s7, m0
	s_mov_b32 m0, s49
	s_nop 2
	global_load_lds_dwordx4 v131, s[76:77]
	s_mov_b32 m0, s7
	s_addc_u32 s31, s31, 0
	s_mov_b32 s7, m0
	s_mov_b32 m0, s52
	s_nop 2
	global_load_lds_dwordx4 v130, s[30:31]
	s_mov_b32 m0, s7
	s_nop 0
	s_mov_b32 s7, m0
	s_mov_b32 m0, s53
	s_nop 2
	global_load_lds_dwordx4 v131, s[30:31]
	s_mov_b32 m0, s7
	s_nop 0
	s_mov_b32 s7, m0
	s_mov_b32 m0, s50
	s_nop 2
	global_load_lds_dwordx4 v132, s[56:57]
	s_mov_b32 m0, s7
	s_nop 0
	s_mov_b32 s7, m0
	s_mov_b32 m0, s51
	s_nop 2
	global_load_lds_dwordx4 v133, s[56:57]
	s_mov_b32 m0, s7
	s_waitcnt vmcnt(8)
	s_waitcnt lgkmcnt(0)
	s_barrier
	s_setprio 1
	v_mfma_f32_16x16x32_bf16 v[0:3], v[24:27], v[196:199], v[0:3]
	v_mfma_f32_16x16x32_bf16 v[4:7], v[112:115], v[196:199], v[4:7]
	v_mfma_f32_16x16x32_bf16 v[140:143], v[24:27], v[172:175], v[140:143]
	v_mfma_f32_16x16x32_bf16 v[144:147], v[112:115], v[172:175], v[144:147]
	v_mfma_f32_16x16x32_bf16 v[148:151], v[24:27], v[180:183], v[148:151]
	v_mfma_f32_16x16x32_bf16 v[152:155], v[112:115], v[180:183], v[152:155]
	v_mfma_f32_16x16x32_bf16 v[156:159], v[24:27], v[188:191], v[156:159]
	v_mfma_f32_16x16x32_bf16 v[160:163], v[112:115], v[188:191], v[160:163]
	v_mfma_f32_16x16x32_bf16 v[0:3], v[28:31], v[200:203], v[0:3]
	v_mfma_f32_16x16x32_bf16 v[4:7], v[116:119], v[200:203], v[4:7]
	v_mfma_f32_16x16x32_bf16 v[140:143], v[28:31], v[176:179], v[140:143]
	v_mfma_f32_16x16x32_bf16 v[144:147], v[116:119], v[176:179], v[144:147]
	v_mfma_f32_16x16x32_bf16 v[148:151], v[28:31], v[184:187], v[148:151]
	v_mfma_f32_16x16x32_bf16 v[152:155], v[116:119], v[184:187], v[152:155]
	v_mfma_f32_16x16x32_bf16 v[156:159], v[28:31], v[192:195], v[156:159]
	v_mfma_f32_16x16x32_bf16 v[160:163], v[116:119], v[192:195], v[160:163]
	s_setprio 0
	s_setprio 1
	v_mfma_f32_16x16x32_bf16 v[8:11], v[120:123], v[172:175], v[8:11]
	v_mfma_f32_16x16x32_bf16 v[12:15], v[164:167], v[172:175], v[12:15]
	v_mfma_f32_16x16x32_bf16 v[24:27], v[120:123], v[180:183], v[60:63]
	v_mfma_f32_16x16x32_bf16 v[28:31], v[164:167], v[180:183], v[100:103]
	v_mfma_f32_16x16x32_bf16 v[60:63], v[120:123], v[188:191], v[104:107]
	v_mfma_f32_16x16x32_bf16 v[100:103], v[164:167], v[188:191], v[108:111]
	v_mfma_f32_16x16x32_bf16 v[16:19], v[120:123], v[196:199], v[16:19]
	v_mfma_f32_16x16x32_bf16 v[20:23], v[164:167], v[196:199], v[20:23]
	v_mfma_f32_16x16x32_bf16 v[8:11], v[124:127], v[176:179], v[8:11]
	v_mfma_f32_16x16x32_bf16 v[12:15], v[168:171], v[176:179], v[12:15]
	v_mfma_f32_16x16x32_bf16 v[24:27], v[124:127], v[184:187], v[24:27]
	v_mfma_f32_16x16x32_bf16 v[28:31], v[168:171], v[184:187], v[28:31]
	v_mfma_f32_16x16x32_bf16 v[60:63], v[124:127], v[192:195], v[60:63]
	v_mfma_f32_16x16x32_bf16 v[100:103], v[168:171], v[192:195], v[100:103]
	v_mfma_f32_16x16x32_bf16 v[16:19], v[124:127], v[200:203], v[16:19]
	v_mfma_f32_16x16x32_bf16 v[20:23], v[168:171], v[200:203], v[20:23]
	s_setprio 0
	s_barrier
	ds_read_b128 v[104:107], v134
	ds_read_b128 v[108:111], v134 offset:1024
	ds_read_b128 v[112:115], v134 offset:2048
	ds_read_b128 v[116:119], v134 offset:3072
	ds_read_b128 v[120:123], v135
	ds_read_b128 v[124:127], v135 offset:1024
	ds_read_b128 v[164:167], v135 offset:2048
	ds_read_b128 v[168:171], v135 offset:3072
	s_add_u32 s56, s62, 0x80
	s_addc_u32 s57, s63, 0
	s_add_u32 s30, s36, 0x80
	s_addc_u32 s31, s37, 0
	ds_read_b128 v[172:175], v136
	ds_read_b128 v[176:179], v136 offset:1024
	ds_read_b128 v[180:183], v136 offset:2048
	ds_read_b128 v[184:187], v136 offset:3072
	ds_read_b128 v[188:191], v136 offset:4096
	ds_read_b128 v[192:195], v136 offset:5120
	ds_read_b128 v[196:199], v136 offset:6144
	ds_read_b128 v[200:203], v136 offset:7168
	s_add_u32 s28, s28, 0x40180
	s_addc_u32 s29, s29, 0
	s_mov_b32 s7, m0
	s_mov_b32 m0, s54
	s_nop 2
	global_load_lds_dwordx4 v132, s[28:29]
	s_mov_b32 m0, s7
	s_nop 0
	s_mov_b32 s7, m0
	s_mov_b32 m0, s55
	s_nop 2
	global_load_lds_dwordx4 v133, s[28:29]
	s_mov_b32 m0, s7
	s_waitcnt vmcnt(8)
	s_waitcnt lgkmcnt(0)
	s_barrier
	s_setprio 1
	v_mfma_f32_16x16x32_bf16 v[88:91], v[104:107], v[196:199], v[88:91]
	v_mfma_f32_16x16x32_bf16 v[64:67], v[104:107], v[172:175], v[64:67]
	v_mfma_f32_16x16x32_bf16 v[68:71], v[112:115], v[172:175], v[68:71]
	v_mfma_f32_16x16x32_bf16 v[72:75], v[104:107], v[180:183], v[72:75]
	v_mfma_f32_16x16x32_bf16 v[76:79], v[112:115], v[180:183], v[76:79]
	v_mfma_f32_16x16x32_bf16 v[80:83], v[104:107], v[188:191], v[80:83]
	v_mfma_f32_16x16x32_bf16 v[84:87], v[112:115], v[188:191], v[84:87]
	v_mfma_f32_16x16x32_bf16 v[204:207], v[108:111], v[200:203], v[88:91]
	v_mfma_f32_16x16x32_bf16 v[88:91], v[112:115], v[196:199], v[92:95]
	v_mfma_f32_16x16x32_bf16 v[64:67], v[108:111], v[176:179], v[64:67]
	v_mfma_f32_16x16x32_bf16 v[68:71], v[116:119], v[176:179], v[68:71]
	v_mfma_f32_16x16x32_bf16 v[72:75], v[108:111], v[184:187], v[72:75]
	v_mfma_f32_16x16x32_bf16 v[76:79], v[116:119], v[184:187], v[76:79]
	v_mfma_f32_16x16x32_bf16 v[80:83], v[108:111], v[192:195], v[80:83]
	v_mfma_f32_16x16x32_bf16 v[84:87], v[116:119], v[192:195], v[84:87]
	v_mfma_f32_16x16x32_bf16 v[92:95], v[116:119], v[200:203], v[88:91]
	s_setprio 0
	s_setprio 1
	v_mfma_f32_16x16x32_bf16 v[48:51], v[164:167], v[188:191], v[48:51]
	v_mfma_f32_16x16x32_bf16 v[88:91], v[120:123], v[172:175], v[96:99]
	v_mfma_f32_16x16x32_bf16 v[32:35], v[164:167], v[172:175], v[32:35]
	v_mfma_f32_16x16x32_bf16 v[36:39], v[120:123], v[180:183], v[36:39]
	v_mfma_f32_16x16x32_bf16 v[40:43], v[164:167], v[180:183], v[40:43]
	v_mfma_f32_16x16x32_bf16 v[44:47], v[120:123], v[188:191], v[44:47]
	v_mfma_f32_16x16x32_bf16 v[172:175], v[168:171], v[192:195], v[48:51]
	v_mfma_f32_16x16x32_bf16 v[48:51], v[120:123], v[196:199], v[52:55]
	v_mfma_f32_16x16x32_bf16 v[32:35], v[168:171], v[176:179], v[32:35]
	v_mfma_f32_16x16x32_bf16 v[36:39], v[124:127], v[184:187], v[36:39]
	v_mfma_f32_16x16x32_bf16 v[40:43], v[168:171], v[184:187], v[40:43]
	v_mfma_f32_16x16x32_bf16 v[44:47], v[124:127], v[192:195], v[44:47]
	v_mfma_f32_16x16x32_bf16 v[52:55], v[124:127], v[200:203], v[48:51]
	v_mfma_f32_16x16x32_bf16 v[48:51], v[164:167], v[196:199], v[56:59]
	v_mfma_f32_16x16x32_bf16 v[208:211], v[124:127], v[176:179], v[88:91]
	v_mfma_f32_16x16x32_bf16 v[176:179], v[168:171], v[200:203], v[48:51]
	s_setprio 0
	s_barrier
	s_nop 3
	ds_read_b128 v[48:51], v136 offset:16384
	ds_read_b128 v[56:59], v136 offset:17408
	ds_read_b128 v[88:91], v136 offset:18432
	ds_read_b128 v[96:99], v136 offset:19456
	ds_read_b128 v[180:183], v136 offset:20480
	ds_read_b128 v[184:187], v136 offset:21504
	ds_read_b128 v[188:191], v136 offset:22528
	ds_read_b128 v[192:195], v136 offset:23552
	s_mov_b32 s7, m0
	s_mov_b32 m0, s40
	s_nop 2
	global_load_lds_dwordx4 v130, s[62:63]
	s_mov_b32 m0, s7
	s_nop 0
	s_mov_b32 s7, m0
	s_mov_b32 m0, s41
	s_nop 2
	global_load_lds_dwordx4 v131, s[62:63]
	s_mov_b32 m0, s7
	s_nop 0
	s_mov_b32 s7, m0
	s_mov_b32 m0, s42
	s_nop 2
	global_load_lds_dwordx4 v130, s[34:35]
	s_mov_b32 m0, s7
	s_nop 0
	s_mov_b32 s7, m0
	s_mov_b32 m0, s43
	s_nop 2
	global_load_lds_dwordx4 v131, s[34:35]
	s_mov_b32 m0, s7
	s_nop 0
	s_mov_b32 s7, m0
	s_mov_b32 m0, s97
	s_nop 2
	global_load_lds_dwordx4 v132, s[36:37]
	s_mov_b32 m0, s7
	s_nop 0
	s_mov_b32 s7, m0
	s_mov_b32 m0, s44
	s_nop 2
	global_load_lds_dwordx4 v133, s[36:37]
	s_mov_b32 m0, s7
	s_waitcnt vmcnt(8)
	s_waitcnt lgkmcnt(0)
	s_barrier
	s_setprio 1
	v_mfma_f32_16x16x32_bf16 v[0:3], v[104:107], v[188:191], v[0:3]
	v_mfma_f32_16x16x32_bf16 v[4:7], v[112:115], v[188:191], v[4:7]
	v_mfma_f32_16x16x32_bf16 v[140:143], v[104:107], v[48:51], v[140:143]
	v_mfma_f32_16x16x32_bf16 v[144:147], v[112:115], v[48:51], v[144:147]
	v_mfma_f32_16x16x32_bf16 v[148:151], v[104:107], v[88:91], v[148:151]
	v_mfma_f32_16x16x32_bf16 v[152:155], v[112:115], v[88:91], v[152:155]
	v_mfma_f32_16x16x32_bf16 v[156:159], v[104:107], v[180:183], v[156:159]
	v_mfma_f32_16x16x32_bf16 v[160:163], v[112:115], v[180:183], v[160:163]
	v_mfma_f32_16x16x32_bf16 v[0:3], v[108:111], v[192:195], v[0:3]
	v_mfma_f32_16x16x32_bf16 v[4:7], v[116:119], v[192:195], v[4:7]
	v_mfma_f32_16x16x32_bf16 v[140:143], v[108:111], v[56:59], v[140:143]
	v_mfma_f32_16x16x32_bf16 v[144:147], v[116:119], v[56:59], v[144:147]
	v_mfma_f32_16x16x32_bf16 v[148:151], v[108:111], v[96:99], v[148:151]
	v_mfma_f32_16x16x32_bf16 v[152:155], v[116:119], v[96:99], v[152:155]
	v_mfma_f32_16x16x32_bf16 v[156:159], v[108:111], v[184:187], v[156:159]
	v_mfma_f32_16x16x32_bf16 v[160:163], v[116:119], v[184:187], v[160:163]
	s_setprio 0
	s_setprio 1
	v_mfma_f32_16x16x32_bf16 v[12:15], v[164:167], v[48:51], v[12:15]
	v_mfma_f32_16x16x32_bf16 v[196:199], v[168:171], v[56:59], v[12:15]
	v_mfma_f32_16x16x32_bf16 v[12:15], v[120:123], v[88:91], v[24:27]
	v_mfma_f32_16x16x32_bf16 v[24:27], v[124:127], v[96:99], v[12:15]
	v_mfma_f32_16x16x32_bf16 v[12:15], v[164:167], v[88:91], v[28:31]
	v_mfma_f32_16x16x32_bf16 v[200:203], v[168:171], v[96:99], v[12:15]
	v_mfma_f32_16x16x32_bf16 v[12:15], v[120:123], v[180:183], v[60:63]
	v_mfma_f32_16x16x32_bf16 v[212:215], v[124:127], v[184:187], v[12:15]
	v_mfma_f32_16x16x32_bf16 v[12:15], v[164:167], v[180:183], v[100:103]
	v_mfma_f32_16x16x32_bf16 v[8:11], v[120:123], v[48:51], v[8:11]
	v_mfma_f32_16x16x32_bf16 v[180:183], v[168:171], v[184:187], v[12:15]
	v_mfma_f32_16x16x32_bf16 v[12:15], v[120:123], v[188:191], v[16:19]
	v_mfma_f32_16x16x32_bf16 v[8:11], v[124:127], v[56:59], v[8:11]
	v_mfma_f32_16x16x32_bf16 v[184:187], v[124:127], v[192:195], v[12:15]
	v_mfma_f32_16x16x32_bf16 v[12:15], v[164:167], v[188:191], v[20:23]
	v_mfma_f32_16x16x32_bf16 v[164:167], v[168:171], v[192:195], v[12:15]
	s_setprio 0
	s_barrier
	s_nop 4
	ds_read_b128 v[12:15], v137
	ds_read_b128 v[16:19], v137 offset:1024
	ds_read_b128 v[168:171], v137 offset:2048
	ds_read_b128 v[188:191], v137 offset:3072
	ds_read_b128 v[192:195], v138
	ds_read_b128 v[216:219], v138 offset:1024
	ds_read_b128 v[220:223], v138 offset:2048
	ds_read_b128 v[224:227], v138 offset:3072
	ds_read_b128 v[20:23], v136 offset:32768
	ds_read_b128 v[28:31], v136 offset:33792
	ds_read_b128 v[60:63], v136 offset:34816
	ds_read_b128 v[100:103], v136 offset:35840
	ds_read_b128 v[228:231], v136 offset:36864
	ds_read_b128 v[232:235], v136 offset:37888
	ds_read_b128 v[236:239], v136 offset:38912
	ds_read_b128 v[240:243], v136 offset:39936
	s_add_u32 s28, s36, 0x40000
	s_addc_u32 s29, s37, 0
	s_mov_b32 s7, m0
	s_mov_b32 m0, s45
	s_nop 2
	global_load_lds_dwordx4 v132, s[28:29]
	s_mov_b32 m0, s7
	s_nop 0
	s_mov_b32 s7, m0
	s_mov_b32 m0, s46
	s_nop 2
	global_load_lds_dwordx4 v133, s[28:29]
	s_mov_b32 m0, s7
	s_waitcnt vmcnt(8)
	s_waitcnt lgkmcnt(0)
	s_barrier
	s_setprio 1
	v_mfma_f32_16x16x32_bf16 v[48:51], v[12:15], v[20:23], v[64:67]
	v_mfma_f32_16x16x32_bf16 v[120:123], v[16:19], v[28:31], v[48:51]
	v_mfma_f32_16x16x32_bf16 v[48:51], v[168:171], v[20:23], v[68:71]
	v_mfma_f32_16x16x32_bf16 v[112:115], v[188:191], v[28:31], v[48:51]
	v_mfma_f32_16x16x32_bf16 v[48:51], v[12:15], v[60:63], v[72:75]
	v_mfma_f32_16x16x32_bf16 v[104:107], v[16:19], v[100:103], v[48:51]
	v_mfma_f32_16x16x32_bf16 v[48:51], v[168:171], v[60:63], v[76:79]
	v_mfma_f32_16x16x32_bf16 v[96:99], v[188:191], v[100:103], v[48:51]
	v_mfma_f32_16x16x32_bf16 v[48:51], v[12:15], v[228:231], v[80:83]
	v_mfma_f32_16x16x32_bf16 v[88:91], v[16:19], v[232:235], v[48:51]
	v_mfma_f32_16x16x32_bf16 v[48:51], v[168:171], v[228:231], v[84:87]
	v_mfma_f32_16x16x32_bf16 v[80:83], v[188:191], v[232:235], v[48:51]
	v_mfma_f32_16x16x32_bf16 v[48:51], v[12:15], v[236:239], v[204:207]
	v_mfma_f32_16x16x32_bf16 v[56:59], v[16:19], v[240:243], v[48:51]
	v_mfma_f32_16x16x32_bf16 v[48:51], v[168:171], v[236:239], v[92:95]
	v_mfma_f32_16x16x32_bf16 v[48:51], v[188:191], v[240:243], v[48:51]
	s_setprio 0
	s_setprio 1
	v_mfma_f32_16x16x32_bf16 v[64:67], v[192:195], v[20:23], v[208:211]
	v_mfma_f32_16x16x32_bf16 v[20:23], v[220:223], v[20:23], v[32:35]
	v_mfma_f32_16x16x32_bf16 v[116:119], v[224:227], v[28:31], v[20:23]
	v_mfma_f32_16x16x32_bf16 v[20:23], v[192:195], v[60:63], v[36:39]
	v_mfma_f32_16x16x32_bf16 v[108:111], v[216:219], v[100:103], v[20:23]
	v_mfma_f32_16x16x32_bf16 v[20:23], v[220:223], v[60:63], v[40:43]
	v_mfma_f32_16x16x32_bf16 v[100:103], v[224:227], v[100:103], v[20:23]
	v_mfma_f32_16x16x32_bf16 v[20:23], v[192:195], v[228:231], v[44:47]
	v_mfma_f32_16x16x32_bf16 v[92:95], v[216:219], v[232:235], v[20:23]
	v_mfma_f32_16x16x32_bf16 v[20:23], v[220:223], v[228:231], v[172:175]
	v_mfma_f32_16x16x32_bf16 v[84:87], v[224:227], v[232:235], v[20:23]
	v_mfma_f32_16x16x32_bf16 v[20:23], v[192:195], v[236:239], v[52:55]
	v_mfma_f32_16x16x32_bf16 v[60:63], v[216:219], v[240:243], v[20:23]
	v_mfma_f32_16x16x32_bf16 v[20:23], v[220:223], v[236:239], v[176:179]
	v_mfma_f32_16x16x32_bf16 v[124:127], v[216:219], v[28:31], v[64:67]
	v_mfma_f32_16x16x32_bf16 v[52:55], v[224:227], v[240:243], v[20:23]
	s_setprio 0
	s_barrier
	ds_read_b128 v[32:35], v136 offset:49152
	ds_read_b128 v[40:43], v136 offset:50176
	ds_read_b128 v[172:175], v136 offset:51200
	ds_read_b128 v[176:179], v136 offset:52224
	ds_read_b128 v[204:207], v136 offset:53248
	ds_read_b128 v[208:211], v136 offset:54272
	ds_read_b128 v[228:231], v136 offset:55296
	ds_read_b128 v[232:235], v136 offset:56320
	s_mov_b32 s7, m0
	s_mov_b32 m0, s48
	s_nop 2
	global_load_lds_dwordx4 v130, s[56:57]
	s_mov_b32 m0, s7
	s_add_u32 s28, s34, 0x80
	s_mov_b32 s7, m0
	s_mov_b32 m0, s49
	s_nop 2
	global_load_lds_dwordx4 v131, s[56:57]
	s_mov_b32 m0, s7
	s_addc_u32 s29, s35, 0
	s_mov_b32 s7, m0
	s_mov_b32 m0, s52
	s_nop 2
	global_load_lds_dwordx4 v130, s[28:29]
	s_mov_b32 m0, s7
	s_nop 0
	s_mov_b32 s7, m0
	s_mov_b32 m0, s53
	s_nop 2
	global_load_lds_dwordx4 v131, s[28:29]
	s_mov_b32 m0, s7
	s_nop 0
	s_mov_b32 s7, m0
	s_mov_b32 m0, s50
	s_nop 2
	global_load_lds_dwordx4 v132, s[30:31]
	s_mov_b32 m0, s7
	s_nop 0
	s_mov_b32 s7, m0
	s_mov_b32 m0, s51
	s_nop 2
	global_load_lds_dwordx4 v133, s[30:31]
	s_mov_b32 m0, s7
	s_waitcnt vmcnt(8)
	s_waitcnt lgkmcnt(0)
	s_barrier
	s_setprio 1
	v_mfma_f32_16x16x32_bf16 v[20:23], v[12:15], v[32:35], v[140:143]
	v_mfma_f32_16x16x32_bf16 v[76:79], v[16:19], v[40:43], v[20:23]
	v_mfma_f32_16x16x32_bf16 v[20:23], v[168:171], v[32:35], v[144:147]
	v_mfma_f32_16x16x32_bf16 v[68:71], v[188:191], v[40:43], v[20:23]
	v_mfma_f32_16x16x32_bf16 v[20:23], v[12:15], v[172:175], v[148:151]
	v_mfma_f32_16x16x32_bf16 v[44:47], v[16:19], v[176:179], v[20:23]
	v_mfma_f32_16x16x32_bf16 v[20:23], v[168:171], v[172:175], v[152:155]
	v_mfma_f32_16x16x32_bf16 v[36:39], v[188:191], v[176:179], v[20:23]
	v_mfma_f32_16x16x32_bf16 v[20:23], v[12:15], v[204:207], v[156:159]
	v_mfma_f32_16x16x32_bf16 v[0:3], v[12:15], v[228:231], v[0:3]
	v_mfma_f32_16x16x32_bf16 v[28:31], v[16:19], v[208:211], v[20:23]
	v_mfma_f32_16x16x32_bf16 v[20:23], v[168:171], v[204:207], v[160:163]
	v_mfma_f32_16x16x32_bf16 v[12:15], v[16:19], v[232:235], v[0:3]
	v_mfma_f32_16x16x32_bf16 v[0:3], v[168:171], v[228:231], v[4:7]
	v_mfma_f32_16x16x32_bf16 v[20:23], v[188:191], v[208:211], v[20:23]
	v_mfma_f32_16x16x32_bf16 v[4:7], v[188:191], v[232:235], v[0:3]
	s_setprio 0
	s_setprio 1
	v_mfma_f32_16x16x32_bf16 v[0:3], v[192:195], v[32:35], v[8:11]
	v_mfma_f32_16x16x32_bf16 v[72:75], v[216:219], v[40:43], v[0:3]
	v_mfma_f32_16x16x32_bf16 v[0:3], v[220:223], v[32:35], v[196:199]
	v_mfma_f32_16x16x32_bf16 v[64:67], v[224:227], v[40:43], v[0:3]
	v_mfma_f32_16x16x32_bf16 v[0:3], v[192:195], v[172:175], v[24:27]
	v_mfma_f32_16x16x32_bf16 v[40:43], v[216:219], v[176:179], v[0:3]
	v_mfma_f32_16x16x32_bf16 v[0:3], v[220:223], v[172:175], v[200:203]
	v_mfma_f32_16x16x32_bf16 v[32:35], v[224:227], v[176:179], v[0:3]
	v_mfma_f32_16x16x32_bf16 v[0:3], v[192:195], v[204:207], v[212:215]
	v_mfma_f32_16x16x32_bf16 v[24:27], v[216:219], v[208:211], v[0:3]
	v_mfma_f32_16x16x32_bf16 v[0:3], v[220:223], v[204:207], v[180:183]
	v_mfma_f32_16x16x32_bf16 v[16:19], v[224:227], v[208:211], v[0:3]
	v_mfma_f32_16x16x32_bf16 v[0:3], v[192:195], v[228:231], v[184:187]
	v_mfma_f32_16x16x32_bf16 v[8:11], v[216:219], v[232:235], v[0:3]
	v_mfma_f32_16x16x32_bf16 v[0:3], v[220:223], v[228:231], v[164:167]
	v_mfma_f32_16x16x32_bf16 v[0:3], v[224:227], v[232:235], v[0:3]
	s_setprio 0
	s_barrier
	s_andn2_b64 vcc, exec, s[10:11]
	s_cbranch_vccnz .LBB0_292
	s_barrier

.LBB0_518:
	v_add_u32_e32 v140, 0x10000, v200
	v_add_u32_e32 v156, 0x14000, v200
	s_add_u32 s34, s30, 0x100
	ds_read_b128 v[128:131], v140
	ds_read_b128 v[132:135], v140 offset:1024
	ds_read_b128 v[136:139], v140 offset:2048
	ds_read_b128 v[140:143], v140 offset:3072
	ds_read_b128 v[144:147], v156
	ds_read_b128 v[148:151], v156 offset:1024
	ds_read_b128 v[152:155], v156 offset:2048
	ds_read_b128 v[156:159], v156 offset:3072
	s_addc_u32 s35, s31, 0
	s_cmp_eq_u32 s48, 28
	s_cselect_b32 s78, s41, s44
	s_cselect_b32 s79, s40, s45
	s_cselect_b32 s37, s42, s47
	s_cselect_b32 s36, s43, s46
	s_cselect_b32 s76, s21, s34
	s_cselect_b32 s77, s19, s35
	s_add_u32 s62, s78, 0x80
	s_addc_u32 s63, s79, 0
	s_add_u32 s56, s76, 0x80
	s_addc_u32 s57, s77, 0
	ds_read_b128 v[160:163], v201
	ds_read_b128 v[164:167], v201 offset:1024
	ds_read_b128 v[168:171], v201 offset:2048
	ds_read_b128 v[172:175], v201 offset:3072
	ds_read_b128 v[176:179], v201 offset:4096
	ds_read_b128 v[180:183], v201 offset:5120
	ds_read_b128 v[184:187], v201 offset:6144
	ds_read_b128 v[188:191], v201 offset:7168
	s_add_u32 s30, s30, 0x80080
	s_addc_u32 s31, s31, 0
	s_mov_b32 s49, m0
	s_mov_b32 m0, s96
	s_nop 2
	global_load_lds_dwordx4 v198, s[30:31]
	s_mov_b32 m0, s49
	s_nop 0
	s_mov_b32 s49, m0
	s_mov_b32 m0, s8
	s_nop 2
	global_load_lds_dwordx4 v199, s[30:31]
	s_mov_b32 m0, s49
	s_waitcnt vmcnt(8)
	s_waitcnt lgkmcnt(0)
	s_barrier
	s_setprio 1
	v_mfma_f32_16x16x32_bf16 v[124:127], v[128:131], v[160:163], v[124:127]
	v_mfma_f32_16x16x32_bf16 v[120:123], v[136:139], v[160:163], v[120:123]
	v_mfma_f32_16x16x32_bf16 v[108:111], v[128:131], v[168:171], v[108:111]
	v_mfma_f32_16x16x32_bf16 v[104:107], v[136:139], v[168:171], v[104:107]
	v_mfma_f32_16x16x32_bf16 v[92:95], v[128:131], v[176:179], v[92:95]
	v_mfma_f32_16x16x32_bf16 v[88:91], v[136:139], v[176:179], v[88:91]
	v_mfma_f32_16x16x32_bf16 v[76:79], v[128:131], v[184:187], v[76:79]
	v_mfma_f32_16x16x32_bf16 v[72:75], v[136:139], v[184:187], v[72:75]
	v_mfma_f32_16x16x32_bf16 v[124:127], v[132:135], v[164:167], v[124:127]
	v_mfma_f32_16x16x32_bf16 v[120:123], v[140:143], v[164:167], v[120:123]
	v_mfma_f32_16x16x32_bf16 v[108:111], v[132:135], v[172:175], v[108:111]
	v_mfma_f32_16x16x32_bf16 v[104:107], v[140:143], v[172:175], v[104:107]
	v_mfma_f32_16x16x32_bf16 v[92:95], v[132:135], v[180:183], v[92:95]
	v_mfma_f32_16x16x32_bf16 v[88:91], v[140:143], v[180:183], v[88:91]
	v_mfma_f32_16x16x32_bf16 v[76:79], v[132:135], v[188:191], v[76:79]
	v_mfma_f32_16x16x32_bf16 v[72:75], v[140:143], v[188:191], v[72:75]
	s_setprio 0
	s_setprio 1
	v_mfma_f32_16x16x32_bf16 v[116:119], v[144:147], v[160:163], v[116:119]
	v_mfma_f32_16x16x32_bf16 v[112:115], v[152:155], v[160:163], v[112:115]
	v_mfma_f32_16x16x32_bf16 v[100:103], v[144:147], v[168:171], v[100:103]
	v_mfma_f32_16x16x32_bf16 v[96:99], v[152:155], v[168:171], v[96:99]
	v_mfma_f32_16x16x32_bf16 v[84:87], v[144:147], v[176:179], v[84:87]
	v_mfma_f32_16x16x32_bf16 v[80:83], v[152:155], v[176:179], v[80:83]
	v_mfma_f32_16x16x32_bf16 v[68:71], v[144:147], v[184:187], v[68:71]
	v_mfma_f32_16x16x32_bf16 v[64:67], v[152:155], v[184:187], v[64:67]
	v_mfma_f32_16x16x32_bf16 v[116:119], v[148:151], v[164:167], v[116:119]
	v_mfma_f32_16x16x32_bf16 v[112:115], v[156:159], v[164:167], v[112:115]
	v_mfma_f32_16x16x32_bf16 v[100:103], v[148:151], v[172:175], v[100:103]
	v_mfma_f32_16x16x32_bf16 v[96:99], v[156:159], v[172:175], v[96:99]
	v_mfma_f32_16x16x32_bf16 v[84:87], v[148:151], v[180:183], v[84:87]
	v_mfma_f32_16x16x32_bf16 v[80:83], v[156:159], v[180:183], v[80:83]
	v_mfma_f32_16x16x32_bf16 v[68:71], v[148:151], v[188:191], v[68:71]
	v_mfma_f32_16x16x32_bf16 v[64:67], v[156:159], v[188:191], v[64:67]
	s_setprio 0
	s_barrier
	ds_read_b128 v[160:163], v201 offset:16384
	ds_read_b128 v[164:167], v201 offset:17408
	ds_read_b128 v[168:171], v201 offset:18432
	ds_read_b128 v[172:175], v201 offset:19456
	ds_read_b128 v[176:179], v201 offset:20480
	ds_read_b128 v[180:183], v201 offset:21504
	ds_read_b128 v[184:187], v201 offset:22528
	ds_read_b128 v[188:191], v201 offset:23552
	s_mov_b32 s30, m0
	s_mov_b32 m0, s86
	s_nop 2
	global_load_lds_dwordx4 v196, s[78:79]
	s_mov_b32 m0, s30
	s_nop 0
	s_mov_b32 s30, m0
	s_mov_b32 m0, s87
	s_nop 2
	global_load_lds_dwordx4 v197, s[78:79]
	s_mov_b32 m0, s30
	s_nop 0
	s_mov_b32 s30, m0
	s_mov_b32 m0, s97
	s_nop 2
	global_load_lds_dwordx4 v196, s[36:37]
	s_mov_b32 m0, s30
	s_nop 0
	s_mov_b32 s30, m0
	s_mov_b32 m0, s38
	s_nop 2
	global_load_lds_dwordx4 v197, s[36:37]
	s_mov_b32 m0, s30
	s_nop 0
	s_mov_b32 s30, m0
	s_mov_b32 m0, s80
	s_nop 2
	global_load_lds_dwordx4 v198, s[76:77]
	s_mov_b32 m0, s30
	s_nop 0
	s_mov_b32 s30, m0
	s_mov_b32 m0, s6
	s_nop 2
	global_load_lds_dwordx4 v199, s[76:77]
	s_mov_b32 m0, s30
	s_waitcnt vmcnt(8)
	s_waitcnt lgkmcnt(0)
	s_barrier
	s_setprio 1
	v_mfma_f32_16x16x32_bf16 v[60:63], v[128:131], v[160:163], v[60:63]
	v_mfma_f32_16x16x32_bf16 v[56:59], v[136:139], v[160:163], v[56:59]
	v_mfma_f32_16x16x32_bf16 v[44:47], v[128:131], v[168:171], v[44:47]
	v_mfma_f32_16x16x32_bf16 v[40:43], v[136:139], v[168:171], v[40:43]
	v_mfma_f32_16x16x32_bf16 v[20:23], v[128:131], v[176:179], v[20:23]
	v_mfma_f32_16x16x32_bf16 v[16:19], v[136:139], v[176:179], v[16:19]
	v_mfma_f32_16x16x32_bf16 v[4:7], v[128:131], v[184:187], v[4:7]
	v_mfma_f32_16x16x32_bf16 v[0:3], v[136:139], v[184:187], v[0:3]
	v_mfma_f32_16x16x32_bf16 v[60:63], v[132:135], v[164:167], v[60:63]
	v_mfma_f32_16x16x32_bf16 v[56:59], v[140:143], v[164:167], v[56:59]
	v_mfma_f32_16x16x32_bf16 v[44:47], v[132:135], v[172:175], v[44:47]
	v_mfma_f32_16x16x32_bf16 v[40:43], v[140:143], v[172:175], v[40:43]
	v_mfma_f32_16x16x32_bf16 v[20:23], v[132:135], v[180:183], v[20:23]
	v_mfma_f32_16x16x32_bf16 v[16:19], v[140:143], v[180:183], v[16:19]
	v_mfma_f32_16x16x32_bf16 v[4:7], v[132:135], v[188:191], v[4:7]
	v_mfma_f32_16x16x32_bf16 v[0:3], v[140:143], v[188:191], v[0:3]
	s_setprio 0
	s_setprio 1
	v_mfma_f32_16x16x32_bf16 v[52:55], v[144:147], v[160:163], v[52:55]
	v_mfma_f32_16x16x32_bf16 v[48:51], v[152:155], v[160:163], v[48:51]
	v_mfma_f32_16x16x32_bf16 v[36:39], v[144:147], v[168:171], v[36:39]
	v_mfma_f32_16x16x32_bf16 v[32:35], v[152:155], v[168:171], v[32:35]
	v_mfma_f32_16x16x32_bf16 v[28:31], v[144:147], v[176:179], v[28:31]
	v_mfma_f32_16x16x32_bf16 v[24:27], v[152:155], v[176:179], v[24:27]
	v_mfma_f32_16x16x32_bf16 v[12:15], v[144:147], v[184:187], v[12:15]
	v_mfma_f32_16x16x32_bf16 v[8:11], v[152:155], v[184:187], v[8:11]
	v_mfma_f32_16x16x32_bf16 v[52:55], v[148:151], v[164:167], v[52:55]
	v_mfma_f32_16x16x32_bf16 v[48:51], v[156:159], v[164:167], v[48:51]
	v_mfma_f32_16x16x32_bf16 v[36:39], v[148:151], v[172:175], v[36:39]
	v_mfma_f32_16x16x32_bf16 v[32:35], v[156:159], v[172:175], v[32:35]
	v_mfma_f32_16x16x32_bf16 v[28:31], v[148:151], v[180:183], v[28:31]
	v_mfma_f32_16x16x32_bf16 v[24:27], v[156:159], v[180:183], v[24:27]
	v_mfma_f32_16x16x32_bf16 v[12:15], v[148:151], v[188:191], v[12:15]
	v_mfma_f32_16x16x32_bf16 v[8:11], v[156:159], v[188:191], v[8:11]
	s_setprio 0
	s_barrier
	v_add_u32_e32 v140, 0x18000, v200
	v_add_u32_e32 v156, 0x1c000, v200
	ds_read_b128 v[128:131], v140
	ds_read_b128 v[132:135], v140 offset:1024
	ds_read_b128 v[136:139], v140 offset:2048
	ds_read_b128 v[140:143], v140 offset:3072
	ds_read_b128 v[144:147], v156
	ds_read_b128 v[148:151], v156 offset:1024
	ds_read_b128 v[152:155], v156 offset:2048
	ds_read_b128 v[156:159], v156 offset:3072
	ds_read_b128 v[160:163], v201 offset:32768
	ds_read_b128 v[164:167], v201 offset:33792
	ds_read_b128 v[168:171], v201 offset:34816
	ds_read_b128 v[172:175], v201 offset:35840
	ds_read_b128 v[176:179], v201 offset:36864
	ds_read_b128 v[180:183], v201 offset:37888
	ds_read_b128 v[184:187], v201 offset:38912
	ds_read_b128 v[188:191], v201 offset:39936
	s_add_u32 s30, s76, 0x80000
	s_addc_u32 s31, s77, 0
	s_mov_b32 s49, m0
	s_mov_b32 m0, s7
	s_nop 2
	global_load_lds_dwordx4 v198, s[30:31]
	s_mov_b32 m0, s49
	s_nop 0
	s_mov_b32 s49, m0
	s_mov_b32 m0, s3
	s_nop 2
	global_load_lds_dwordx4 v199, s[30:31]
	s_mov_b32 m0, s49
	s_waitcnt vmcnt(8)
	s_waitcnt lgkmcnt(0)
	s_barrier
	s_setprio 1
	v_mfma_f32_16x16x32_bf16 v[124:127], v[128:131], v[160:163], v[124:127]
	v_mfma_f32_16x16x32_bf16 v[120:123], v[136:139], v[160:163], v[120:123]
	v_mfma_f32_16x16x32_bf16 v[108:111], v[128:131], v[168:171], v[108:111]
	v_mfma_f32_16x16x32_bf16 v[104:107], v[136:139], v[168:171], v[104:107]
	v_mfma_f32_16x16x32_bf16 v[92:95], v[128:131], v[176:179], v[92:95]
	v_mfma_f32_16x16x32_bf16 v[88:91], v[136:139], v[176:179], v[88:91]
	v_mfma_f32_16x16x32_bf16 v[76:79], v[128:131], v[184:187], v[76:79]
	v_mfma_f32_16x16x32_bf16 v[72:75], v[136:139], v[184:187], v[72:75]
	v_mfma_f32_16x16x32_bf16 v[124:127], v[132:135], v[164:167], v[124:127]
	v_mfma_f32_16x16x32_bf16 v[120:123], v[140:143], v[164:167], v[120:123]
	v_mfma_f32_16x16x32_bf16 v[108:111], v[132:135], v[172:175], v[108:111]
	v_mfma_f32_16x16x32_bf16 v[104:107], v[140:143], v[172:175], v[104:107]
	v_mfma_f32_16x16x32_bf16 v[92:95], v[132:135], v[180:183], v[92:95]
	v_mfma_f32_16x16x32_bf16 v[88:91], v[140:143], v[180:183], v[88:91]
	v_mfma_f32_16x16x32_bf16 v[76:79], v[132:135], v[188:191], v[76:79]
	v_mfma_f32_16x16x32_bf16 v[72:75], v[140:143], v[188:191], v[72:75]
	s_setprio 0
	s_setprio 1
	v_mfma_f32_16x16x32_bf16 v[116:119], v[144:147], v[160:163], v[116:119]
	v_mfma_f32_16x16x32_bf16 v[112:115], v[152:155], v[160:163], v[112:115]
	v_mfma_f32_16x16x32_bf16 v[100:103], v[144:147], v[168:171], v[100:103]
	v_mfma_f32_16x16x32_bf16 v[96:99], v[152:155], v[168:171], v[96:99]
	v_mfma_f32_16x16x32_bf16 v[84:87], v[144:147], v[176:179], v[84:87]
	v_mfma_f32_16x16x32_bf16 v[80:83], v[152:155], v[176:179], v[80:83]
	v_mfma_f32_16x16x32_bf16 v[68:71], v[144:147], v[184:187], v[68:71]
	v_mfma_f32_16x16x32_bf16 v[64:67], v[152:155], v[184:187], v[64:67]
	v_mfma_f32_16x16x32_bf16 v[116:119], v[148:151], v[164:167], v[116:119]
	v_mfma_f32_16x16x32_bf16 v[112:115], v[156:159], v[164:167], v[112:115]
	v_mfma_f32_16x16x32_bf16 v[100:103], v[148:151], v[172:175], v[100:103]
	v_mfma_f32_16x16x32_bf16 v[96:99], v[156:159], v[172:175], v[96:99]
	v_mfma_f32_16x16x32_bf16 v[84:87], v[148:151], v[180:183], v[84:87]
	v_mfma_f32_16x16x32_bf16 v[80:83], v[156:159], v[180:183], v[80:83]
	v_mfma_f32_16x16x32_bf16 v[68:71], v[148:151], v[188:191], v[68:71]
	v_mfma_f32_16x16x32_bf16 v[64:67], v[156:159], v[188:191], v[64:67]
	s_setprio 0
	s_barrier
	ds_read_b128 v[160:163], v201 offset:49152
	ds_read_b128 v[164:167], v201 offset:50176
	ds_read_b128 v[168:171], v201 offset:51200
	ds_read_b128 v[172:175], v201 offset:52224
	ds_read_b128 v[176:179], v201 offset:53248
	ds_read_b128 v[180:183], v201 offset:54272
	ds_read_b128 v[184:187], v201 offset:55296
	ds_read_b128 v[188:191], v201 offset:56320
	s_mov_b32 s30, m0
	s_mov_b32 m0, s2
	s_nop 2
	global_load_lds_dwordx4 v196, s[62:63]
	s_mov_b32 m0, s30
	s_nop 0
	s_mov_b32 s30, m0
	s_mov_b32 m0, s83
	s_nop 2
	global_load_lds_dwordx4 v197, s[62:63]
	s_mov_b32 m0, s30
	s_add_u32 s30, s36, 0x80
	s_addc_u32 s31, s37, 0
	s_mov_b32 s36, m0
	s_mov_b32 m0, s0
	s_nop 2
	global_load_lds_dwordx4 v196, s[30:31]
	s_mov_b32 m0, s36
	s_nop 0
	s_mov_b32 s36, m0
	s_mov_b32 m0, s1
	s_nop 2
	global_load_lds_dwordx4 v197, s[30:31]
	s_mov_b32 m0, s36
	s_mov_b32 s30, m0
	s_mov_b32 m0, s84
	s_nop 2
	global_load_lds_dwordx4 v198, s[56:57]
	s_mov_b32 m0, s30
	s_nop 0
	s_mov_b32 s30, m0
	s_mov_b32 m0, s85
	s_nop 2
	global_load_lds_dwordx4 v199, s[56:57]
	s_mov_b32 m0, s30
	s_waitcnt vmcnt(8)
	s_waitcnt lgkmcnt(0)
	s_barrier
	s_setprio 1
	v_mfma_f32_16x16x32_bf16 v[60:63], v[128:131], v[160:163], v[60:63]
	v_mfma_f32_16x16x32_bf16 v[56:59], v[136:139], v[160:163], v[56:59]
	v_mfma_f32_16x16x32_bf16 v[44:47], v[128:131], v[168:171], v[44:47]
	v_mfma_f32_16x16x32_bf16 v[40:43], v[136:139], v[168:171], v[40:43]
	v_mfma_f32_16x16x32_bf16 v[20:23], v[128:131], v[176:179], v[20:23]
	v_mfma_f32_16x16x32_bf16 v[16:19], v[136:139], v[176:179], v[16:19]
	v_mfma_f32_16x16x32_bf16 v[4:7], v[128:131], v[184:187], v[4:7]
	v_mfma_f32_16x16x32_bf16 v[0:3], v[136:139], v[184:187], v[0:3]
	v_mfma_f32_16x16x32_bf16 v[60:63], v[132:135], v[164:167], v[60:63]
	v_mfma_f32_16x16x32_bf16 v[56:59], v[140:143], v[164:167], v[56:59]
	v_mfma_f32_16x16x32_bf16 v[44:47], v[132:135], v[172:175], v[44:47]
	v_mfma_f32_16x16x32_bf16 v[40:43], v[140:143], v[172:175], v[40:43]
	v_mfma_f32_16x16x32_bf16 v[20:23], v[132:135], v[180:183], v[20:23]
	v_mfma_f32_16x16x32_bf16 v[16:19], v[140:143], v[180:183], v[16:19]
	v_mfma_f32_16x16x32_bf16 v[4:7], v[132:135], v[188:191], v[4:7]
	v_mfma_f32_16x16x32_bf16 v[0:3], v[140:143], v[188:191], v[0:3]
	s_setprio 0
	s_setprio 1
	v_mfma_f32_16x16x32_bf16 v[52:55], v[144:147], v[160:163], v[52:55]
	v_mfma_f32_16x16x32_bf16 v[48:51], v[152:155], v[160:163], v[48:51]
	v_mfma_f32_16x16x32_bf16 v[36:39], v[144:147], v[168:171], v[36:39]
	v_mfma_f32_16x16x32_bf16 v[32:35], v[152:155], v[168:171], v[32:35]
	v_mfma_f32_16x16x32_bf16 v[28:31], v[144:147], v[176:179], v[28:31]
	v_mfma_f32_16x16x32_bf16 v[24:27], v[152:155], v[176:179], v[24:27]
	v_mfma_f32_16x16x32_bf16 v[12:15], v[144:147], v[184:187], v[12:15]
	v_mfma_f32_16x16x32_bf16 v[8:11], v[152:155], v[184:187], v[8:11]
	v_mfma_f32_16x16x32_bf16 v[52:55], v[148:151], v[164:167], v[52:55]
	v_mfma_f32_16x16x32_bf16 v[48:51], v[156:159], v[164:167], v[48:51]
	v_mfma_f32_16x16x32_bf16 v[36:39], v[148:151], v[172:175], v[36:39]
	v_mfma_f32_16x16x32_bf16 v[32:35], v[156:159], v[172:175], v[32:35]
	v_mfma_f32_16x16x32_bf16 v[28:31], v[148:151], v[180:183], v[28:31]
	v_mfma_f32_16x16x32_bf16 v[24:27], v[156:159], v[180:183], v[24:27]
	v_mfma_f32_16x16x32_bf16 v[12:15], v[148:151], v[188:191], v[12:15]
	v_mfma_f32_16x16x32_bf16 v[8:11], v[156:159], v[188:191], v[8:11]
	s_setprio 0
	s_barrier
	s_add_i32 s48, s48, 2
	s_add_u32 s44, s44, 0x100
	s_addc_u32 s45, s45, 0
	s_add_u32 s46, s46, 0x100
	s_addc_u32 s47, s47, 0
	s_cmp_gt_u32 s48, 29
	s_mov_b64 s[30:31], s[34:35]
	s_cbranch_scc1 .LBB0_521

.LBB0_695:
	s_add_u32 s10, s6, s36
	s_addc_u32 s11, s7, s37
	s_add_u32 s76, s10, 0x100
	s_addc_u32 s77, s11, 0
	s_add_u32 s62, s14, s36
	s_addc_u32 s63, s15, s37
	s_add_u32 s62, s62, 0x100
	s_addc_u32 s63, s63, 0
	s_add_u32 s78, s16, s36
	v_add_u32_e32 v128, 0x10000, v134
	s_addc_u32 s79, s17, s37
	ds_read_b128 v[138:141], v128
	ds_read_b128 v[142:145], v128 offset:1024
	ds_read_b128 v[146:149], v128 offset:2048
	ds_read_b128 v[150:153], v128 offset:3072
	v_add_u32_e32 v128, 0x14000, v134
	s_add_u32 s78, s78, 0x100
	ds_read_b128 v[154:157], v128
	ds_read_b128 v[158:161], v128 offset:1024
	ds_read_b128 v[162:165], v128 offset:2048
	ds_read_b128 v[166:169], v128 offset:3072
	s_addc_u32 s79, s79, 0
	s_cmp_eq_u32 vcc_lo, 12
	s_cselect_b32 s82, s87, s62
	s_cselect_b32 s83, s86, s63
	s_cselect_b32 s63, s96, s79
	s_cselect_b32 s62, s97, s78
	s_cselect_b32 s80, s25, s76
	s_cselect_b32 s81, s23, s77
	s_add_u32 s78, s82, 0x80
	s_addc_u32 s79, s83, 0
	s_add_u32 s76, s80, 0x80
	s_addc_u32 s77, s81, 0
	ds_read_b128 v[170:173], v135
	ds_read_b128 v[174:177], v135 offset:1024
	ds_read_b128 v[178:181], v135 offset:2048
	ds_read_b128 v[182:185], v135 offset:3072
	ds_read_b128 v[186:189], v135 offset:4096
	ds_read_b128 v[190:193], v135 offset:5120
	ds_read_b128 v[194:197], v135 offset:6144
	ds_read_b128 v[198:201], v135 offset:7168
	s_add_u32 s10, s10, 0x40080
	s_addc_u32 s11, s11, 0
	s_mov_b32 vcc_hi, m0
	s_mov_b32 m0, s55
	s_nop 2
	global_load_lds_dwordx4 v132, s[10:11]
	s_mov_b32 m0, vcc_hi
	s_nop 0
	s_mov_b32 vcc_hi, m0
	s_mov_b32 m0, s84
	s_nop 2
	global_load_lds_dwordx4 v133, s[10:11]
	s_mov_b32 m0, vcc_hi
	s_waitcnt vmcnt(8)
	s_waitcnt lgkmcnt(0)
	s_barrier
	s_setprio 1
	v_mfma_scale_f32_16x16x128_f8f6f4 v[124:127], v[138:145], v[170:177], v[124:127], v136, v136 op_sel_hi:[0,0,0]
	v_mfma_scale_f32_16x16x128_f8f6f4 v[120:123], v[146:153], v[170:177], v[120:123], v136, v136 op_sel_hi:[0,0,0]
	v_mfma_scale_f32_16x16x128_f8f6f4 v[116:119], v[138:145], v[178:185], v[116:119], v136, v136 op_sel_hi:[0,0,0]
	v_mfma_scale_f32_16x16x128_f8f6f4 v[112:115], v[146:153], v[178:185], v[112:115], v136, v136 op_sel_hi:[0,0,0]
	v_mfma_scale_f32_16x16x128_f8f6f4 v[202:205], v[138:145], v[186:193], v[92:95], v136, v136 op_sel_hi:[0,0,0]
	v_mfma_scale_f32_16x16x128_f8f6f4 v[206:209], v[146:153], v[186:193], v[88:91], v136, v136 op_sel_hi:[0,0,0]
	v_mfma_scale_f32_16x16x128_f8f6f4 v[210:213], v[138:145], v[194:201], v[84:87], v136, v136 op_sel_hi:[0,0,0]
	v_mfma_scale_f32_16x16x128_f8f6f4 v[214:217], v[146:153], v[194:201], v[80:83], v136, v136 op_sel_hi:[0,0,0]
	s_setprio 0
	s_setprio 1
	v_mfma_scale_f32_16x16x128_f8f6f4 v[108:111], v[154:161], v[170:177], v[108:111], v136, v136 op_sel_hi:[0,0,0]
	v_mfma_scale_f32_16x16x128_f8f6f4 v[104:107], v[162:169], v[170:177], v[104:107], v136, v136 op_sel_hi:[0,0,0]
	v_mfma_scale_f32_16x16x128_f8f6f4 v[100:103], v[154:161], v[178:185], v[100:103], v136, v136 op_sel_hi:[0,0,0]
	v_mfma_scale_f32_16x16x128_f8f6f4 v[96:99], v[162:169], v[178:185], v[96:99], v136, v136 op_sel_hi:[0,0,0]
	v_mfma_scale_f32_16x16x128_f8f6f4 v[170:173], v[154:161], v[186:193], v[76:79], v136, v136 op_sel_hi:[0,0,0]
	v_mfma_scale_f32_16x16x128_f8f6f4 v[174:177], v[162:169], v[186:193], v[72:75], v136, v136 op_sel_hi:[0,0,0]
	v_mfma_scale_f32_16x16x128_f8f6f4 v[178:181], v[154:161], v[194:201], v[68:71], v136, v136 op_sel_hi:[0,0,0]
	v_mfma_scale_f32_16x16x128_f8f6f4 v[182:185], v[162:169], v[194:201], v[64:67], v136, v136 op_sel_hi:[0,0,0]
	s_setprio 0
	s_barrier
	s_nop 4
	ds_read_b128 v[64:67], v135 offset:16384
	ds_read_b128 v[68:71], v135 offset:17408
	ds_read_b128 v[72:75], v135 offset:18432
	ds_read_b128 v[76:79], v135 offset:19456
	ds_read_b128 v[80:83], v135 offset:20480
	ds_read_b128 v[84:87], v135 offset:21504
	ds_read_b128 v[88:91], v135 offset:22528
	ds_read_b128 v[92:95], v135 offset:23552
	s_mov_b32 s10, m0
	s_mov_b32 m0, s13
	s_nop 2
	global_load_lds_dwordx4 v137, s[82:83]
	s_mov_b32 m0, s10
	s_nop 0
	s_mov_b32 s10, m0
	s_mov_b32 m0, s43
	s_nop 2
	global_load_lds_dwordx4 v254, s[82:83]
	s_mov_b32 m0, s10
	s_nop 0
	s_mov_b32 s10, m0
	s_mov_b32 m0, s44
	s_nop 2
	global_load_lds_dwordx4 v137, s[62:63]
	s_mov_b32 m0, s10
	s_nop 0
	s_mov_b32 s10, m0
	s_mov_b32 m0, s45
	s_nop 2
	global_load_lds_dwordx4 v254, s[62:63]
	s_mov_b32 m0, s10
	s_nop 0
	s_mov_b32 s10, m0
	s_mov_b32 m0, s5
	s_nop 2
	global_load_lds_dwordx4 v132, s[80:81]
	s_mov_b32 m0, s10
	s_nop 0
	s_mov_b32 s10, m0
	s_mov_b32 m0, s46
	s_nop 2
	global_load_lds_dwordx4 v133, s[80:81]
	s_mov_b32 m0, s10
	s_waitcnt vmcnt(8)
	s_waitcnt lgkmcnt(0)
	s_barrier
	s_setprio 1
	v_mfma_scale_f32_16x16x128_f8f6f4 v[60:63], v[138:145], v[64:71], v[60:63], v136, v136 op_sel_hi:[0,0,0]
	v_mfma_scale_f32_16x16x128_f8f6f4 v[186:189], v[146:153], v[64:71], v[56:59], v136, v136 op_sel_hi:[0,0,0]
	v_mfma_scale_f32_16x16x128_f8f6f4 v[190:193], v[138:145], v[72:79], v[52:55], v136, v136 op_sel_hi:[0,0,0]
	v_mfma_scale_f32_16x16x128_f8f6f4 v[194:197], v[146:153], v[72:79], v[48:51], v136, v136 op_sel_hi:[0,0,0]
	v_mfma_scale_f32_16x16x128_f8f6f4 v[198:201], v[138:145], v[80:87], v[12:15], v136, v136 op_sel_hi:[0,0,0]
	v_mfma_scale_f32_16x16x128_f8f6f4 v[218:221], v[146:153], v[80:87], v[8:11], v136, v136 op_sel_hi:[0,0,0]
	v_mfma_scale_f32_16x16x128_f8f6f4 v[222:225], v[138:145], v[88:95], v[4:7], v136, v136 op_sel_hi:[0,0,0]
	v_mfma_scale_f32_16x16x128_f8f6f4 v[226:229], v[146:153], v[88:95], v[0:3], v136, v136 op_sel_hi:[0,0,0]
	s_setprio 0
	s_setprio 1
	v_mfma_scale_f32_16x16x128_f8f6f4 v[24:27], v[162:169], v[80:87], v[24:27], v136, v136 op_sel_hi:[0,0,0]
	v_mfma_scale_f32_16x16x128_f8f6f4 v[230:233], v[154:161], v[64:71], v[44:47], v136, v136 op_sel_hi:[0,0,0]
	v_mfma_scale_f32_16x16x128_f8f6f4 v[234:237], v[162:169], v[64:71], v[40:43], v136, v136 op_sel_hi:[0,0,0]
	v_mfma_scale_f32_16x16x128_f8f6f4 v[238:241], v[154:161], v[72:79], v[36:39], v136, v136 op_sel_hi:[0,0,0]
	v_mfma_scale_f32_16x16x128_f8f6f4 v[242:245], v[162:169], v[72:79], v[20:23], v136, v136 op_sel_hi:[0,0,0]
	v_mfma_scale_f32_16x16x128_f8f6f4 v[246:249], v[154:161], v[80:87], v[16:19], v136, v136 op_sel_hi:[0,0,0]
	v_mfma_scale_f32_16x16x128_f8f6f4 v[250:253], v[154:161], v[88:95], v[28:31], v136, v136 op_sel_hi:[0,0,0]
	v_mfma_scale_f32_16x16x128_f8f6f4 v[128:131], v[162:169], v[88:95], v[32:35], v136, v136 op_sel_hi:[0,0,0]
	s_setprio 0
	s_barrier
	v_add_u32_e32 v8, 0x18000, v134
	ds_read_b128 v[0:3], v8
	ds_read_b128 v[4:7], v8 offset:1024
	ds_read_b128 v[16:19], v8 offset:2048
	ds_read_b128 v[20:23], v8 offset:3072
	v_add_u32_e32 v8, 0x1c000, v134
	ds_read_b128 v[28:31], v8
	ds_read_b128 v[32:35], v8 offset:1024
	ds_read_b128 v[138:141], v8 offset:2048
	ds_read_b128 v[142:145], v8 offset:3072
	ds_read_b128 v[8:11], v135 offset:32768
	ds_read_b128 v[12:15], v135 offset:33792
	ds_read_b128 v[36:39], v135 offset:34816
	ds_read_b128 v[40:43], v135 offset:35840
	ds_read_b128 v[44:47], v135 offset:36864
	ds_read_b128 v[48:51], v135 offset:37888
	ds_read_b128 v[52:55], v135 offset:38912
	ds_read_b128 v[56:59], v135 offset:39936
	s_add_u32 s10, s80, 0x40000
	s_addc_u32 s11, s81, 0
	s_mov_b32 s80, m0
	s_mov_b32 m0, s47
	s_nop 2
	global_load_lds_dwordx4 v132, s[10:11]
	s_mov_b32 m0, s80
	s_nop 0
	s_mov_b32 s80, m0
	s_mov_b32 m0, s48
	s_nop 2
	global_load_lds_dwordx4 v133, s[10:11]
	s_mov_b32 m0, s80
	s_waitcnt vmcnt(8)
	s_waitcnt lgkmcnt(0)
	s_barrier
	s_setprio 1
	v_mfma_scale_f32_16x16x128_f8f6f4 v[124:127], v[0:7], v[8:15], v[124:127], v136, v136 op_sel_hi:[0,0,0]
	v_mfma_scale_f32_16x16x128_f8f6f4 v[120:123], v[16:23], v[8:15], v[120:123], v136, v136 op_sel_hi:[0,0,0]
	v_mfma_scale_f32_16x16x128_f8f6f4 v[116:119], v[0:7], v[36:43], v[116:119], v136, v136 op_sel_hi:[0,0,0]
	v_mfma_scale_f32_16x16x128_f8f6f4 v[112:115], v[16:23], v[36:43], v[112:115], v136, v136 op_sel_hi:[0,0,0]
	v_mfma_scale_f32_16x16x128_f8f6f4 v[92:95], v[0:7], v[44:51], v[202:205], v136, v136 op_sel_hi:[0,0,0]
	v_mfma_scale_f32_16x16x128_f8f6f4 v[88:91], v[16:23], v[44:51], v[206:209], v136, v136 op_sel_hi:[0,0,0]
	v_mfma_scale_f32_16x16x128_f8f6f4 v[84:87], v[0:7], v[52:59], v[210:213], v136, v136 op_sel_hi:[0,0,0]
	v_mfma_scale_f32_16x16x128_f8f6f4 v[80:83], v[16:23], v[52:59], v[214:217], v136, v136 op_sel_hi:[0,0,0]
	s_setprio 0
	s_setprio 1
	v_mfma_scale_f32_16x16x128_f8f6f4 v[108:111], v[28:35], v[8:15], v[108:111], v136, v136 op_sel_hi:[0,0,0]
	v_mfma_scale_f32_16x16x128_f8f6f4 v[104:107], v[138:145], v[8:15], v[104:107], v136, v136 op_sel_hi:[0,0,0]
	v_mfma_scale_f32_16x16x128_f8f6f4 v[100:103], v[28:35], v[36:43], v[100:103], v136, v136 op_sel_hi:[0,0,0]
	v_mfma_scale_f32_16x16x128_f8f6f4 v[96:99], v[138:145], v[36:43], v[96:99], v136, v136 op_sel_hi:[0,0,0]
	v_mfma_scale_f32_16x16x128_f8f6f4 v[76:79], v[28:35], v[44:51], v[170:173], v136, v136 op_sel_hi:[0,0,0]
	v_mfma_scale_f32_16x16x128_f8f6f4 v[72:75], v[138:145], v[44:51], v[174:177], v136, v136 op_sel_hi:[0,0,0]
	v_mfma_scale_f32_16x16x128_f8f6f4 v[68:71], v[28:35], v[52:59], v[178:181], v136, v136 op_sel_hi:[0,0,0]
	v_mfma_scale_f32_16x16x128_f8f6f4 v[64:67], v[138:145], v[52:59], v[182:185], v136, v136 op_sel_hi:[0,0,0]
	s_setprio 0
	s_barrier
	ds_read_b128 v[36:39], v135 offset:49152
	ds_read_b128 v[40:43], v135 offset:50176
	ds_read_b128 v[146:149], v135 offset:51200
	ds_read_b128 v[150:153], v135 offset:52224
	ds_read_b128 v[154:157], v135 offset:53248
	ds_read_b128 v[158:161], v135 offset:54272
	ds_read_b128 v[162:165], v135 offset:55296
	ds_read_b128 v[166:169], v135 offset:56320
	s_mov_b32 s10, m0
	s_mov_b32 m0, s49
	s_nop 2
	global_load_lds_dwordx4 v137, s[78:79]
	s_mov_b32 m0, s10
	s_nop 0
	s_mov_b32 s10, m0
	s_mov_b32 m0, s50
	s_nop 2
	global_load_lds_dwordx4 v254, s[78:79]
	s_mov_b32 m0, s10
	s_add_u32 s10, s62, 0x80
	s_addc_u32 s11, s63, 0
	s_mov_b32 s62, m0
	s_mov_b32 m0, s53
	s_nop 2
	global_load_lds_dwordx4 v137, s[10:11]
	s_mov_b32 m0, s62
	s_nop 0
	s_mov_b32 s62, m0
	s_mov_b32 m0, s54
	s_nop 2
	global_load_lds_dwordx4 v254, s[10:11]
	s_mov_b32 m0, s62
	s_mov_b32 s10, m0
	s_mov_b32 m0, s51
	s_nop 2
	global_load_lds_dwordx4 v132, s[76:77]
	s_mov_b32 m0, s10
	s_nop 0
	s_mov_b32 s10, m0
	s_mov_b32 m0, s52
	s_nop 2
	global_load_lds_dwordx4 v133, s[76:77]
	s_mov_b32 m0, s10
	s_waitcnt vmcnt(8)
	s_waitcnt lgkmcnt(0)
	s_barrier
	s_setprio 1
	v_mfma_scale_f32_16x16x128_f8f6f4 v[60:63], v[0:7], v[36:43], v[60:63], v136, v136 op_sel_hi:[0,0,0]
	v_mfma_scale_f32_16x16x128_f8f6f4 v[56:59], v[16:23], v[36:43], v[186:189], v136, v136 op_sel_hi:[0,0,0]
	v_mfma_scale_f32_16x16x128_f8f6f4 v[52:55], v[0:7], v[146:153], v[190:193], v136, v136 op_sel_hi:[0,0,0]
	v_mfma_scale_f32_16x16x128_f8f6f4 v[48:51], v[16:23], v[146:153], v[194:197], v136, v136 op_sel_hi:[0,0,0]
	v_mfma_scale_f32_16x16x128_f8f6f4 v[12:15], v[0:7], v[154:161], v[198:201], v136, v136 op_sel_hi:[0,0,0]
	v_mfma_scale_f32_16x16x128_f8f6f4 v[8:11], v[16:23], v[154:161], v[218:221], v136, v136 op_sel_hi:[0,0,0]
	v_mfma_scale_f32_16x16x128_f8f6f4 v[4:7], v[0:7], v[162:169], v[222:225], v136, v136 op_sel_hi:[0,0,0]
	v_mfma_scale_f32_16x16x128_f8f6f4 v[0:3], v[16:23], v[162:169], v[226:229], v136, v136 op_sel_hi:[0,0,0]
	s_setprio 0
	s_setprio 1
	v_mfma_scale_f32_16x16x128_f8f6f4 v[44:47], v[28:35], v[36:43], v[230:233], v136, v136 op_sel_hi:[0,0,0]
	v_mfma_scale_f32_16x16x128_f8f6f4 v[40:43], v[138:145], v[36:43], v[234:237], v136, v136 op_sel_hi:[0,0,0]
	v_mfma_scale_f32_16x16x128_f8f6f4 v[36:39], v[28:35], v[146:153], v[238:241], v136, v136 op_sel_hi:[0,0,0]
	v_mfma_scale_f32_16x16x128_f8f6f4 v[20:23], v[138:145], v[146:153], v[242:245], v136, v136 op_sel_hi:[0,0,0]
	v_mfma_scale_f32_16x16x128_f8f6f4 v[16:19], v[28:35], v[154:161], v[246:249], v136, v136 op_sel_hi:[0,0,0]
	v_mfma_scale_f32_16x16x128_f8f6f4 v[24:27], v[138:145], v[154:161], v[24:27], v136, v136 op_sel_hi:[0,0,0]
	v_mfma_scale_f32_16x16x128_f8f6f4 v[28:31], v[28:35], v[162:169], v[250:253], v136, v136 op_sel_hi:[0,0,0]
	v_mfma_scale_f32_16x16x128_f8f6f4 v[32:35], v[138:145], v[162:169], v[128:131], v136, v136 op_sel_hi:[0,0,0]
	s_setprio 0
	s_barrier
	s_add_i32 vcc_lo, vcc_lo, 2
	s_add_u32 s36, s36, 0x100
	s_addc_u32 s37, s37, 0
	s_cmp_gt_u32 vcc_lo, 13
	s_cbranch_scc0 .LBB0_695
	s_and_b64 vcc, exec, s[20:21]
	s_cbranch_vccz .LBB0_698
	s_barrier

.Lz7_a:
	s_waitcnt vmcnt(8)
	s_waitcnt lgkmcnt(0)
	s_barrier
	s_setprio 1
	v_mfma_scale_f32_16x16x128_f8f6f4 v[140:143], v[116:123], v[180:187], v[140:143], v153, v153 op_sel_hi:[0,0,0]
	v_mfma_scale_f32_16x16x128_f8f6f4 v[132:135], v[156:163], v[180:187], v[132:135], v153, v153 op_sel_hi:[0,0,0]
	v_mfma_scale_f32_16x16x128_f8f6f4 v[124:127], v[116:123], v[188:195], v[124:127], v153, v153 op_sel_hi:[0,0,0]
	v_mfma_scale_f32_16x16x128_f8f6f4 v[108:111], v[156:163], v[188:195], v[108:111], v153, v153 op_sel_hi:[0,0,0]
	v_mfma_scale_f32_16x16x128_f8f6f4 v[144:147], v[116:123], v[196:203], v[96:99], v153, v153 op_sel_hi:[0,0,0]
	v_mfma_scale_f32_16x16x128_f8f6f4 v[212:215], v[156:163], v[196:203], v[88:91], v153, v153 op_sel_hi:[0,0,0]
	v_mfma_scale_f32_16x16x128_f8f6f4 v[216:219], v[116:123], v[204:211], v[80:83], v153, v153 op_sel_hi:[0,0,0]
	v_mfma_scale_f32_16x16x128_f8f6f4 v[220:223], v[156:163], v[204:211], v[72:75], v153, v153 op_sel_hi:[0,0,0]
	s_setprio 0
	s_setprio 1
	v_mfma_scale_f32_16x16x128_f8f6f4 v[136:139], v[164:171], v[180:187], v[136:139], v153, v153 op_sel_hi:[0,0,0]
	v_mfma_scale_f32_16x16x128_f8f6f4 v[128:131], v[172:179], v[180:187], v[128:131], v153, v153 op_sel_hi:[0,0,0]
	v_mfma_scale_f32_16x16x128_f8f6f4 v[112:115], v[164:171], v[188:195], v[112:115], v153, v153 op_sel_hi:[0,0,0]
	v_mfma_scale_f32_16x16x128_f8f6f4 v[100:103], v[172:179], v[188:195], v[100:103], v153, v153 op_sel_hi:[0,0,0]
	v_mfma_scale_f32_16x16x128_f8f6f4 v[180:183], v[164:171], v[196:203], v[92:95], v153, v153 op_sel_hi:[0,0,0]
	v_mfma_scale_f32_16x16x128_f8f6f4 v[184:187], v[172:179], v[196:203], v[84:87], v153, v153 op_sel_hi:[0,0,0]
	v_mfma_scale_f32_16x16x128_f8f6f4 v[188:191], v[164:171], v[204:211], v[76:79], v153, v153 op_sel_hi:[0,0,0]
	v_mfma_scale_f32_16x16x128_f8f6f4 v[192:195], v[172:179], v[204:211], v[68:71], v153, v153 op_sel_hi:[0,0,0]
	s_setprio 0
	s_barrier
	s_nop 4
	ds_read_b128 v[68:71], v152 offset:16384
	ds_read_b128 v[72:75], v152 offset:17408
	ds_read_b128 v[76:79], v152 offset:18432
	ds_read_b128 v[80:83], v152 offset:19456
	ds_read_b128 v[84:87], v152 offset:20480
	ds_read_b128 v[88:91], v152 offset:21504
	ds_read_b128 v[92:95], v152 offset:22528
	ds_read_b128 v[96:99], v152 offset:23552
	s_mov_b32 s72, m0
	s_mov_b32 m0, s3
	s_nop 2
	global_load_lds_dwordx4 v252, s[64:65]
	s_mov_b32 m0, s72
	s_nop 0
	s_mov_b32 s72, m0
	s_mov_b32 m0, s27
	s_nop 2
	global_load_lds_dwordx4 v253, s[64:65]
	s_mov_b32 m0, s72
	s_mov_b32 s64, m0
	s_mov_b32 m0, s33
	s_nop 2
	global_load_lds_dwordx4 v252, s[62:63]
	s_mov_b32 m0, s64
	s_nop 0
	s_mov_b32 s64, m0
	s_mov_b32 m0, s40
	s_nop 2
	global_load_lds_dwordx4 v253, s[62:63]
	s_mov_b32 m0, s64
	s_mov_b32 s62, m0
	s_mov_b32 m0, s2
	s_nop 2
	global_load_lds_dwordx4 v104, s[60:61]
	s_mov_b32 m0, s62
	s_nop 0
	s_mov_b32 s62, m0
	s_mov_b32 m0, s41
	s_nop 2
	global_load_lds_dwordx4 v105, s[60:61]
	s_mov_b32 m0, s62
	s_cmp_lg_u32 s83, -2
	s_cbranch_scc1 .Lz7_b
	v_mov_b32_e32 v64, 0
	v_mov_b32_e32 v65, 0
	v_pk_mov_b32 v[66:67], v[64:65], v[64:65]
	v_pk_mov_b32 v[56:57], v[64:65], v[64:65]
	v_pk_mov_b32 v[58:59], v[64:65], v[64:65]
	v_pk_mov_b32 v[48:49], v[64:65], v[64:65]
	v_pk_mov_b32 v[50:51], v[64:65], v[64:65]
	v_pk_mov_b32 v[40:41], v[64:65], v[64:65]
	v_pk_mov_b32 v[42:43], v[64:65], v[64:65]
	v_pk_mov_b32 v[28:29], v[64:65], v[64:65]
	v_pk_mov_b32 v[30:31], v[64:65], v[64:65]
	v_pk_mov_b32 v[20:21], v[64:65], v[64:65]
	v_pk_mov_b32 v[22:23], v[64:65], v[64:65]
	v_pk_mov_b32 v[12:13], v[64:65], v[64:65]
	v_pk_mov_b32 v[14:15], v[64:65], v[64:65]
	v_pk_mov_b32 v[4:5], v[64:65], v[64:65]
	v_pk_mov_b32 v[6:7], v[64:65], v[64:65]
	v_pk_mov_b32 v[60:61], v[64:65], v[64:65]
	v_pk_mov_b32 v[62:63], v[64:65], v[64:65]
	v_pk_mov_b32 v[52:53], v[64:65], v[64:65]
	v_pk_mov_b32 v[54:55], v[64:65], v[64:65]
	v_pk_mov_b32 v[32:33], v[64:65], v[64:65]
	v_pk_mov_b32 v[34:35], v[64:65], v[64:65]
	v_pk_mov_b32 v[44:45], v[64:65], v[64:65]
	v_pk_mov_b32 v[46:47], v[64:65], v[64:65]
	v_pk_mov_b32 v[24:25], v[64:65], v[64:65]
	v_pk_mov_b32 v[26:27], v[64:65], v[64:65]
	v_pk_mov_b32 v[16:17], v[64:65], v[64:65]
	v_pk_mov_b32 v[18:19], v[64:65], v[64:65]
	v_pk_mov_b32 v[8:9], v[64:65], v[64:65]
	v_pk_mov_b32 v[10:11], v[64:65], v[64:65]
	v_pk_mov_b32 v[0:1], v[64:65], v[64:65]
	v_pk_mov_b32 v[2:3], v[64:65], v[64:65]

.Lp7_rag_1:
	s_barrier
	s_nop 3
	v_add_u32_e32 v8, 0x18000, v254
	ds_read_b128 v[0:3], v8
	ds_read_b128 v[4:7], v8 offset:1024
	ds_read_b128 v[116:119], v8 offset:2048
	ds_read_b128 v[120:123], v8 offset:3072
	v_add_u32_e32 v8, 0x1c000, v254
	ds_read_b128 v[156:159], v8
	ds_read_b128 v[160:163], v8 offset:1024
	ds_read_b128 v[164:167], v8 offset:2048
	ds_read_b128 v[168:171], v8 offset:3072
	ds_read_b128 v[8:11], v152 offset:32768
	ds_read_b128 v[12:15], v152 offset:33792
	ds_read_b128 v[16:19], v152 offset:34816
	ds_read_b128 v[20:23], v152 offset:35840
	ds_read_b128 v[24:27], v152 offset:36864
	ds_read_b128 v[28:31], v152 offset:37888
	ds_read_b128 v[40:43], v152 offset:38912
	ds_read_b128 v[44:47], v152 offset:39936
	s_mov_b32 s62, m0
	s_mov_b32 m0, s42
	s_nop 2
	global_load_lds_dwordx4 v106, s[60:61]
	s_mov_b32 m0, s62
	s_nop 0
	s_mov_b32 s62, m0
	s_mov_b32 m0, s43
	s_nop 2
	global_load_lds_dwordx4 v107, s[60:61]
	s_mov_b32 m0, s62
	s_waitcnt vmcnt(8)
	s_waitcnt lgkmcnt(0)
	s_barrier
	s_setprio 1
	v_mfma_scale_f32_16x16x128_f8f6f4 v[140:143], v[0:7], v[8:15], v[140:143], v153, v153 op_sel_hi:[0,0,0]
	v_mfma_scale_f32_16x16x128_f8f6f4 v[132:135], v[116:123], v[8:15], v[132:135], v153, v153 op_sel_hi:[0,0,0]
	v_mfma_scale_f32_16x16x128_f8f6f4 v[124:127], v[0:7], v[16:23], v[124:127], v153, v153 op_sel_hi:[0,0,0]
	v_mfma_scale_f32_16x16x128_f8f6f4 v[108:111], v[116:123], v[16:23], v[108:111], v153, v153 op_sel_hi:[0,0,0]
	v_mfma_scale_f32_16x16x128_f8f6f4 v[96:99], v[0:7], v[24:31], v[144:147], v153, v153 op_sel_hi:[0,0,0]
	v_mfma_scale_f32_16x16x128_f8f6f4 v[88:91], v[116:123], v[24:31], v[212:215], v153, v153 op_sel_hi:[0,0,0]
	v_mfma_scale_f32_16x16x128_f8f6f4 v[80:83], v[0:7], v[40:47], v[216:219], v153, v153 op_sel_hi:[0,0,0]
	v_mfma_scale_f32_16x16x128_f8f6f4 v[72:75], v[116:123], v[40:47], v[220:223], v153, v153 op_sel_hi:[0,0,0]
	s_setprio 0
	s_setprio 1
	v_mfma_scale_f32_16x16x128_f8f6f4 v[136:139], v[156:163], v[8:15], v[136:139], v153, v153 op_sel_hi:[0,0,0]
	v_mfma_scale_f32_16x16x128_f8f6f4 v[128:131], v[164:171], v[8:15], v[128:131], v153, v153 op_sel_hi:[0,0,0]
	v_mfma_scale_f32_16x16x128_f8f6f4 v[112:115], v[156:163], v[16:23], v[112:115], v153, v153 op_sel_hi:[0,0,0]
	v_mfma_scale_f32_16x16x128_f8f6f4 v[100:103], v[164:171], v[16:23], v[100:103], v153, v153 op_sel_hi:[0,0,0]
	v_mfma_scale_f32_16x16x128_f8f6f4 v[92:95], v[156:163], v[24:31], v[180:183], v153, v153 op_sel_hi:[0,0,0]
	v_mfma_scale_f32_16x16x128_f8f6f4 v[84:87], v[164:171], v[24:31], v[184:187], v153, v153 op_sel_hi:[0,0,0]
	v_mfma_scale_f32_16x16x128_f8f6f4 v[76:79], v[156:163], v[40:47], v[188:191], v153, v153 op_sel_hi:[0,0,0]
	v_mfma_scale_f32_16x16x128_f8f6f4 v[68:71], v[164:171], v[40:47], v[192:195], v153, v153 op_sel_hi:[0,0,0]
	s_setprio 0
	s_barrier
	ds_read_b128 v[172:175], v152 offset:49152
	ds_read_b128 v[176:179], v152 offset:50176
	ds_read_b128 v[180:183], v152 offset:51200
	ds_read_b128 v[184:187], v152 offset:52224
	ds_read_b128 v[188:191], v152 offset:53248
	ds_read_b128 v[192:195], v152 offset:54272
	ds_read_b128 v[196:199], v152 offset:55296
	ds_read_b128 v[200:203], v152 offset:56320
	s_mov_b32 s60, m0
	s_mov_b32 m0, s46
	s_nop 2
	global_load_lds_dwordx4 v252, s[56:57]
	s_mov_b32 m0, s60
	s_nop 0
	s_mov_b32 s60, m0
	s_mov_b32 m0, s48
	s_nop 2
	global_load_lds_dwordx4 v253, s[56:57]
	s_mov_b32 m0, s60
	s_mov_b32 s56, m0
	s_mov_b32 m0, s53
	s_nop 2
	global_load_lds_dwordx4 v252, s[58:59]
	s_mov_b32 m0, s56
	s_nop 0
	s_mov_b32 s56, m0
	s_mov_b32 m0, s54
	s_nop 2
	global_load_lds_dwordx4 v253, s[58:59]
	s_mov_b32 m0, s56
	s_nop 0
	s_mov_b32 s56, m0
	s_mov_b32 m0, s49
	s_nop 2
	global_load_lds_dwordx4 v104, s[36:37]
	s_mov_b32 m0, s56
	s_nop 0
	s_mov_b32 s56, m0
	s_mov_b32 m0, s52
	s_nop 2
	global_load_lds_dwordx4 v105, s[36:37]
	s_mov_b32 m0, s56
	s_waitcnt vmcnt(8)
	s_waitcnt lgkmcnt(0)
	s_cmp_lg_u32 s32, 0
	s_cbranch_scc1 .Lp7_ragskip_3
	s_barrier
	s_setprio 1
	s_waitcnt lgkmcnt(6)
	v_mfma_scale_f32_16x16x128_f8f6f4 v[64:67], v[0:7], v[172:179], v[64:67], v153, v153 op_sel_hi:[0,0,0]
	v_mfma_scale_f32_16x16x128_f8f6f4 v[56:59], v[116:123], v[172:179], v[56:59], v153, v153 op_sel_hi:[0,0,0]
	s_waitcnt lgkmcnt(4)
	v_mfma_scale_f32_16x16x128_f8f6f4 v[48:51], v[0:7], v[180:187], v[48:51], v153, v153 op_sel_hi:[0,0,0]
	v_mfma_scale_f32_16x16x128_f8f6f4 v[40:43], v[116:123], v[180:187], v[204:207], v153, v153 op_sel_hi:[0,0,0]
	s_waitcnt lgkmcnt(2)
	v_mfma_scale_f32_16x16x128_f8f6f4 v[28:31], v[0:7], v[188:195], v[208:211], v153, v153 op_sel_hi:[0,0,0]
	v_mfma_scale_f32_16x16x128_f8f6f4 v[20:23], v[116:123], v[188:195], v[224:227], v153, v153 op_sel_hi:[0,0,0]
	s_waitcnt lgkmcnt(0)
	v_mfma_scale_f32_16x16x128_f8f6f4 v[12:15], v[0:7], v[196:203], v[228:231], v153, v153 op_sel_hi:[0,0,0]
	v_mfma_scale_f32_16x16x128_f8f6f4 v[4:7], v[116:123], v[196:203], v[232:235], v153, v153 op_sel_hi:[0,0,0]
	s_setprio 0
	s_setprio 1
	v_mfma_scale_f32_16x16x128_f8f6f4 v[60:63], v[156:163], v[172:179], v[60:63], v153, v153 op_sel_hi:[0,0,0]
	v_mfma_scale_f32_16x16x128_f8f6f4 v[52:55], v[164:171], v[172:179], v[52:55], v153, v153 op_sel_hi:[0,0,0]
	v_mfma_scale_f32_16x16x128_f8f6f4 v[44:47], v[156:163], v[180:187], v[236:239], v153, v153 op_sel_hi:[0,0,0]
	v_mfma_scale_f32_16x16x128_f8f6f4 v[32:35], v[164:171], v[180:187], v[32:35], v153, v153 op_sel_hi:[0,0,0]
	v_mfma_scale_f32_16x16x128_f8f6f4 v[24:27], v[156:163], v[188:195], v[240:243], v153, v153 op_sel_hi:[0,0,0]
	v_mfma_scale_f32_16x16x128_f8f6f4 v[16:19], v[164:171], v[188:195], v[244:247], v153, v153 op_sel_hi:[0,0,0]
	v_mfma_scale_f32_16x16x128_f8f6f4 v[8:11], v[156:163], v[196:203], v[248:251], v153, v153 op_sel_hi:[0,0,0]
	v_mfma_scale_f32_16x16x128_f8f6f4 v[0:3], v[164:171], v[196:203], v[148:151], v153, v153 op_sel_hi:[0,0,0]
	s_setprio 0

.Lz8_a:
	s_waitcnt vmcnt(8)
	s_waitcnt lgkmcnt(0)
	s_barrier
	s_setprio 1
	v_mfma_scale_f32_16x16x128_f8f6f4 v[124:127], v[128:135], v[172:179], v[124:127], v169, v169 op_sel_hi:[0,0,0]
	v_mfma_scale_f32_16x16x128_f8f6f4 v[120:123], v[136:143], v[172:179], v[120:123], v169, v169 op_sel_hi:[0,0,0]
	v_mfma_scale_f32_16x16x128_f8f6f4 v[108:111], v[128:135], v[180:187], v[108:111], v169, v169 op_sel_hi:[0,0,0]
	v_mfma_scale_f32_16x16x128_f8f6f4 v[104:107], v[136:143], v[180:187], v[104:107], v169, v169 op_sel_hi:[0,0,0]
	v_mfma_scale_f32_16x16x128_f8f6f4 v[204:207], v[128:135], v[188:195], v[92:95], v169, v169 op_sel_hi:[0,0,0]
	v_mfma_scale_f32_16x16x128_f8f6f4 v[208:211], v[136:143], v[188:195], v[88:91], v169, v169 op_sel_hi:[0,0,0]
	v_mfma_scale_f32_16x16x128_f8f6f4 v[212:215], v[128:135], v[196:203], v[76:79], v169, v169 op_sel_hi:[0,0,0]
	v_mfma_scale_f32_16x16x128_f8f6f4 v[216:219], v[136:143], v[196:203], v[72:75], v169, v169 op_sel_hi:[0,0,0]
	s_setprio 0
	s_setprio 1
	v_mfma_scale_f32_16x16x128_f8f6f4 v[116:119], v[144:151], v[172:179], v[116:119], v169, v169 op_sel_hi:[0,0,0]
	v_mfma_scale_f32_16x16x128_f8f6f4 v[112:115], v[152:159], v[172:179], v[112:115], v169, v169 op_sel_hi:[0,0,0]
	v_mfma_scale_f32_16x16x128_f8f6f4 v[100:103], v[144:151], v[180:187], v[100:103], v169, v169 op_sel_hi:[0,0,0]
	v_mfma_scale_f32_16x16x128_f8f6f4 v[96:99], v[152:159], v[180:187], v[96:99], v169, v169 op_sel_hi:[0,0,0]
	v_mfma_scale_f32_16x16x128_f8f6f4 v[172:175], v[144:151], v[188:195], v[84:87], v169, v169 op_sel_hi:[0,0,0]
	v_mfma_scale_f32_16x16x128_f8f6f4 v[176:179], v[152:159], v[188:195], v[80:83], v169, v169 op_sel_hi:[0,0,0]
	v_mfma_scale_f32_16x16x128_f8f6f4 v[180:183], v[144:151], v[196:203], v[68:71], v169, v169 op_sel_hi:[0,0,0]
	v_mfma_scale_f32_16x16x128_f8f6f4 v[184:187], v[152:159], v[196:203], v[64:67], v169, v169 op_sel_hi:[0,0,0]
	s_setprio 0
	s_barrier
	s_nop 4
	ds_read_b128 v[64:67], v168 offset:16384
	ds_read_b128 v[68:71], v168 offset:17408
	ds_read_b128 v[72:75], v168 offset:18432
	ds_read_b128 v[76:79], v168 offset:19456
	ds_read_b128 v[80:83], v168 offset:20480
	ds_read_b128 v[84:87], v168 offset:21504
	ds_read_b128 v[88:91], v168 offset:22528
	ds_read_b128 v[92:95], v168 offset:23552
	s_mov_b32 s34, m0
	s_mov_b32 m0, s31
	s_nop 2
	global_load_lds_dwordx4 v162, s[60:61]
	s_mov_b32 m0, s34
	s_nop 0
	s_mov_b32 s34, m0
	s_mov_b32 m0, s44
	s_nop 2
	global_load_lds_dwordx4 v163, s[60:61]
	s_mov_b32 m0, s34
	s_nop 0
	s_mov_b32 s34, m0
	s_mov_b32 m0, s45
	s_nop 2
	global_load_lds_dwordx4 v162, s[46:47]
	s_mov_b32 m0, s34
	s_nop 0
	s_mov_b32 s34, m0
	s_mov_b32 m0, s48
	s_nop 2
	global_load_lds_dwordx4 v163, s[46:47]
	s_mov_b32 m0, s34
	s_nop 0
	s_mov_b32 s34, m0
	s_mov_b32 m0, s2
	s_nop 2
	global_load_lds_dwordx4 v164, s[58:59]
	s_mov_b32 m0, s34
	s_nop 0
	s_mov_b32 s34, m0
	s_mov_b32 m0, s49
	s_nop 2
	global_load_lds_dwordx4 v165, s[58:59]
	s_mov_b32 m0, s34
	s_cmp_lg_u32 s80, -2
	s_cbranch_scc1 .Lz8_b
	v_mov_b32_e32 v60, 0
	v_mov_b32_e32 v61, 0
	v_pk_mov_b32 v[62:63], v[60:61], v[60:61]
	v_pk_mov_b32 v[56:57], v[60:61], v[60:61]
	v_pk_mov_b32 v[58:59], v[60:61], v[60:61]
	v_pk_mov_b32 v[44:45], v[60:61], v[60:61]
	v_pk_mov_b32 v[46:47], v[60:61], v[60:61]
	v_pk_mov_b32 v[40:41], v[60:61], v[60:61]
	v_pk_mov_b32 v[42:43], v[60:61], v[60:61]
	v_pk_mov_b32 v[24:25], v[60:61], v[60:61]
	v_pk_mov_b32 v[26:27], v[60:61], v[60:61]
	v_pk_mov_b32 v[12:13], v[60:61], v[60:61]
	v_pk_mov_b32 v[14:15], v[60:61], v[60:61]
	v_pk_mov_b32 v[4:5], v[60:61], v[60:61]
	v_pk_mov_b32 v[6:7], v[60:61], v[60:61]
	v_pk_mov_b32 v[0:1], v[60:61], v[60:61]
	v_pk_mov_b32 v[2:3], v[60:61], v[60:61]
	v_pk_mov_b32 v[52:53], v[60:61], v[60:61]
	v_pk_mov_b32 v[54:55], v[60:61], v[60:61]
	v_pk_mov_b32 v[48:49], v[60:61], v[60:61]
	v_pk_mov_b32 v[50:51], v[60:61], v[60:61]
	v_pk_mov_b32 v[28:29], v[60:61], v[60:61]
	v_pk_mov_b32 v[30:31], v[60:61], v[60:61]
	v_pk_mov_b32 v[20:21], v[60:61], v[60:61]
	v_pk_mov_b32 v[22:23], v[60:61], v[60:61]
	v_pk_mov_b32 v[36:37], v[60:61], v[60:61]
	v_pk_mov_b32 v[38:39], v[60:61], v[60:61]
	v_pk_mov_b32 v[32:33], v[60:61], v[60:61]
	v_pk_mov_b32 v[34:35], v[60:61], v[60:61]
	v_pk_mov_b32 v[16:17], v[60:61], v[60:61]
	v_pk_mov_b32 v[18:19], v[60:61], v[60:61]
	v_pk_mov_b32 v[8:9], v[60:61], v[60:61]
	v_pk_mov_b32 v[10:11], v[60:61], v[60:61]

.Lp8_rag_1:
	s_barrier
	ds_read_b128 v[0:3], v170
	ds_read_b128 v[4:7], v170 offset:1024
	s_nop 1
	ds_read_b128 v[16:19], v170 offset:2048
	ds_read_b128 v[20:23], v170 offset:3072
	ds_read_b128 v[128:131], v171
	ds_read_b128 v[132:135], v171 offset:1024
	ds_read_b128 v[136:139], v171 offset:2048
	ds_read_b128 v[140:143], v171 offset:3072
	ds_read_b128 v[8:11], v168 offset:32768
	ds_read_b128 v[12:15], v168 offset:33792
	ds_read_b128 v[24:27], v168 offset:34816
	ds_read_b128 v[28:31], v168 offset:35840
	ds_read_b128 v[32:35], v168 offset:36864
	ds_read_b128 v[36:39], v168 offset:37888
	ds_read_b128 v[40:43], v168 offset:38912
	ds_read_b128 v[44:47], v168 offset:39936
	s_add_u32 s34, s58, 0x40000
	s_addc_u32 s35, s59, 0
	s_mov_b32 s58, m0
	s_mov_b32 m0, s52
	s_nop 2
	global_load_lds_dwordx4 v164, s[34:35]
	s_mov_b32 m0, s58
	s_nop 0
	s_mov_b32 s58, m0
	s_mov_b32 m0, s53
	s_nop 2
	global_load_lds_dwordx4 v165, s[34:35]
	s_mov_b32 m0, s58
	s_waitcnt vmcnt(8)
	s_waitcnt lgkmcnt(0)
	s_barrier
	s_setprio 1
	v_mfma_scale_f32_16x16x128_f8f6f4 v[124:127], v[0:7], v[8:15], v[124:127], v169, v169 op_sel_hi:[0,0,0]
	v_mfma_scale_f32_16x16x128_f8f6f4 v[120:123], v[16:23], v[8:15], v[120:123], v169, v169 op_sel_hi:[0,0,0]
	v_mfma_scale_f32_16x16x128_f8f6f4 v[108:111], v[0:7], v[24:31], v[108:111], v169, v169 op_sel_hi:[0,0,0]
	v_mfma_scale_f32_16x16x128_f8f6f4 v[104:107], v[16:23], v[24:31], v[104:107], v169, v169 op_sel_hi:[0,0,0]
	v_mfma_scale_f32_16x16x128_f8f6f4 v[92:95], v[0:7], v[32:39], v[204:207], v169, v169 op_sel_hi:[0,0,0]
	v_mfma_scale_f32_16x16x128_f8f6f4 v[88:91], v[16:23], v[32:39], v[208:211], v169, v169 op_sel_hi:[0,0,0]
	v_mfma_scale_f32_16x16x128_f8f6f4 v[76:79], v[0:7], v[40:47], v[212:215], v169, v169 op_sel_hi:[0,0,0]
	v_mfma_scale_f32_16x16x128_f8f6f4 v[72:75], v[16:23], v[40:47], v[216:219], v169, v169 op_sel_hi:[0,0,0]
	s_setprio 0
	s_setprio 1
	v_mfma_scale_f32_16x16x128_f8f6f4 v[116:119], v[128:135], v[8:15], v[116:119], v169, v169 op_sel_hi:[0,0,0]
	v_mfma_scale_f32_16x16x128_f8f6f4 v[112:115], v[136:143], v[8:15], v[112:115], v169, v169 op_sel_hi:[0,0,0]
	v_mfma_scale_f32_16x16x128_f8f6f4 v[100:103], v[128:135], v[24:31], v[100:103], v169, v169 op_sel_hi:[0,0,0]
	v_mfma_scale_f32_16x16x128_f8f6f4 v[96:99], v[136:143], v[24:31], v[96:99], v169, v169 op_sel_hi:[0,0,0]
	v_mfma_scale_f32_16x16x128_f8f6f4 v[84:87], v[128:135], v[32:39], v[172:175], v169, v169 op_sel_hi:[0,0,0]
	v_mfma_scale_f32_16x16x128_f8f6f4 v[80:83], v[136:143], v[32:39], v[176:179], v169, v169 op_sel_hi:[0,0,0]
	v_mfma_scale_f32_16x16x128_f8f6f4 v[68:71], v[128:135], v[40:47], v[180:183], v169, v169 op_sel_hi:[0,0,0]
	v_mfma_scale_f32_16x16x128_f8f6f4 v[64:67], v[136:143], v[40:47], v[184:187], v169, v169 op_sel_hi:[0,0,0]
	s_setprio 0
	s_barrier
	ds_read_b128 v[28:31], v168 offset:49152
	ds_read_b128 v[32:35], v168 offset:50176
	ds_read_b128 v[144:147], v168 offset:51200
	ds_read_b128 v[148:151], v168 offset:52224
	ds_read_b128 v[152:155], v168 offset:53248
	ds_read_b128 v[156:159], v168 offset:54272
	ds_read_b128 v[172:175], v168 offset:55296
	ds_read_b128 v[176:179], v168 offset:56320
	s_mov_b32 s34, m0
	s_mov_b32 m0, s54
	s_nop 2
	global_load_lds_dwordx4 v162, s[56:57]
	s_mov_b32 m0, s34
	s_nop 0
	s_mov_b32 s34, m0
	s_mov_b32 m0, s55
	s_nop 2
	global_load_lds_dwordx4 v163, s[56:57]
	s_mov_b32 m0, s34
	s_add_u32 s34, s46, 0x80
	s_addc_u32 s35, s47, 0
	s_mov_b32 s46, m0
	s_mov_b32 m0, s64
	s_nop 2
	global_load_lds_dwordx4 v162, s[34:35]
	s_mov_b32 m0, s46
	s_nop 0
	s_mov_b32 s46, m0
	s_mov_b32 m0, s65
	s_nop 2
	global_load_lds_dwordx4 v163, s[34:35]
	s_mov_b32 m0, s46
	s_mov_b32 s34, m0
	s_mov_b32 m0, s62
	s_nop 2
	global_load_lds_dwordx4 v164, s[50:51]
	s_mov_b32 m0, s34
	s_nop 0
	s_mov_b32 s34, m0
	s_mov_b32 m0, s63
	s_nop 2
	global_load_lds_dwordx4 v165, s[50:51]
	s_mov_b32 m0, s34
	s_waitcnt vmcnt(8)
	s_waitcnt lgkmcnt(0)
	s_cmp_le_i32 s42, s32
	s_cbranch_scc1 .Lp8_ragskip_3
	s_barrier
	s_setprio 1
	s_waitcnt lgkmcnt(6)
	v_mfma_scale_f32_16x16x128_f8f6f4 v[60:63], v[0:7], v[28:35], v[60:63], v169, v169 op_sel_hi:[0,0,0]
	v_mfma_scale_f32_16x16x128_f8f6f4 v[56:59], v[16:23], v[28:35], v[56:59], v169, v169 op_sel_hi:[0,0,0]
	s_waitcnt lgkmcnt(4)
	v_mfma_scale_f32_16x16x128_f8f6f4 v[44:47], v[0:7], v[144:151], v[188:191], v169, v169 op_sel_hi:[0,0,0]
	v_mfma_scale_f32_16x16x128_f8f6f4 v[40:43], v[16:23], v[144:151], v[192:195], v169, v169 op_sel_hi:[0,0,0]
	s_waitcnt lgkmcnt(2)
	v_mfma_scale_f32_16x16x128_f8f6f4 v[24:27], v[0:7], v[152:159], v[196:199], v169, v169 op_sel_hi:[0,0,0]
	v_mfma_scale_f32_16x16x128_f8f6f4 v[12:15], v[16:23], v[152:159], v[200:203], v169, v169 op_sel_hi:[0,0,0]
	s_waitcnt lgkmcnt(0)
	v_mfma_scale_f32_16x16x128_f8f6f4 v[4:7], v[0:7], v[172:179], v[220:223], v169, v169 op_sel_hi:[0,0,0]
	v_mfma_scale_f32_16x16x128_f8f6f4 v[0:3], v[16:23], v[172:179], v[224:227], v169, v169 op_sel_hi:[0,0,0]
	s_setprio 0
	s_setprio 1
	v_mfma_scale_f32_16x16x128_f8f6f4 v[52:55], v[128:135], v[28:35], v[52:55], v169, v169 op_sel_hi:[0,0,0]
	v_mfma_scale_f32_16x16x128_f8f6f4 v[48:51], v[136:143], v[28:35], v[48:51], v169, v169 op_sel_hi:[0,0,0]
	v_mfma_scale_f32_16x16x128_f8f6f4 v[28:31], v[128:135], v[144:151], v[228:231], v169, v169 op_sel_hi:[0,0,0]
	v_mfma_scale_f32_16x16x128_f8f6f4 v[20:23], v[136:143], v[144:151], v[232:235], v169, v169 op_sel_hi:[0,0,0]
	v_mfma_scale_f32_16x16x128_f8f6f4 v[36:39], v[128:135], v[152:159], v[236:239], v169, v169 op_sel_hi:[0,0,0]
	v_mfma_scale_f32_16x16x128_f8f6f4 v[32:35], v[136:143], v[152:159], v[240:243], v169, v169 op_sel_hi:[0,0,0]
	v_mfma_scale_f32_16x16x128_f8f6f4 v[16:19], v[128:135], v[172:179], v[244:247], v169, v169 op_sel_hi:[0,0,0]
	v_mfma_scale_f32_16x16x128_f8f6f4 v[8:11], v[136:143], v[172:179], v[248:251], v169, v169 op_sel_hi:[0,0,0]
	s_setprio 0

.LBB0_1186:
	ds_read_b128 v[0:3], v134
	ds_read_b128 v[4:7], v134 offset:1024
	ds_read_b128 v[8:11], v134 offset:2048
	ds_read_b128 v[12:15], v134 offset:3072
	ds_read_b128 v[16:19], v136
	ds_read_b128 v[20:23], v136 offset:1024
	ds_read_b128 v[24:27], v136 offset:2048
	ds_read_b128 v[28:31], v136 offset:3072
	s_and_b64 s[24:25], s[18:19], exec
	s_cselect_b32 s27, s13, s21
	s_cselect_b32 s26, s12, s20
	s_cselect_b32 s29, s15, s31
	s_cselect_b32 s28, s14, s30
	s_cselect_b32 s25, s17, s23
	s_cselect_b32 s24, s16, s22
	s_add_u32 s36, s20, 0x100
	s_addc_u32 s37, s21, 0
	s_add_u32 s46, s30, 0x100
	s_addc_u32 s47, s31, 0
	s_add_u32 s40, s22, 0x100
	s_addc_u32 s41, s23, 0
	s_add_u32 s34, s30, 0x180
	s_addc_u32 s35, s31, 0
	s_add_u32 s30, s20, 0x180
	s_addc_u32 s31, s21, 0
	ds_read_b128 v[32:35], v137
	ds_read_b128 v[36:39], v137 offset:1024
	ds_read_b128 v[40:43], v137 offset:2048
	ds_read_b128 v[44:47], v137 offset:3072
	ds_read_b128 v[48:51], v137 offset:4096
	ds_read_b128 v[52:55], v137 offset:5120
	ds_read_b128 v[56:59], v137 offset:6144
	ds_read_b128 v[60:63], v137 offset:7168
	s_add_u32 s74, s20, 0x10080
	s_addc_u32 s75, s21, 0
	s_mov_b32 s73, m0
	s_mov_b32 m0, s62
	s_nop 2
	global_load_lds_dwordx4 v132, s[74:75]
	s_mov_b32 m0, s73
	s_nop 0
	s_mov_b32 s73, m0
	s_mov_b32 m0, s63
	s_nop 2
	global_load_lds_dwordx4 v133, s[74:75]
	s_mov_b32 m0, s73
	s_waitcnt vmcnt(8)
	s_waitcnt lgkmcnt(0)
	s_barrier
	s_setprio 1
	v_mfma_f32_16x16x32_bf16 v[64:67], v[0:3], v[32:35], 0
	v_mfma_f32_16x16x32_bf16 v[68:71], v[8:11], v[32:35], 0
	v_mfma_f32_16x16x32_bf16 v[72:75], v[0:3], v[40:43], 0
	v_mfma_f32_16x16x32_bf16 v[76:79], v[8:11], v[40:43], 0
	v_mfma_f32_16x16x32_bf16 v[80:83], v[0:3], v[48:51], 0
	v_mfma_f32_16x16x32_bf16 v[84:87], v[8:11], v[48:51], 0
	v_mfma_f32_16x16x32_bf16 v[88:91], v[0:3], v[56:59], 0
	v_mfma_f32_16x16x32_bf16 v[92:95], v[8:11], v[56:59], 0
	v_mfma_f32_16x16x32_bf16 v[64:67], v[4:7], v[36:39], v[64:67]
	v_mfma_f32_16x16x32_bf16 v[68:71], v[12:15], v[36:39], v[68:71]
	v_mfma_f32_16x16x32_bf16 v[72:75], v[4:7], v[44:47], v[72:75]
	v_mfma_f32_16x16x32_bf16 v[76:79], v[12:15], v[44:47], v[76:79]
	v_mfma_f32_16x16x32_bf16 v[80:83], v[4:7], v[52:55], v[80:83]
	v_mfma_f32_16x16x32_bf16 v[84:87], v[12:15], v[52:55], v[84:87]
	v_mfma_f32_16x16x32_bf16 v[88:91], v[4:7], v[60:63], v[88:91]
	v_mfma_f32_16x16x32_bf16 v[92:95], v[12:15], v[60:63], v[92:95]
	s_setprio 0
	s_setprio 1
	v_mfma_f32_16x16x32_bf16 v[96:99], v[16:19], v[32:35], 0
	v_mfma_f32_16x16x32_bf16 v[32:35], v[24:27], v[32:35], 0
	v_mfma_f32_16x16x32_bf16 v[96:99], v[20:23], v[36:39], v[96:99]
	v_mfma_f32_16x16x32_bf16 v[32:35], v[28:31], v[36:39], v[32:35]
	v_mfma_f32_16x16x32_bf16 v[36:39], v[16:19], v[40:43], 0
	v_mfma_f32_16x16x32_bf16 v[40:43], v[24:27], v[40:43], 0
	v_mfma_f32_16x16x32_bf16 v[36:39], v[20:23], v[44:47], v[36:39]
	v_mfma_f32_16x16x32_bf16 v[40:43], v[28:31], v[44:47], v[40:43]
	v_mfma_f32_16x16x32_bf16 v[44:47], v[16:19], v[48:51], 0
	v_mfma_f32_16x16x32_bf16 v[48:51], v[24:27], v[48:51], 0
	v_mfma_f32_16x16x32_bf16 v[44:47], v[20:23], v[52:55], v[44:47]
	v_mfma_f32_16x16x32_bf16 v[48:51], v[28:31], v[52:55], v[48:51]
	v_mfma_f32_16x16x32_bf16 v[52:55], v[16:19], v[56:59], 0
	v_mfma_f32_16x16x32_bf16 v[56:59], v[24:27], v[56:59], 0
	v_mfma_f32_16x16x32_bf16 v[52:55], v[20:23], v[60:63], v[52:55]
	v_mfma_f32_16x16x32_bf16 v[56:59], v[28:31], v[60:63], v[56:59]
	s_setprio 0
	s_barrier
	ds_read_b128 v[60:63], v137 offset:16384
	ds_read_b128 v[100:103], v137 offset:17408
	ds_read_b128 v[104:107], v137 offset:18432
	ds_read_b128 v[108:111], v137 offset:19456
	ds_read_b128 v[112:115], v137 offset:20480
	ds_read_b128 v[116:119], v137 offset:21504
	ds_read_b128 v[120:123], v137 offset:22528
	ds_read_b128 v[124:127], v137 offset:23552
	s_mov_b32 s73, m0
	s_mov_b32 m0, s49
	s_nop 2
	global_load_lds_dwordx4 v130, s[46:47]
	s_mov_b32 m0, s73
	s_nop 0
	s_mov_b32 s73, m0
	s_mov_b32 m0, s50
	s_nop 2
	global_load_lds_dwordx4 v131, s[46:47]
	s_mov_b32 m0, s73
	s_mov_b32 s46, m0
	s_mov_b32 m0, s51
	s_nop 2
	global_load_lds_dwordx4 v130, s[40:41]
	s_mov_b32 m0, s46
	s_nop 0
	s_mov_b32 s46, m0
	s_mov_b32 m0, s52
	s_nop 2
	global_load_lds_dwordx4 v131, s[40:41]
	s_mov_b32 m0, s46
	s_mov_b32 s40, m0
	s_mov_b32 m0, s2
	s_nop 2
	global_load_lds_dwordx4 v132, s[36:37]
	s_mov_b32 m0, s40
	s_nop 0
	s_mov_b32 s40, m0
	s_mov_b32 m0, s53
	s_nop 2
	global_load_lds_dwordx4 v133, s[36:37]
	s_mov_b32 m0, s40
	s_waitcnt vmcnt(8)
	s_waitcnt lgkmcnt(0)
	s_barrier
	s_setprio 1
	v_mfma_f32_16x16x32_bf16 v[140:143], v[0:3], v[60:63], 0
	v_mfma_f32_16x16x32_bf16 v[148:151], v[0:3], v[104:107], 0
	v_mfma_f32_16x16x32_bf16 v[156:159], v[0:3], v[112:115], 0
	v_mfma_f32_16x16x32_bf16 v[0:3], v[0:3], v[120:123], 0
	v_mfma_f32_16x16x32_bf16 v[140:143], v[4:7], v[100:103], v[140:143]
	v_mfma_f32_16x16x32_bf16 v[148:151], v[4:7], v[108:111], v[148:151]
	v_mfma_f32_16x16x32_bf16 v[156:159], v[4:7], v[116:119], v[156:159]
	v_mfma_f32_16x16x32_bf16 v[0:3], v[4:7], v[124:127], v[0:3]
	v_mfma_f32_16x16x32_bf16 v[4:7], v[8:11], v[120:123], 0
	v_mfma_f32_16x16x32_bf16 v[144:147], v[8:11], v[60:63], 0
	v_mfma_f32_16x16x32_bf16 v[152:155], v[8:11], v[104:107], 0
	v_mfma_f32_16x16x32_bf16 v[160:163], v[8:11], v[112:115], 0
	v_mfma_f32_16x16x32_bf16 v[4:7], v[12:15], v[124:127], v[4:7]
	v_mfma_f32_16x16x32_bf16 v[144:147], v[12:15], v[100:103], v[144:147]
	v_mfma_f32_16x16x32_bf16 v[152:155], v[12:15], v[108:111], v[152:155]
	v_mfma_f32_16x16x32_bf16 v[160:163], v[12:15], v[116:119], v[160:163]
	s_setprio 0
	s_setprio 1
	v_mfma_f32_16x16x32_bf16 v[8:11], v[16:19], v[60:63], 0
	v_mfma_f32_16x16x32_bf16 v[12:15], v[24:27], v[60:63], 0
	v_mfma_f32_16x16x32_bf16 v[8:11], v[20:23], v[100:103], v[8:11]
	v_mfma_f32_16x16x32_bf16 v[12:15], v[28:31], v[100:103], v[12:15]
	v_mfma_f32_16x16x32_bf16 v[60:63], v[16:19], v[104:107], 0
	v_mfma_f32_16x16x32_bf16 v[100:103], v[24:27], v[104:107], 0
	v_mfma_f32_16x16x32_bf16 v[104:107], v[16:19], v[112:115], 0
	v_mfma_f32_16x16x32_bf16 v[16:19], v[16:19], v[120:123], 0
	v_mfma_f32_16x16x32_bf16 v[60:63], v[20:23], v[108:111], v[60:63]
	v_mfma_f32_16x16x32_bf16 v[100:103], v[28:31], v[108:111], v[100:103]
	v_mfma_f32_16x16x32_bf16 v[104:107], v[20:23], v[116:119], v[104:107]
	v_mfma_f32_16x16x32_bf16 v[108:111], v[24:27], v[112:115], 0
	v_mfma_f32_16x16x32_bf16 v[16:19], v[20:23], v[124:127], v[16:19]
	v_mfma_f32_16x16x32_bf16 v[20:23], v[24:27], v[120:123], 0
	v_mfma_f32_16x16x32_bf16 v[108:111], v[28:31], v[116:119], v[108:111]
	v_mfma_f32_16x16x32_bf16 v[20:23], v[28:31], v[124:127], v[20:23]
	s_setprio 0
	s_barrier
	ds_read_b128 v[24:27], v138
	ds_read_b128 v[28:31], v138 offset:1024
	ds_read_b128 v[112:115], v138 offset:2048
	ds_read_b128 v[116:119], v138 offset:3072
	ds_read_b128 v[120:123], v139
	ds_read_b128 v[124:127], v139 offset:1024
	ds_read_b128 v[164:167], v139 offset:2048
	ds_read_b128 v[168:171], v139 offset:3072
	ds_read_b128 v[172:175], v137 offset:32768
	ds_read_b128 v[176:179], v137 offset:33792
	ds_read_b128 v[180:183], v137 offset:34816
	ds_read_b128 v[184:187], v137 offset:35840
	ds_read_b128 v[188:191], v137 offset:36864
	ds_read_b128 v[192:195], v137 offset:37888
	ds_read_b128 v[196:199], v137 offset:38912
	ds_read_b128 v[200:203], v137 offset:39936
	s_add_u32 s36, s20, 0x10100
	s_addc_u32 s37, s21, 0
	s_mov_b32 s40, m0
	s_mov_b32 m0, s54
	s_nop 2
	global_load_lds_dwordx4 v132, s[36:37]
	s_mov_b32 m0, s40
	s_nop 0
	s_mov_b32 s40, m0
	s_mov_b32 m0, s55
	s_nop 2
	global_load_lds_dwordx4 v133, s[36:37]
	s_mov_b32 m0, s40
	s_waitcnt vmcnt(8)
	s_waitcnt lgkmcnt(0)
	s_barrier
	s_setprio 1
	v_mfma_f32_16x16x32_bf16 v[64:67], v[24:27], v[172:175], v[64:67]
	v_mfma_f32_16x16x32_bf16 v[68:71], v[112:115], v[172:175], v[68:71]
	v_mfma_f32_16x16x32_bf16 v[72:75], v[24:27], v[180:183], v[72:75]
	v_mfma_f32_16x16x32_bf16 v[76:79], v[112:115], v[180:183], v[76:79]
	v_mfma_f32_16x16x32_bf16 v[80:83], v[24:27], v[188:191], v[80:83]
	v_mfma_f32_16x16x32_bf16 v[84:87], v[112:115], v[188:191], v[84:87]
	v_mfma_f32_16x16x32_bf16 v[88:91], v[24:27], v[196:199], v[88:91]
	v_mfma_f32_16x16x32_bf16 v[92:95], v[112:115], v[196:199], v[92:95]
	v_mfma_f32_16x16x32_bf16 v[64:67], v[28:31], v[176:179], v[64:67]
	v_mfma_f32_16x16x32_bf16 v[68:71], v[116:119], v[176:179], v[68:71]
	v_mfma_f32_16x16x32_bf16 v[72:75], v[28:31], v[184:187], v[72:75]
	v_mfma_f32_16x16x32_bf16 v[76:79], v[116:119], v[184:187], v[76:79]
	v_mfma_f32_16x16x32_bf16 v[80:83], v[28:31], v[192:195], v[80:83]
	v_mfma_f32_16x16x32_bf16 v[84:87], v[116:119], v[192:195], v[84:87]
	v_mfma_f32_16x16x32_bf16 v[88:91], v[28:31], v[200:203], v[88:91]
	v_mfma_f32_16x16x32_bf16 v[92:95], v[116:119], v[200:203], v[92:95]
	s_setprio 0
	s_setprio 1
	v_mfma_f32_16x16x32_bf16 v[96:99], v[120:123], v[172:175], v[96:99]
	v_mfma_f32_16x16x32_bf16 v[32:35], v[164:167], v[172:175], v[32:35]
	v_mfma_f32_16x16x32_bf16 v[36:39], v[120:123], v[180:183], v[36:39]
	v_mfma_f32_16x16x32_bf16 v[40:43], v[164:167], v[180:183], v[40:43]
	v_mfma_f32_16x16x32_bf16 v[44:47], v[120:123], v[188:191], v[44:47]
	v_mfma_f32_16x16x32_bf16 v[48:51], v[164:167], v[188:191], v[48:51]
	v_mfma_f32_16x16x32_bf16 v[52:55], v[120:123], v[196:199], v[52:55]
	v_mfma_f32_16x16x32_bf16 v[56:59], v[164:167], v[196:199], v[56:59]
	v_mfma_f32_16x16x32_bf16 v[96:99], v[124:127], v[176:179], v[96:99]
	v_mfma_f32_16x16x32_bf16 v[32:35], v[168:171], v[176:179], v[32:35]
	v_mfma_f32_16x16x32_bf16 v[36:39], v[124:127], v[184:187], v[36:39]
	v_mfma_f32_16x16x32_bf16 v[40:43], v[168:171], v[184:187], v[40:43]
	v_mfma_f32_16x16x32_bf16 v[44:47], v[124:127], v[192:195], v[44:47]
	v_mfma_f32_16x16x32_bf16 v[48:51], v[168:171], v[192:195], v[48:51]
	v_mfma_f32_16x16x32_bf16 v[52:55], v[124:127], v[200:203], v[52:55]
	v_mfma_f32_16x16x32_bf16 v[56:59], v[168:171], v[200:203], v[56:59]
	s_setprio 0
	s_barrier
	ds_read_b128 v[172:175], v137 offset:49152
	ds_read_b128 v[176:179], v137 offset:50176
	ds_read_b128 v[180:183], v137 offset:51200
	ds_read_b128 v[184:187], v137 offset:52224
	ds_read_b128 v[188:191], v137 offset:53248
	ds_read_b128 v[192:195], v137 offset:54272
	ds_read_b128 v[196:199], v137 offset:55296
	ds_read_b128 v[200:203], v137 offset:56320
	s_mov_b32 s36, m0
	s_mov_b32 m0, s56
	s_nop 2
	global_load_lds_dwordx4 v130, s[34:35]
	s_mov_b32 m0, s36
	s_add_u32 s22, s22, 0x180
	s_mov_b32 s36, m0
	s_mov_b32 m0, s57
	s_nop 2
	global_load_lds_dwordx4 v131, s[34:35]
	s_mov_b32 m0, s36
	s_addc_u32 s23, s23, 0
	s_mov_b32 s34, m0
	s_mov_b32 m0, s60
	s_nop 2
	global_load_lds_dwordx4 v130, s[22:23]
	s_mov_b32 m0, s34
	s_nop 0
	s_mov_b32 s34, m0
	s_mov_b32 m0, s61
	s_nop 2
	global_load_lds_dwordx4 v131, s[22:23]
	s_mov_b32 m0, s34
	s_mov_b32 s22, m0
	s_mov_b32 m0, s58
	s_nop 2
	global_load_lds_dwordx4 v132, s[30:31]
	s_mov_b32 m0, s22
	s_nop 0
	s_mov_b32 s22, m0
	s_mov_b32 m0, s59
	s_nop 2
	global_load_lds_dwordx4 v133, s[30:31]
	s_mov_b32 m0, s22
	s_waitcnt vmcnt(8)
	s_waitcnt lgkmcnt(0)
	s_barrier
	s_setprio 1
	v_mfma_f32_16x16x32_bf16 v[0:3], v[24:27], v[196:199], v[0:3]
	v_mfma_f32_16x16x32_bf16 v[4:7], v[112:115], v[196:199], v[4:7]
	v_mfma_f32_16x16x32_bf16 v[140:143], v[24:27], v[172:175], v[140:143]
	v_mfma_f32_16x16x32_bf16 v[144:147], v[112:115], v[172:175], v[144:147]
	v_mfma_f32_16x16x32_bf16 v[148:151], v[24:27], v[180:183], v[148:151]
	v_mfma_f32_16x16x32_bf16 v[152:155], v[112:115], v[180:183], v[152:155]
	v_mfma_f32_16x16x32_bf16 v[156:159], v[24:27], v[188:191], v[156:159]
	v_mfma_f32_16x16x32_bf16 v[160:163], v[112:115], v[188:191], v[160:163]
	v_mfma_f32_16x16x32_bf16 v[0:3], v[28:31], v[200:203], v[0:3]
	v_mfma_f32_16x16x32_bf16 v[4:7], v[116:119], v[200:203], v[4:7]
	v_mfma_f32_16x16x32_bf16 v[140:143], v[28:31], v[176:179], v[140:143]
	v_mfma_f32_16x16x32_bf16 v[144:147], v[116:119], v[176:179], v[144:147]
	v_mfma_f32_16x16x32_bf16 v[148:151], v[28:31], v[184:187], v[148:151]
	v_mfma_f32_16x16x32_bf16 v[152:155], v[116:119], v[184:187], v[152:155]
	v_mfma_f32_16x16x32_bf16 v[156:159], v[28:31], v[192:195], v[156:159]
	v_mfma_f32_16x16x32_bf16 v[160:163], v[116:119], v[192:195], v[160:163]
	s_setprio 0
	s_setprio 1
	v_mfma_f32_16x16x32_bf16 v[8:11], v[120:123], v[172:175], v[8:11]
	v_mfma_f32_16x16x32_bf16 v[12:15], v[164:167], v[172:175], v[12:15]
	v_mfma_f32_16x16x32_bf16 v[24:27], v[120:123], v[180:183], v[60:63]
	v_mfma_f32_16x16x32_bf16 v[28:31], v[164:167], v[180:183], v[100:103]
	v_mfma_f32_16x16x32_bf16 v[60:63], v[120:123], v[188:191], v[104:107]
	v_mfma_f32_16x16x32_bf16 v[100:103], v[164:167], v[188:191], v[108:111]
	v_mfma_f32_16x16x32_bf16 v[16:19], v[120:123], v[196:199], v[16:19]
	v_mfma_f32_16x16x32_bf16 v[20:23], v[164:167], v[196:199], v[20:23]
	v_mfma_f32_16x16x32_bf16 v[8:11], v[124:127], v[176:179], v[8:11]
	v_mfma_f32_16x16x32_bf16 v[12:15], v[168:171], v[176:179], v[12:15]
	v_mfma_f32_16x16x32_bf16 v[24:27], v[124:127], v[184:187], v[24:27]
	v_mfma_f32_16x16x32_bf16 v[28:31], v[168:171], v[184:187], v[28:31]
	v_mfma_f32_16x16x32_bf16 v[60:63], v[124:127], v[192:195], v[60:63]
	v_mfma_f32_16x16x32_bf16 v[100:103], v[168:171], v[192:195], v[100:103]
	v_mfma_f32_16x16x32_bf16 v[16:19], v[124:127], v[200:203], v[16:19]
	v_mfma_f32_16x16x32_bf16 v[20:23], v[168:171], v[200:203], v[20:23]
	s_setprio 0
	s_barrier
	ds_read_b128 v[104:107], v134
	ds_read_b128 v[108:111], v134 offset:1024
	ds_read_b128 v[112:115], v134 offset:2048
	ds_read_b128 v[116:119], v134 offset:3072
	ds_read_b128 v[120:123], v136
	ds_read_b128 v[124:127], v136 offset:1024
	ds_read_b128 v[164:167], v136 offset:2048
	ds_read_b128 v[168:171], v136 offset:3072
	s_add_u32 s30, s28, 0x80
	s_addc_u32 s31, s29, 0
	s_add_u32 s22, s26, 0x80
	s_addc_u32 s23, s27, 0
	ds_read_b128 v[172:175], v137
	ds_read_b128 v[176:179], v137 offset:1024
	ds_read_b128 v[180:183], v137 offset:2048
	ds_read_b128 v[184:187], v137 offset:3072
	ds_read_b128 v[188:191], v137 offset:4096
	ds_read_b128 v[192:195], v137 offset:5120
	ds_read_b128 v[196:199], v137 offset:6144
	ds_read_b128 v[200:203], v137 offset:7168
	s_add_u32 s20, s20, 0x10180
	s_addc_u32 s21, s21, 0
	s_mov_b32 s34, m0
	s_mov_b32 m0, s62
	s_nop 2
	global_load_lds_dwordx4 v132, s[20:21]
	s_mov_b32 m0, s34
	s_nop 0
	s_mov_b32 s34, m0
	s_mov_b32 m0, s63
	s_nop 2
	global_load_lds_dwordx4 v133, s[20:21]
	s_mov_b32 m0, s34
	s_waitcnt vmcnt(8)
	s_waitcnt lgkmcnt(0)
	s_barrier
	s_setprio 1
	v_mfma_f32_16x16x32_bf16 v[88:91], v[104:107], v[196:199], v[88:91]
	v_mfma_f32_16x16x32_bf16 v[64:67], v[104:107], v[172:175], v[64:67]
	v_mfma_f32_16x16x32_bf16 v[68:71], v[112:115], v[172:175], v[68:71]
	v_mfma_f32_16x16x32_bf16 v[72:75], v[104:107], v[180:183], v[72:75]
	v_mfma_f32_16x16x32_bf16 v[76:79], v[112:115], v[180:183], v[76:79]
	v_mfma_f32_16x16x32_bf16 v[80:83], v[104:107], v[188:191], v[80:83]
	v_mfma_f32_16x16x32_bf16 v[84:87], v[112:115], v[188:191], v[84:87]
	v_mfma_f32_16x16x32_bf16 v[204:207], v[108:111], v[200:203], v[88:91]
	v_mfma_f32_16x16x32_bf16 v[88:91], v[112:115], v[196:199], v[92:95]
	v_mfma_f32_16x16x32_bf16 v[64:67], v[108:111], v[176:179], v[64:67]
	v_mfma_f32_16x16x32_bf16 v[68:71], v[116:119], v[176:179], v[68:71]
	v_mfma_f32_16x16x32_bf16 v[72:75], v[108:111], v[184:187], v[72:75]
	v_mfma_f32_16x16x32_bf16 v[76:79], v[116:119], v[184:187], v[76:79]
	v_mfma_f32_16x16x32_bf16 v[80:83], v[108:111], v[192:195], v[80:83]
	v_mfma_f32_16x16x32_bf16 v[84:87], v[116:119], v[192:195], v[84:87]
	v_mfma_f32_16x16x32_bf16 v[92:95], v[116:119], v[200:203], v[88:91]
	s_setprio 0
	s_setprio 1
	v_mfma_f32_16x16x32_bf16 v[48:51], v[164:167], v[188:191], v[48:51]
	v_mfma_f32_16x16x32_bf16 v[88:91], v[120:123], v[172:175], v[96:99]
	v_mfma_f32_16x16x32_bf16 v[32:35], v[164:167], v[172:175], v[32:35]
	v_mfma_f32_16x16x32_bf16 v[36:39], v[120:123], v[180:183], v[36:39]
	v_mfma_f32_16x16x32_bf16 v[40:43], v[164:167], v[180:183], v[40:43]
	v_mfma_f32_16x16x32_bf16 v[44:47], v[120:123], v[188:191], v[44:47]
	v_mfma_f32_16x16x32_bf16 v[172:175], v[168:171], v[192:195], v[48:51]
	v_mfma_f32_16x16x32_bf16 v[48:51], v[120:123], v[196:199], v[52:55]
	v_mfma_f32_16x16x32_bf16 v[32:35], v[168:171], v[176:179], v[32:35]
	v_mfma_f32_16x16x32_bf16 v[36:39], v[124:127], v[184:187], v[36:39]
	v_mfma_f32_16x16x32_bf16 v[40:43], v[168:171], v[184:187], v[40:43]
	v_mfma_f32_16x16x32_bf16 v[44:47], v[124:127], v[192:195], v[44:47]
	v_mfma_f32_16x16x32_bf16 v[52:55], v[124:127], v[200:203], v[48:51]
	v_mfma_f32_16x16x32_bf16 v[48:51], v[164:167], v[196:199], v[56:59]
	v_mfma_f32_16x16x32_bf16 v[208:211], v[124:127], v[176:179], v[88:91]
	v_mfma_f32_16x16x32_bf16 v[176:179], v[168:171], v[200:203], v[48:51]
	s_setprio 0
	s_barrier
	s_nop 3
	ds_read_b128 v[48:51], v137 offset:16384
	ds_read_b128 v[56:59], v137 offset:17408
	ds_read_b128 v[88:91], v137 offset:18432
	ds_read_b128 v[96:99], v137 offset:19456
	ds_read_b128 v[180:183], v137 offset:20480
	ds_read_b128 v[184:187], v137 offset:21504
	ds_read_b128 v[188:191], v137 offset:22528
	ds_read_b128 v[192:195], v137 offset:23552
	s_mov_b32 s20, m0
	s_mov_b32 m0, s49
	s_nop 2
	global_load_lds_dwordx4 v130, s[28:29]
	s_mov_b32 m0, s20
	s_nop 0
	s_mov_b32 s20, m0
	s_mov_b32 m0, s50
	s_nop 2
	global_load_lds_dwordx4 v131, s[28:29]
	s_mov_b32 m0, s20
	s_nop 0
	s_mov_b32 s20, m0
	s_mov_b32 m0, s51
	s_nop 2
	global_load_lds_dwordx4 v130, s[24:25]
	s_mov_b32 m0, s20
	s_nop 0
	s_mov_b32 s20, m0
	s_mov_b32 m0, s52
	s_nop 2
	global_load_lds_dwordx4 v131, s[24:25]
	s_mov_b32 m0, s20
	s_nop 0
	s_mov_b32 s20, m0
	s_mov_b32 m0, s2
	s_nop 2
	global_load_lds_dwordx4 v132, s[26:27]
	s_mov_b32 m0, s20
	s_nop 0
	s_mov_b32 s20, m0
	s_mov_b32 m0, s53
	s_nop 2
	global_load_lds_dwordx4 v133, s[26:27]
	s_mov_b32 m0, s20
	s_waitcnt vmcnt(8)
	s_waitcnt lgkmcnt(0)
	s_barrier
	s_setprio 1
	v_mfma_f32_16x16x32_bf16 v[0:3], v[104:107], v[188:191], v[0:3]
	v_mfma_f32_16x16x32_bf16 v[4:7], v[112:115], v[188:191], v[4:7]
	v_mfma_f32_16x16x32_bf16 v[140:143], v[104:107], v[48:51], v[140:143]
	v_mfma_f32_16x16x32_bf16 v[144:147], v[112:115], v[48:51], v[144:147]
	v_mfma_f32_16x16x32_bf16 v[148:151], v[104:107], v[88:91], v[148:151]
	v_mfma_f32_16x16x32_bf16 v[152:155], v[112:115], v[88:91], v[152:155]
	v_mfma_f32_16x16x32_bf16 v[156:159], v[104:107], v[180:183], v[156:159]
	v_mfma_f32_16x16x32_bf16 v[160:163], v[112:115], v[180:183], v[160:163]
	v_mfma_f32_16x16x32_bf16 v[0:3], v[108:111], v[192:195], v[0:3]
	v_mfma_f32_16x16x32_bf16 v[4:7], v[116:119], v[192:195], v[4:7]
	v_mfma_f32_16x16x32_bf16 v[140:143], v[108:111], v[56:59], v[140:143]
	v_mfma_f32_16x16x32_bf16 v[144:147], v[116:119], v[56:59], v[144:147]
	v_mfma_f32_16x16x32_bf16 v[148:151], v[108:111], v[96:99], v[148:151]
	v_mfma_f32_16x16x32_bf16 v[152:155], v[116:119], v[96:99], v[152:155]
	v_mfma_f32_16x16x32_bf16 v[156:159], v[108:111], v[184:187], v[156:159]
	v_mfma_f32_16x16x32_bf16 v[160:163], v[116:119], v[184:187], v[160:163]
	s_setprio 0
	s_setprio 1
	v_mfma_f32_16x16x32_bf16 v[12:15], v[164:167], v[48:51], v[12:15]
	v_mfma_f32_16x16x32_bf16 v[196:199], v[168:171], v[56:59], v[12:15]
	v_mfma_f32_16x16x32_bf16 v[12:15], v[120:123], v[88:91], v[24:27]
	v_mfma_f32_16x16x32_bf16 v[24:27], v[124:127], v[96:99], v[12:15]
	v_mfma_f32_16x16x32_bf16 v[12:15], v[164:167], v[88:91], v[28:31]
	v_mfma_f32_16x16x32_bf16 v[200:203], v[168:171], v[96:99], v[12:15]
	v_mfma_f32_16x16x32_bf16 v[12:15], v[120:123], v[180:183], v[60:63]
	v_mfma_f32_16x16x32_bf16 v[212:215], v[124:127], v[184:187], v[12:15]
	v_mfma_f32_16x16x32_bf16 v[12:15], v[164:167], v[180:183], v[100:103]
	v_mfma_f32_16x16x32_bf16 v[8:11], v[120:123], v[48:51], v[8:11]
	v_mfma_f32_16x16x32_bf16 v[180:183], v[168:171], v[184:187], v[12:15]
	v_mfma_f32_16x16x32_bf16 v[12:15], v[120:123], v[188:191], v[16:19]
	v_mfma_f32_16x16x32_bf16 v[8:11], v[124:127], v[56:59], v[8:11]
	v_mfma_f32_16x16x32_bf16 v[184:187], v[124:127], v[192:195], v[12:15]
	v_mfma_f32_16x16x32_bf16 v[12:15], v[164:167], v[188:191], v[20:23]
	v_mfma_f32_16x16x32_bf16 v[164:167], v[168:171], v[192:195], v[12:15]
	s_setprio 0
	s_barrier
	s_nop 4
	ds_read_b128 v[12:15], v138
	ds_read_b128 v[16:19], v138 offset:1024
	ds_read_b128 v[168:171], v138 offset:2048
	ds_read_b128 v[188:191], v138 offset:3072
	ds_read_b128 v[192:195], v139
	ds_read_b128 v[216:219], v139 offset:1024
	ds_read_b128 v[220:223], v139 offset:2048
	ds_read_b128 v[224:227], v139 offset:3072
	ds_read_b128 v[20:23], v137 offset:32768
	ds_read_b128 v[28:31], v137 offset:33792
	ds_read_b128 v[60:63], v137 offset:34816
	ds_read_b128 v[100:103], v137 offset:35840
	ds_read_b128 v[228:231], v137 offset:36864
	ds_read_b128 v[232:235], v137 offset:37888
	ds_read_b128 v[236:239], v137 offset:38912
	ds_read_b128 v[240:243], v137 offset:39936
	s_add_u32 s20, s26, 0x10000
	s_addc_u32 s21, s27, 0
	s_mov_b32 s26, m0
	s_mov_b32 m0, s54
	s_nop 2
	global_load_lds_dwordx4 v132, s[20:21]
	s_mov_b32 m0, s26
	s_nop 0
	s_mov_b32 s26, m0
	s_mov_b32 m0, s55
	s_nop 2
	global_load_lds_dwordx4 v133, s[20:21]
	s_mov_b32 m0, s26
	s_waitcnt vmcnt(8)
	s_waitcnt lgkmcnt(0)
	s_barrier
	s_setprio 1
	v_mfma_f32_16x16x32_bf16 v[48:51], v[12:15], v[20:23], v[64:67]
	v_mfma_f32_16x16x32_bf16 v[120:123], v[16:19], v[28:31], v[48:51]
	v_mfma_f32_16x16x32_bf16 v[48:51], v[168:171], v[20:23], v[68:71]
	v_mfma_f32_16x16x32_bf16 v[112:115], v[188:191], v[28:31], v[48:51]
	v_mfma_f32_16x16x32_bf16 v[48:51], v[12:15], v[60:63], v[72:75]
	v_mfma_f32_16x16x32_bf16 v[104:107], v[16:19], v[100:103], v[48:51]
	v_mfma_f32_16x16x32_bf16 v[48:51], v[168:171], v[60:63], v[76:79]
	v_mfma_f32_16x16x32_bf16 v[96:99], v[188:191], v[100:103], v[48:51]
	v_mfma_f32_16x16x32_bf16 v[48:51], v[12:15], v[228:231], v[80:83]
	v_mfma_f32_16x16x32_bf16 v[88:91], v[16:19], v[232:235], v[48:51]
	v_mfma_f32_16x16x32_bf16 v[48:51], v[168:171], v[228:231], v[84:87]
	v_mfma_f32_16x16x32_bf16 v[80:83], v[188:191], v[232:235], v[48:51]
	v_mfma_f32_16x16x32_bf16 v[48:51], v[12:15], v[236:239], v[204:207]
	v_mfma_f32_16x16x32_bf16 v[56:59], v[16:19], v[240:243], v[48:51]
	v_mfma_f32_16x16x32_bf16 v[48:51], v[168:171], v[236:239], v[92:95]
	v_mfma_f32_16x16x32_bf16 v[48:51], v[188:191], v[240:243], v[48:51]
	s_setprio 0
	s_setprio 1
	v_mfma_f32_16x16x32_bf16 v[64:67], v[192:195], v[20:23], v[208:211]
	v_mfma_f32_16x16x32_bf16 v[20:23], v[220:223], v[20:23], v[32:35]
	v_mfma_f32_16x16x32_bf16 v[116:119], v[224:227], v[28:31], v[20:23]
	v_mfma_f32_16x16x32_bf16 v[20:23], v[192:195], v[60:63], v[36:39]
	v_mfma_f32_16x16x32_bf16 v[108:111], v[216:219], v[100:103], v[20:23]
	v_mfma_f32_16x16x32_bf16 v[20:23], v[220:223], v[60:63], v[40:43]
	v_mfma_f32_16x16x32_bf16 v[100:103], v[224:227], v[100:103], v[20:23]
	v_mfma_f32_16x16x32_bf16 v[20:23], v[192:195], v[228:231], v[44:47]
	v_mfma_f32_16x16x32_bf16 v[92:95], v[216:219], v[232:235], v[20:23]
	v_mfma_f32_16x16x32_bf16 v[20:23], v[220:223], v[228:231], v[172:175]
	v_mfma_f32_16x16x32_bf16 v[84:87], v[224:227], v[232:235], v[20:23]
	v_mfma_f32_16x16x32_bf16 v[20:23], v[192:195], v[236:239], v[52:55]
	v_mfma_f32_16x16x32_bf16 v[60:63], v[216:219], v[240:243], v[20:23]
	v_mfma_f32_16x16x32_bf16 v[20:23], v[220:223], v[236:239], v[176:179]
	v_mfma_f32_16x16x32_bf16 v[124:127], v[216:219], v[28:31], v[64:67]
	v_mfma_f32_16x16x32_bf16 v[52:55], v[224:227], v[240:243], v[20:23]
	s_setprio 0
	s_barrier
	ds_read_b128 v[32:35], v137 offset:49152
	ds_read_b128 v[40:43], v137 offset:50176
	ds_read_b128 v[172:175], v137 offset:51200
	ds_read_b128 v[176:179], v137 offset:52224
	ds_read_b128 v[204:207], v137 offset:53248
	ds_read_b128 v[208:211], v137 offset:54272
	ds_read_b128 v[228:231], v137 offset:55296
	ds_read_b128 v[232:235], v137 offset:56320
	s_mov_b32 s20, m0
	s_mov_b32 m0, s56
	s_nop 2
	global_load_lds_dwordx4 v130, s[30:31]
	s_mov_b32 m0, s20
	s_nop 0
	s_mov_b32 s20, m0
	s_mov_b32 m0, s57
	s_nop 2
	global_load_lds_dwordx4 v131, s[30:31]
	s_mov_b32 m0, s20
	s_add_u32 s20, s24, 0x80
	s_addc_u32 s21, s25, 0
	s_mov_b32 s24, m0
	s_mov_b32 m0, s60
	s_nop 2
	global_load_lds_dwordx4 v130, s[20:21]
	s_mov_b32 m0, s24
	s_nop 0
	s_mov_b32 s24, m0
	s_mov_b32 m0, s61
	s_nop 2
	global_load_lds_dwordx4 v131, s[20:21]
	s_mov_b32 m0, s24
	s_mov_b32 s20, m0
	s_mov_b32 m0, s58
	s_nop 2
	global_load_lds_dwordx4 v132, s[22:23]
	s_mov_b32 m0, s20
	s_nop 0
	s_mov_b32 s20, m0
	s_mov_b32 m0, s59
	s_nop 2
	global_load_lds_dwordx4 v133, s[22:23]
	s_mov_b32 m0, s20
	s_waitcnt vmcnt(8)
	s_waitcnt lgkmcnt(0)
	s_barrier
	s_setprio 1
	v_mfma_f32_16x16x32_bf16 v[20:23], v[12:15], v[32:35], v[140:143]
	v_mfma_f32_16x16x32_bf16 v[76:79], v[16:19], v[40:43], v[20:23]
	v_mfma_f32_16x16x32_bf16 v[20:23], v[168:171], v[32:35], v[144:147]
	v_mfma_f32_16x16x32_bf16 v[68:71], v[188:191], v[40:43], v[20:23]
	v_mfma_f32_16x16x32_bf16 v[20:23], v[12:15], v[172:175], v[148:151]
	v_mfma_f32_16x16x32_bf16 v[44:47], v[16:19], v[176:179], v[20:23]
	v_mfma_f32_16x16x32_bf16 v[20:23], v[168:171], v[172:175], v[152:155]
	v_mfma_f32_16x16x32_bf16 v[36:39], v[188:191], v[176:179], v[20:23]
	v_mfma_f32_16x16x32_bf16 v[20:23], v[12:15], v[204:207], v[156:159]
	v_mfma_f32_16x16x32_bf16 v[0:3], v[12:15], v[228:231], v[0:3]
	v_mfma_f32_16x16x32_bf16 v[28:31], v[16:19], v[208:211], v[20:23]
	v_mfma_f32_16x16x32_bf16 v[20:23], v[168:171], v[204:207], v[160:163]
	v_mfma_f32_16x16x32_bf16 v[12:15], v[16:19], v[232:235], v[0:3]
	v_mfma_f32_16x16x32_bf16 v[0:3], v[168:171], v[228:231], v[4:7]
	v_mfma_f32_16x16x32_bf16 v[20:23], v[188:191], v[208:211], v[20:23]
	v_mfma_f32_16x16x32_bf16 v[4:7], v[188:191], v[232:235], v[0:3]
	s_setprio 0
	s_setprio 1
	v_mfma_f32_16x16x32_bf16 v[0:3], v[192:195], v[32:35], v[8:11]
	v_mfma_f32_16x16x32_bf16 v[72:75], v[216:219], v[40:43], v[0:3]
	v_mfma_f32_16x16x32_bf16 v[0:3], v[220:223], v[32:35], v[196:199]
	v_mfma_f32_16x16x32_bf16 v[64:67], v[224:227], v[40:43], v[0:3]
	v_mfma_f32_16x16x32_bf16 v[0:3], v[192:195], v[172:175], v[24:27]
	v_mfma_f32_16x16x32_bf16 v[40:43], v[216:219], v[176:179], v[0:3]
	v_mfma_f32_16x16x32_bf16 v[0:3], v[220:223], v[172:175], v[200:203]
	v_mfma_f32_16x16x32_bf16 v[32:35], v[224:227], v[176:179], v[0:3]
	v_mfma_f32_16x16x32_bf16 v[0:3], v[192:195], v[204:207], v[212:215]
	v_mfma_f32_16x16x32_bf16 v[24:27], v[216:219], v[208:211], v[0:3]
	v_mfma_f32_16x16x32_bf16 v[0:3], v[220:223], v[204:207], v[180:183]
	v_mfma_f32_16x16x32_bf16 v[16:19], v[224:227], v[208:211], v[0:3]
	v_mfma_f32_16x16x32_bf16 v[0:3], v[192:195], v[228:231], v[184:187]
	v_mfma_f32_16x16x32_bf16 v[8:11], v[216:219], v[232:235], v[0:3]
	v_mfma_f32_16x16x32_bf16 v[0:3], v[220:223], v[228:231], v[164:167]
	v_mfma_f32_16x16x32_bf16 v[0:3], v[224:227], v[232:235], v[0:3]
	s_setprio 0
	s_barrier
	s_andn2_b64 vcc, exec, s[10:11]
	s_cbranch_vccnz .LBB0_1188
	s_barrier

.LBB0_1200:
	v_and_b32_e32 v5, 15, v4
	v_or_b32_e32 v6, s0, v5
	s_add_u32 s14, s20, 0x80
	v_lshlrev_b32_e32 v8, 6, v6
	v_and_b32_e32 v9, 48, v4
	s_movk_i32 s9, 0x3c0
	s_addc_u32 s15, s21, 0
	s_add_i32 s26, 0, 0x18000
	v_and_or_b32 v8, v8, s9, v9
	s_waitcnt vmcnt(2)
	s_barrier
	s_add_i32 s9, s3, s26
	s_mov_b32 s11, m0
	s_mov_b32 m0, s9
	s_nop 2
	global_load_lds_dwordx4 v0, s[14:15]
	s_mov_b32 m0, s11
	s_add_i32 s11, s2, 0x1a000
	s_mov_b32 s16, m0
	s_mov_b32 m0, s11
	s_nop 2
	global_load_lds_dwordx4 v1, s[14:15]
	s_mov_b32 m0, s16
	v_ashrrev_i32_e32 v7, 6, v4
	s_add_u32 s16, s12, 0x80
	v_lshl_add_u32 v10, v7, 10, s33
	s_addc_u32 s17, s13, 0
	s_add_i32 s33, s2, 0x8000
	s_mov_b32 s24, m0
	s_mov_b32 m0, s33
	s_nop 2
	global_load_lds_dwordx4 v2, s[16:17]
	s_mov_b32 m0, s24
	v_add_lshl_u32 v7, v7, s38, 10
	s_add_i32 s38, s2, 0xa000
	s_mov_b32 s24, m0
	s_mov_b32 m0, s38
	s_nop 2
	global_load_lds_dwordx4 v3, s[16:17]
	s_mov_b32 m0, s24
	s_add_u32 s24, s20, 0x10080
	s_addc_u32 s25, s21, 0
	s_add_i32 s27, 0, 0x1c000
	s_add_i32 s3, s3, s27
	s_add_i32 s39, s2, 0x1e000
	s_add_i32 s53, s2, 0xc000
	s_add_i32 s54, s2, 0xe000
	s_add_u32 s40, s12, 0x100
	s_addc_u32 s41, s13, 0
	v_lshlrev_b32_e32 v4, 2, v4
	s_add_u32 s50, s20, 0x100
	v_lshl_or_b32 v5, v5, 6, v9
	v_and_b32_e32 v4, 32, v4
	s_addc_u32 s51, s21, 0
	v_lshlrev_b32_e32 v6, 2, v6
	v_bitop3_b32 v5, v5, v7, v4 bitop3:0xde
	s_add_u32 s46, s20, 0x10100
	v_and_b32_e32 v6, 32, v6
	s_mov_b32 s28, m0
	s_mov_b32 m0, s3
	s_nop 2
	global_load_lds_dwordx4 v0, s[24:25]
	s_mov_b32 m0, s28
	v_add_u32_e32 v4, 0, v5
	s_addc_u32 s47, s21, 0
	v_bitop3_b32 v6, v8, v10, v6 bitop3:0xde
	s_mov_b32 s28, m0
	s_mov_b32 m0, s39
	s_nop 2
	global_load_lds_dwordx4 v1, s[24:25]
	s_mov_b32 m0, s28
	v_add_u32_e32 v198, 0x10000, v4
	s_add_u32 s30, s20, 0x180
	s_waitcnt vmcnt(6)
	s_barrier
	v_add_u32_e32 v199, 0x14000, v4
	v_add_u32_e32 v4, 0, v6
	s_addc_u32 s31, s21, 0
	ds_read_b128 v[6:9], v198
	ds_read_b128 v[10:13], v198 offset:1024
	ds_read_b128 v[14:17], v198 offset:2048
	ds_read_b128 v[18:21], v198 offset:3072
	ds_read_b128 v[22:25], v199
	ds_read_b128 v[26:29], v199 offset:1024
	ds_read_b128 v[30:33], v199 offset:2048
	ds_read_b128 v[34:37], v199 offset:3072
	s_add_u32 s28, s12, 0x180
	s_addc_u32 s29, s13, 0
	s_add_u32 s56, s12, 0x10080
	s_addc_u32 s57, s13, 0
	s_add_u32 s36, s12, 0x10100
	s_addc_u32 s37, s13, 0
	s_add_u32 s34, s20, 0x10180
	s_addc_u32 s35, s21, 0
	v_add_u32_e32 v222, s26, v5
	s_add_u32 s26, s12, 0x10180
	v_add_u32_e32 v5, s27, v5
	s_addc_u32 s27, s13, 0
	v_readlane_b32 s55, v255, 0
	s_cmpk_gt_u32 s55, 0xff
	ds_read_b128 v[38:41], v4
	s_waitcnt vmcnt(4)
	ds_read_b128 v[42:45], v4 offset:1024
	ds_read_b128 v[46:49], v4 offset:2048
	ds_read_b128 v[50:53], v4 offset:3072
	ds_read_b128 v[54:57], v4 offset:4096
	ds_read_b128 v[58:61], v4 offset:5120
	ds_read_b128 v[62:65], v4 offset:6144
	ds_read_b128 v[66:69], v4 offset:7168
	s_mov_b32 s55, m0
	s_mov_b32 m0, s53
	s_nop 2
	global_load_lds_dwordx4 v2, s[56:57]
	s_mov_b32 m0, s55
	s_nop 0
	s_mov_b32 s55, m0
	s_mov_b32 m0, s54
	s_nop 2
	global_load_lds_dwordx4 v3, s[56:57]
	s_mov_b32 m0, s55
	s_waitcnt vmcnt(8)
	s_waitcnt lgkmcnt(0)
	s_barrier
	s_setprio 1
	v_mfma_f32_16x16x32_bf16 v[70:73], v[6:9], v[38:41], 0
	v_mfma_f32_16x16x32_bf16 v[74:77], v[14:17], v[38:41], 0
	v_mfma_f32_16x16x32_bf16 v[78:81], v[6:9], v[46:49], 0
	v_mfma_f32_16x16x32_bf16 v[82:85], v[14:17], v[46:49], 0
	v_mfma_f32_16x16x32_bf16 v[86:89], v[6:9], v[54:57], 0
	v_mfma_f32_16x16x32_bf16 v[90:93], v[14:17], v[54:57], 0
	v_mfma_f32_16x16x32_bf16 v[94:97], v[6:9], v[62:65], 0
	v_mfma_f32_16x16x32_bf16 v[98:101], v[14:17], v[62:65], 0
	v_mfma_f32_16x16x32_bf16 v[70:73], v[10:13], v[42:45], v[70:73]
	v_mfma_f32_16x16x32_bf16 v[74:77], v[18:21], v[42:45], v[74:77]
	v_mfma_f32_16x16x32_bf16 v[78:81], v[10:13], v[50:53], v[78:81]
	v_mfma_f32_16x16x32_bf16 v[82:85], v[18:21], v[50:53], v[82:85]
	v_mfma_f32_16x16x32_bf16 v[86:89], v[10:13], v[58:61], v[86:89]
	v_mfma_f32_16x16x32_bf16 v[90:93], v[18:21], v[58:61], v[90:93]
	v_mfma_f32_16x16x32_bf16 v[94:97], v[10:13], v[66:69], v[94:97]
	v_mfma_f32_16x16x32_bf16 v[98:101], v[18:21], v[66:69], v[98:101]
	s_setprio 0
	s_setprio 1
	v_mfma_f32_16x16x32_bf16 v[102:105], v[22:25], v[38:41], 0
	v_mfma_f32_16x16x32_bf16 v[38:41], v[30:33], v[38:41], 0
	v_mfma_f32_16x16x32_bf16 v[102:105], v[26:29], v[42:45], v[102:105]
	v_mfma_f32_16x16x32_bf16 v[38:41], v[34:37], v[42:45], v[38:41]
	v_mfma_f32_16x16x32_bf16 v[42:45], v[22:25], v[46:49], 0
	v_mfma_f32_16x16x32_bf16 v[46:49], v[30:33], v[46:49], 0
	v_mfma_f32_16x16x32_bf16 v[42:45], v[26:29], v[50:53], v[42:45]
	v_mfma_f32_16x16x32_bf16 v[46:49], v[34:37], v[50:53], v[46:49]
	v_mfma_f32_16x16x32_bf16 v[50:53], v[22:25], v[54:57], 0
	v_mfma_f32_16x16x32_bf16 v[54:57], v[30:33], v[54:57], 0
	v_mfma_f32_16x16x32_bf16 v[50:53], v[26:29], v[58:61], v[50:53]
	v_mfma_f32_16x16x32_bf16 v[54:57], v[34:37], v[58:61], v[54:57]
	v_mfma_f32_16x16x32_bf16 v[58:61], v[22:25], v[62:65], 0
	v_mfma_f32_16x16x32_bf16 v[62:65], v[30:33], v[62:65], 0
	v_mfma_f32_16x16x32_bf16 v[58:61], v[26:29], v[66:69], v[58:61]
	v_mfma_f32_16x16x32_bf16 v[62:65], v[34:37], v[66:69], v[62:65]
	s_setprio 0
	s_barrier
	ds_read_b128 v[66:69], v4 offset:16384
	ds_read_b128 v[106:109], v4 offset:17408
	ds_read_b128 v[110:113], v4 offset:18432
	ds_read_b128 v[114:117], v4 offset:19456
	ds_read_b128 v[118:121], v4 offset:20480
	ds_read_b128 v[122:125], v4 offset:21504
	ds_read_b128 v[126:129], v4 offset:22528
	ds_read_b128 v[130:133], v4 offset:23552
	s_mov_b32 s55, m0
	s_mov_b32 m0, s44
	s_nop 2
	global_load_lds_dwordx4 v0, s[50:51]
	s_mov_b32 m0, s55
	s_nop 0
	s_mov_b32 s55, m0
	s_mov_b32 m0, s45
	s_nop 2
	global_load_lds_dwordx4 v1, s[50:51]
	s_mov_b32 m0, s55
	s_mov_b32 s50, m0
	s_mov_b32 m0, s48
	s_nop 2
	global_load_lds_dwordx4 v0, s[46:47]
	s_mov_b32 m0, s50
	s_nop 0
	s_mov_b32 s50, m0
	s_mov_b32 m0, s49
	s_nop 2
	global_load_lds_dwordx4 v1, s[46:47]
	s_mov_b32 m0, s50
	s_mov_b32 s46, m0
	s_mov_b32 m0, s2
	s_nop 2
	global_load_lds_dwordx4 v2, s[40:41]
	s_mov_b32 m0, s46
	s_nop 0
	s_mov_b32 s46, m0
	s_mov_b32 m0, s52
	s_nop 2
	global_load_lds_dwordx4 v3, s[40:41]
	s_mov_b32 m0, s46
	s_waitcnt vmcnt(8)
	s_waitcnt lgkmcnt(0)
	s_barrier
	s_setprio 1
	s_waitcnt lgkmcnt(7)
	v_mfma_f32_16x16x32_bf16 v[134:137], v[6:9], v[66:69], 0
	s_waitcnt lgkmcnt(5)
	v_mfma_f32_16x16x32_bf16 v[142:145], v[6:9], v[110:113], 0
	s_waitcnt vmcnt(2) lgkmcnt(3)
	v_mfma_f32_16x16x32_bf16 v[150:153], v[6:9], v[118:121], 0
	s_waitcnt lgkmcnt(1)
	v_mfma_f32_16x16x32_bf16 v[6:9], v[6:9], v[126:129], 0
	v_mfma_f32_16x16x32_bf16 v[134:137], v[10:13], v[106:109], v[134:137]
	v_mfma_f32_16x16x32_bf16 v[142:145], v[10:13], v[114:117], v[142:145]
	v_mfma_f32_16x16x32_bf16 v[150:153], v[10:13], v[122:125], v[150:153]
	s_waitcnt lgkmcnt(0)
	v_mfma_f32_16x16x32_bf16 v[6:9], v[10:13], v[130:133], v[6:9]
	v_mfma_f32_16x16x32_bf16 v[10:13], v[14:17], v[126:129], 0
	v_mfma_f32_16x16x32_bf16 v[138:141], v[14:17], v[66:69], 0
	s_waitcnt vmcnt(0)
	v_mfma_f32_16x16x32_bf16 v[146:149], v[14:17], v[110:113], 0
	v_mfma_f32_16x16x32_bf16 v[154:157], v[14:17], v[118:121], 0
	v_mfma_f32_16x16x32_bf16 v[10:13], v[18:21], v[130:133], v[10:13]
	v_mfma_f32_16x16x32_bf16 v[138:141], v[18:21], v[106:109], v[138:141]
	v_mfma_f32_16x16x32_bf16 v[146:149], v[18:21], v[114:117], v[146:149]
	v_mfma_f32_16x16x32_bf16 v[154:157], v[18:21], v[122:125], v[154:157]
	s_setprio 0
	s_setprio 1
	v_mfma_f32_16x16x32_bf16 v[14:17], v[22:25], v[66:69], 0
	v_mfma_f32_16x16x32_bf16 v[18:21], v[30:33], v[66:69], 0
	v_mfma_f32_16x16x32_bf16 v[14:17], v[26:29], v[106:109], v[14:17]
	v_mfma_f32_16x16x32_bf16 v[18:21], v[34:37], v[106:109], v[18:21]
	v_mfma_f32_16x16x32_bf16 v[66:69], v[22:25], v[110:113], 0
	v_mfma_f32_16x16x32_bf16 v[106:109], v[30:33], v[110:113], 0
	v_mfma_f32_16x16x32_bf16 v[110:113], v[22:25], v[118:121], 0
	v_mfma_f32_16x16x32_bf16 v[22:25], v[22:25], v[126:129], 0
	v_mfma_f32_16x16x32_bf16 v[66:69], v[26:29], v[114:117], v[66:69]
	v_mfma_f32_16x16x32_bf16 v[106:109], v[34:37], v[114:117], v[106:109]
	v_mfma_f32_16x16x32_bf16 v[110:113], v[26:29], v[122:125], v[110:113]
	v_mfma_f32_16x16x32_bf16 v[114:117], v[30:33], v[118:121], 0
	v_mfma_f32_16x16x32_bf16 v[22:25], v[26:29], v[130:133], v[22:25]
	v_mfma_f32_16x16x32_bf16 v[26:29], v[30:33], v[126:129], 0
	v_mfma_f32_16x16x32_bf16 v[114:117], v[34:37], v[122:125], v[114:117]
	v_mfma_f32_16x16x32_bf16 v[26:29], v[34:37], v[130:133], v[26:29]
	s_setprio 0
	s_barrier
	ds_read_b128 v[30:33], v222
	ds_read_b128 v[34:37], v222 offset:1024
	ds_read_b128 v[118:121], v222 offset:2048
	ds_read_b128 v[122:125], v222 offset:3072
	ds_read_b128 v[126:129], v5
	ds_read_b128 v[130:133], v5 offset:1024
	ds_read_b128 v[158:161], v5 offset:2048
	ds_read_b128 v[162:165], v5 offset:3072
	ds_read_b128 v[166:169], v4 offset:32768
	ds_read_b128 v[170:173], v4 offset:33792
	ds_read_b128 v[174:177], v4 offset:34816
	ds_read_b128 v[178:181], v4 offset:35840
	ds_read_b128 v[182:185], v4 offset:36864
	ds_read_b128 v[186:189], v4 offset:37888
	ds_read_b128 v[190:193], v4 offset:38912
	ds_read_b128 v[194:197], v4 offset:39936
	s_mov_b32 s40, m0
	s_mov_b32 m0, s42
	s_nop 2
	global_load_lds_dwordx4 v2, s[36:37]
	s_mov_b32 m0, s40
	s_nop 0
	s_mov_b32 s40, m0
	s_mov_b32 m0, s43
	s_nop 2
	global_load_lds_dwordx4 v3, s[36:37]
	s_mov_b32 m0, s40
	s_waitcnt vmcnt(8)
	s_waitcnt lgkmcnt(0)
	s_barrier
	s_setprio 1
	v_mfma_f32_16x16x32_bf16 v[70:73], v[30:33], v[166:169], v[70:73]
	v_mfma_f32_16x16x32_bf16 v[74:77], v[118:121], v[166:169], v[74:77]
	v_mfma_f32_16x16x32_bf16 v[78:81], v[30:33], v[174:177], v[78:81]
	v_mfma_f32_16x16x32_bf16 v[82:85], v[118:121], v[174:177], v[82:85]
	v_mfma_f32_16x16x32_bf16 v[86:89], v[30:33], v[182:185], v[86:89]
	v_mfma_f32_16x16x32_bf16 v[90:93], v[118:121], v[182:185], v[90:93]
	v_mfma_f32_16x16x32_bf16 v[94:97], v[30:33], v[190:193], v[94:97]
	v_mfma_f32_16x16x32_bf16 v[98:101], v[118:121], v[190:193], v[98:101]
	v_mfma_f32_16x16x32_bf16 v[70:73], v[34:37], v[170:173], v[70:73]
	v_mfma_f32_16x16x32_bf16 v[74:77], v[122:125], v[170:173], v[74:77]
	v_mfma_f32_16x16x32_bf16 v[78:81], v[34:37], v[178:181], v[78:81]
	v_mfma_f32_16x16x32_bf16 v[82:85], v[122:125], v[178:181], v[82:85]
	v_mfma_f32_16x16x32_bf16 v[86:89], v[34:37], v[186:189], v[86:89]
	v_mfma_f32_16x16x32_bf16 v[90:93], v[122:125], v[186:189], v[90:93]
	v_mfma_f32_16x16x32_bf16 v[94:97], v[34:37], v[194:197], v[94:97]
	v_mfma_f32_16x16x32_bf16 v[98:101], v[122:125], v[194:197], v[98:101]
	s_setprio 0
	s_setprio 1
	v_mfma_f32_16x16x32_bf16 v[102:105], v[126:129], v[166:169], v[102:105]
	v_mfma_f32_16x16x32_bf16 v[38:41], v[158:161], v[166:169], v[38:41]
	v_mfma_f32_16x16x32_bf16 v[42:45], v[126:129], v[174:177], v[42:45]
	v_mfma_f32_16x16x32_bf16 v[46:49], v[158:161], v[174:177], v[46:49]
	v_mfma_f32_16x16x32_bf16 v[50:53], v[126:129], v[182:185], v[50:53]
	v_mfma_f32_16x16x32_bf16 v[54:57], v[158:161], v[182:185], v[54:57]
	v_mfma_f32_16x16x32_bf16 v[58:61], v[126:129], v[190:193], v[58:61]
	v_mfma_f32_16x16x32_bf16 v[62:65], v[158:161], v[190:193], v[62:65]
	v_mfma_f32_16x16x32_bf16 v[102:105], v[130:133], v[170:173], v[102:105]
	v_mfma_f32_16x16x32_bf16 v[38:41], v[162:165], v[170:173], v[38:41]
	v_mfma_f32_16x16x32_bf16 v[42:45], v[130:133], v[178:181], v[42:45]
	v_mfma_f32_16x16x32_bf16 v[46:49], v[162:165], v[178:181], v[46:49]
	v_mfma_f32_16x16x32_bf16 v[50:53], v[130:133], v[186:189], v[50:53]
	v_mfma_f32_16x16x32_bf16 v[54:57], v[162:165], v[186:189], v[54:57]
	v_mfma_f32_16x16x32_bf16 v[58:61], v[130:133], v[194:197], v[58:61]
	v_mfma_f32_16x16x32_bf16 v[62:65], v[162:165], v[194:197], v[62:65]
	s_setprio 0
	s_barrier
	ds_read_b128 v[166:169], v4 offset:49152
	ds_read_b128 v[170:173], v4 offset:50176
	ds_read_b128 v[174:177], v4 offset:51200
	ds_read_b128 v[178:181], v4 offset:52224
	ds_read_b128 v[182:185], v4 offset:53248
	ds_read_b128 v[186:189], v4 offset:54272
	ds_read_b128 v[190:193], v4 offset:55296
	ds_read_b128 v[194:197], v4 offset:56320
	s_mov_b32 s36, m0
	s_mov_b32 m0, s9
	s_nop 2
	global_load_lds_dwordx4 v0, s[30:31]
	s_mov_b32 m0, s36
	s_nop 0
	s_mov_b32 s36, m0
	s_mov_b32 m0, s11
	s_nop 2
	global_load_lds_dwordx4 v1, s[30:31]
	s_mov_b32 m0, s36
	s_mov_b32 s30, m0
	s_mov_b32 m0, s3
	s_nop 2
	global_load_lds_dwordx4 v0, s[34:35]
	s_mov_b32 m0, s30
	s_nop 0
	s_mov_b32 s30, m0
	s_mov_b32 m0, s39
	s_nop 2
	global_load_lds_dwordx4 v1, s[34:35]
	s_mov_b32 m0, s30
	s_nop 0
	s_mov_b32 s30, m0
	s_mov_b32 m0, s33
	s_nop 2
	global_load_lds_dwordx4 v2, s[28:29]
	s_mov_b32 m0, s30
	s_nop 0
	s_mov_b32 s30, m0
	s_mov_b32 m0, s38
	s_nop 2
	global_load_lds_dwordx4 v3, s[28:29]
	s_mov_b32 m0, s30
	s_waitcnt vmcnt(8)
	s_waitcnt lgkmcnt(0)
	s_barrier
	s_setprio 1
	v_mfma_f32_16x16x32_bf16 v[6:9], v[30:33], v[190:193], v[6:9]
	v_mfma_f32_16x16x32_bf16 v[10:13], v[118:121], v[190:193], v[10:13]
	v_mfma_f32_16x16x32_bf16 v[134:137], v[30:33], v[166:169], v[134:137]
	v_mfma_f32_16x16x32_bf16 v[138:141], v[118:121], v[166:169], v[138:141]
	v_mfma_f32_16x16x32_bf16 v[142:145], v[30:33], v[174:177], v[142:145]
	v_mfma_f32_16x16x32_bf16 v[146:149], v[118:121], v[174:177], v[146:149]
	v_mfma_f32_16x16x32_bf16 v[150:153], v[30:33], v[182:185], v[150:153]
	v_mfma_f32_16x16x32_bf16 v[154:157], v[118:121], v[182:185], v[154:157]
	v_mfma_f32_16x16x32_bf16 v[6:9], v[34:37], v[194:197], v[6:9]
	v_mfma_f32_16x16x32_bf16 v[10:13], v[122:125], v[194:197], v[10:13]
	v_mfma_f32_16x16x32_bf16 v[134:137], v[34:37], v[170:173], v[134:137]
	v_mfma_f32_16x16x32_bf16 v[138:141], v[122:125], v[170:173], v[138:141]
	v_mfma_f32_16x16x32_bf16 v[142:145], v[34:37], v[178:181], v[142:145]
	v_mfma_f32_16x16x32_bf16 v[146:149], v[122:125], v[178:181], v[146:149]
	v_mfma_f32_16x16x32_bf16 v[150:153], v[34:37], v[186:189], v[150:153]
	v_mfma_f32_16x16x32_bf16 v[154:157], v[122:125], v[186:189], v[154:157]
	s_setprio 0
	s_setprio 1
	v_mfma_f32_16x16x32_bf16 v[14:17], v[126:129], v[166:169], v[14:17]
	v_mfma_f32_16x16x32_bf16 v[18:21], v[158:161], v[166:169], v[18:21]
	v_mfma_f32_16x16x32_bf16 v[30:33], v[126:129], v[174:177], v[66:69]
	v_mfma_f32_16x16x32_bf16 v[34:37], v[158:161], v[174:177], v[106:109]
	v_mfma_f32_16x16x32_bf16 v[66:69], v[126:129], v[182:185], v[110:113]
	v_mfma_f32_16x16x32_bf16 v[106:109], v[158:161], v[182:185], v[114:117]
	v_mfma_f32_16x16x32_bf16 v[22:25], v[126:129], v[190:193], v[22:25]
	v_mfma_f32_16x16x32_bf16 v[26:29], v[158:161], v[190:193], v[26:29]
	v_mfma_f32_16x16x32_bf16 v[14:17], v[130:133], v[170:173], v[14:17]
	v_mfma_f32_16x16x32_bf16 v[18:21], v[162:165], v[170:173], v[18:21]
	v_mfma_f32_16x16x32_bf16 v[30:33], v[130:133], v[178:181], v[30:33]
	v_mfma_f32_16x16x32_bf16 v[34:37], v[162:165], v[178:181], v[34:37]
	v_mfma_f32_16x16x32_bf16 v[66:69], v[130:133], v[186:189], v[66:69]
	v_mfma_f32_16x16x32_bf16 v[106:109], v[162:165], v[186:189], v[106:109]
	v_mfma_f32_16x16x32_bf16 v[22:25], v[130:133], v[194:197], v[22:25]
	v_mfma_f32_16x16x32_bf16 v[26:29], v[162:165], v[194:197], v[26:29]
	s_setprio 0
	s_barrier
	ds_read_b128 v[110:113], v198
	ds_read_b128 v[114:117], v198 offset:1024
	ds_read_b128 v[118:121], v198 offset:2048
	ds_read_b128 v[122:125], v198 offset:3072
	ds_read_b128 v[126:129], v199
	ds_read_b128 v[130:133], v199 offset:1024
	ds_read_b128 v[158:161], v199 offset:2048
	ds_read_b128 v[162:165], v199 offset:3072
	ds_read_b128 v[166:169], v4
	ds_read_b128 v[170:173], v4 offset:1024
	ds_read_b128 v[174:177], v4 offset:2048
	ds_read_b128 v[178:181], v4 offset:3072
	ds_read_b128 v[182:185], v4 offset:4096
	ds_read_b128 v[186:189], v4 offset:5120
	ds_read_b128 v[190:193], v4 offset:6144
	ds_read_b128 v[194:197], v4 offset:7168
	s_mov_b32 s28, m0
	s_mov_b32 m0, s53
	s_nop 2
	global_load_lds_dwordx4 v2, s[26:27]
	s_mov_b32 m0, s28
	s_nop 0
	s_mov_b32 s28, m0
	s_mov_b32 m0, s54
	s_nop 2
	global_load_lds_dwordx4 v3, s[26:27]
	s_mov_b32 m0, s28
	s_waitcnt vmcnt(8)
	s_waitcnt lgkmcnt(0)
	s_barrier
	s_setprio 1
	v_mfma_f32_16x16x32_bf16 v[90:93], v[118:121], v[182:185], v[90:93]
	v_mfma_f32_16x16x32_bf16 v[70:73], v[110:113], v[166:169], v[70:73]
	v_mfma_f32_16x16x32_bf16 v[74:77], v[118:121], v[166:169], v[74:77]
	v_mfma_f32_16x16x32_bf16 v[78:81], v[110:113], v[174:177], v[78:81]
	v_mfma_f32_16x16x32_bf16 v[82:85], v[118:121], v[174:177], v[82:85]
	v_mfma_f32_16x16x32_bf16 v[86:89], v[110:113], v[182:185], v[86:89]
	v_mfma_f32_16x16x32_bf16 v[198:201], v[122:125], v[186:189], v[90:93]
	v_mfma_f32_16x16x32_bf16 v[90:93], v[110:113], v[190:193], v[94:97]
	v_mfma_f32_16x16x32_bf16 v[70:73], v[114:117], v[170:173], v[70:73]
	v_mfma_f32_16x16x32_bf16 v[74:77], v[122:125], v[170:173], v[74:77]
	v_mfma_f32_16x16x32_bf16 v[78:81], v[114:117], v[178:181], v[78:81]
	v_mfma_f32_16x16x32_bf16 v[82:85], v[122:125], v[178:181], v[82:85]
	v_mfma_f32_16x16x32_bf16 v[86:89], v[114:117], v[186:189], v[86:89]
	v_mfma_f32_16x16x32_bf16 v[92:95], v[114:117], v[194:197], v[90:93]
	v_mfma_f32_16x16x32_bf16 v[96:99], v[118:121], v[190:193], v[98:101]
	v_mfma_f32_16x16x32_bf16 v[202:205], v[122:125], v[194:197], v[96:99]
	s_setprio 0
	s_setprio 1
	v_mfma_f32_16x16x32_bf16 v[46:49], v[158:161], v[174:177], v[46:49]
	v_mfma_f32_16x16x32_bf16 v[96:99], v[126:129], v[166:169], v[102:105]
	v_mfma_f32_16x16x32_bf16 v[38:41], v[158:161], v[166:169], v[38:41]
	v_mfma_f32_16x16x32_bf16 v[166:169], v[162:165], v[178:181], v[46:49]
	v_mfma_f32_16x16x32_bf16 v[46:49], v[126:129], v[182:185], v[50:53]
	v_mfma_f32_16x16x32_bf16 v[100:103], v[130:133], v[170:173], v[96:99]
	v_mfma_f32_16x16x32_bf16 v[38:41], v[162:165], v[170:173], v[38:41]
	v_mfma_f32_16x16x32_bf16 v[170:173], v[130:133], v[186:189], v[46:49]
	v_mfma_f32_16x16x32_bf16 v[46:49], v[158:161], v[182:185], v[54:57]
	v_mfma_f32_16x16x32_bf16 v[42:45], v[126:129], v[174:177], v[42:45]
	v_mfma_f32_16x16x32_bf16 v[52:55], v[162:165], v[186:189], v[46:49]
	v_mfma_f32_16x16x32_bf16 v[46:49], v[126:129], v[190:193], v[58:61]
	v_mfma_f32_16x16x32_bf16 v[42:45], v[130:133], v[178:181], v[42:45]
	v_mfma_f32_16x16x32_bf16 v[174:177], v[130:133], v[194:197], v[46:49]
	v_mfma_f32_16x16x32_bf16 v[46:49], v[158:161], v[190:193], v[62:65]
	v_mfma_f32_16x16x32_bf16 v[178:181], v[162:165], v[194:197], v[46:49]
	s_setprio 0
	s_barrier
	s_nop 4
	ds_read_b128 v[46:49], v4 offset:16384
	ds_read_b128 v[56:59], v4 offset:17408
	ds_read_b128 v[60:63], v4 offset:18432
	ds_read_b128 v[96:99], v4 offset:19456
	ds_read_b128 v[182:185], v4 offset:20480
	ds_read_b128 v[186:189], v4 offset:21504
	ds_read_b128 v[190:193], v4 offset:22528
	ds_read_b128 v[194:197], v4 offset:23552
	s_mov_b32 s26, m0
	s_mov_b32 m0, s44
	s_nop 2
	global_load_lds_dwordx4 v0, s[20:21]
	s_mov_b32 m0, s26
	s_nop 0
	s_mov_b32 s26, m0
	s_mov_b32 m0, s45
	s_nop 2
	global_load_lds_dwordx4 v1, s[20:21]
	s_mov_b32 m0, s26
	s_mov_b32 s20, m0
	s_mov_b32 m0, s48
	s_nop 2
	global_load_lds_dwordx4 v0, s[18:19]
	s_mov_b32 m0, s20
	s_nop 0
	s_mov_b32 s20, m0
	s_mov_b32 m0, s49
	s_nop 2
	global_load_lds_dwordx4 v1, s[18:19]
	s_mov_b32 m0, s20
	s_mov_b32 s18, m0
	s_mov_b32 m0, s2
	s_nop 2
	global_load_lds_dwordx4 v2, s[12:13]
	s_mov_b32 m0, s18
	s_mov_b32 s2, m0
	s_mov_b32 m0, s52
	s_nop 2
	global_load_lds_dwordx4 v3, s[12:13]
	s_mov_b32 m0, s2
	s_waitcnt vmcnt(8)
	s_waitcnt lgkmcnt(0)
	s_barrier
	s_setprio 1
	v_mfma_f32_16x16x32_bf16 v[6:9], v[110:113], v[190:193], v[6:9]
	v_mfma_f32_16x16x32_bf16 v[134:137], v[110:113], v[46:49], v[134:137]
	v_mfma_f32_16x16x32_bf16 v[138:141], v[118:121], v[46:49], v[138:141]
	v_mfma_f32_16x16x32_bf16 v[142:145], v[110:113], v[60:63], v[142:145]
	v_mfma_f32_16x16x32_bf16 v[146:149], v[118:121], v[60:63], v[146:149]
	v_mfma_f32_16x16x32_bf16 v[150:153], v[110:113], v[182:185], v[150:153]
	v_mfma_f32_16x16x32_bf16 v[154:157], v[118:121], v[182:185], v[154:157]
	v_mfma_f32_16x16x32_bf16 v[6:9], v[114:117], v[194:197], v[6:9]
	v_mfma_f32_16x16x32_bf16 v[10:13], v[118:121], v[190:193], v[10:13]
	v_mfma_f32_16x16x32_bf16 v[134:137], v[114:117], v[56:59], v[134:137]
	v_mfma_f32_16x16x32_bf16 v[138:141], v[122:125], v[56:59], v[138:141]
	v_mfma_f32_16x16x32_bf16 v[142:145], v[114:117], v[96:99], v[142:145]
	v_mfma_f32_16x16x32_bf16 v[146:149], v[122:125], v[96:99], v[146:149]
	v_mfma_f32_16x16x32_bf16 v[150:153], v[114:117], v[186:189], v[150:153]
	v_mfma_f32_16x16x32_bf16 v[154:157], v[122:125], v[186:189], v[154:157]
	v_mfma_f32_16x16x32_bf16 v[206:209], v[122:125], v[194:197], v[10:13]
	s_setprio 0
	s_setprio 1
	v_mfma_f32_16x16x32_bf16 v[10:13], v[126:129], v[46:49], v[14:17]
	v_mfma_f32_16x16x32_bf16 v[210:213], v[130:133], v[56:59], v[10:13]
	v_mfma_f32_16x16x32_bf16 v[10:13], v[158:161], v[46:49], v[18:21]
	v_mfma_f32_16x16x32_bf16 v[16:19], v[162:165], v[56:59], v[10:13]
	v_mfma_f32_16x16x32_bf16 v[10:13], v[126:129], v[60:63], v[30:33]
	v_mfma_f32_16x16x32_bf16 v[214:217], v[130:133], v[96:99], v[10:13]
	v_mfma_f32_16x16x32_bf16 v[10:13], v[158:161], v[60:63], v[34:37]
	v_mfma_f32_16x16x32_bf16 v[32:35], v[162:165], v[96:99], v[10:13]
	v_mfma_f32_16x16x32_bf16 v[10:13], v[126:129], v[182:185], v[66:69]
	v_mfma_f32_16x16x32_bf16 v[218:221], v[130:133], v[186:189], v[10:13]
	v_mfma_f32_16x16x32_bf16 v[10:13], v[158:161], v[182:185], v[106:109]
	v_mfma_f32_16x16x32_bf16 v[182:185], v[162:165], v[186:189], v[10:13]
	v_mfma_f32_16x16x32_bf16 v[10:13], v[126:129], v[190:193], v[22:25]
	v_mfma_f32_16x16x32_bf16 v[128:131], v[130:133], v[194:197], v[10:13]
	v_mfma_f32_16x16x32_bf16 v[10:13], v[158:161], v[190:193], v[26:29]
	v_mfma_f32_16x16x32_bf16 v[158:161], v[162:165], v[194:197], v[10:13]
	s_setprio 0
	s_barrier
	s_nop 4
	ds_read_b128 v[10:13], v222
	ds_read_b128 v[24:27], v222 offset:1024
	ds_read_b128 v[64:67], v222 offset:2048
	ds_read_b128 v[162:165], v222 offset:3072
	ds_read_b128 v[186:189], v5
	ds_read_b128 v[190:193], v5 offset:1024
	ds_read_b128 v[194:197], v5 offset:2048
	ds_read_b128 v[222:225], v5 offset:3072
	ds_read_b128 v[20:23], v4 offset:32768
	ds_read_b128 v[28:31], v4 offset:33792
	ds_read_b128 v[60:63], v4 offset:34816
	ds_read_b128 v[226:229], v4 offset:35840
	ds_read_b128 v[230:233], v4 offset:36864
	ds_read_b128 v[234:237], v4 offset:37888
	ds_read_b128 v[238:241], v4 offset:38912
	ds_read_b128 v[242:245], v4 offset:39936
	s_mov_b32 s2, m0
	s_mov_b32 m0, s42
	s_nop 2
	global_load_lds_dwordx4 v2, s[22:23]
	s_mov_b32 m0, s2
	s_nop 0
	s_mov_b32 s2, m0
	s_mov_b32 m0, s43
	s_nop 2
	global_load_lds_dwordx4 v3, s[22:23]
	s_mov_b32 m0, s2
	s_waitcnt vmcnt(8)
	s_waitcnt lgkmcnt(0)
	s_barrier
	s_setprio 1
	v_mfma_f32_16x16x32_bf16 v[46:49], v[10:13], v[20:23], v[70:73]
	v_mfma_f32_16x16x32_bf16 v[120:123], v[24:27], v[28:31], v[46:49]
	v_mfma_f32_16x16x32_bf16 v[46:49], v[64:67], v[20:23], v[74:77]
	v_mfma_f32_16x16x32_bf16 v[112:115], v[162:165], v[28:31], v[46:49]
	v_mfma_f32_16x16x32_bf16 v[46:49], v[10:13], v[60:63], v[78:81]
	v_mfma_f32_16x16x32_bf16 v[104:107], v[24:27], v[226:229], v[46:49]
	v_mfma_f32_16x16x32_bf16 v[46:49], v[64:67], v[60:63], v[82:85]
	v_mfma_f32_16x16x32_bf16 v[96:99], v[162:165], v[226:229], v[46:49]
	v_mfma_f32_16x16x32_bf16 v[46:49], v[10:13], v[230:233], v[86:89]
	v_mfma_f32_16x16x32_bf16 v[88:91], v[24:27], v[234:237], v[46:49]
	v_mfma_f32_16x16x32_bf16 v[46:49], v[64:67], v[230:233], v[198:201]
	v_mfma_f32_16x16x32_bf16 v[80:83], v[162:165], v[234:237], v[46:49]
	v_mfma_f32_16x16x32_bf16 v[46:49], v[10:13], v[238:241], v[92:95]
	v_mfma_f32_16x16x32_bf16 v[56:59], v[24:27], v[242:245], v[46:49]
	v_mfma_f32_16x16x32_bf16 v[46:49], v[64:67], v[238:241], v[202:205]
	v_mfma_f32_16x16x32_bf16 v[48:51], v[162:165], v[242:245], v[46:49]
	s_setprio 0
	s_setprio 1
	v_mfma_f32_16x16x32_bf16 v[68:71], v[186:189], v[20:23], v[100:103]
	v_mfma_f32_16x16x32_bf16 v[20:23], v[194:197], v[20:23], v[38:41]
	v_mfma_f32_16x16x32_bf16 v[116:119], v[222:225], v[28:31], v[20:23]
	v_mfma_f32_16x16x32_bf16 v[20:23], v[186:189], v[60:63], v[42:45]
	v_mfma_f32_16x16x32_bf16 v[108:111], v[190:193], v[226:229], v[20:23]
	v_mfma_f32_16x16x32_bf16 v[20:23], v[194:197], v[60:63], v[166:169]
	v_mfma_f32_16x16x32_bf16 v[100:103], v[222:225], v[226:229], v[20:23]
	v_mfma_f32_16x16x32_bf16 v[20:23], v[186:189], v[230:233], v[170:173]
	v_mfma_f32_16x16x32_bf16 v[92:95], v[190:193], v[234:237], v[20:23]
	v_mfma_f32_16x16x32_bf16 v[20:23], v[194:197], v[230:233], v[52:55]
	v_mfma_f32_16x16x32_bf16 v[84:87], v[222:225], v[234:237], v[20:23]
	v_mfma_f32_16x16x32_bf16 v[20:23], v[186:189], v[238:241], v[174:177]
	v_mfma_f32_16x16x32_bf16 v[60:63], v[190:193], v[242:245], v[20:23]
	v_mfma_f32_16x16x32_bf16 v[20:23], v[194:197], v[238:241], v[178:181]
	v_mfma_f32_16x16x32_bf16 v[124:127], v[190:193], v[28:31], v[68:71]
	v_mfma_f32_16x16x32_bf16 v[52:55], v[222:225], v[242:245], v[20:23]
	s_setprio 0
	s_barrier
	ds_read_b128 v[40:43], v4 offset:49152
	ds_read_b128 v[166:169], v4 offset:50176
	ds_read_b128 v[170:173], v4 offset:51200
	ds_read_b128 v[174:177], v4 offset:52224
	ds_read_b128 v[178:181], v4 offset:53248
	ds_read_b128 v[198:201], v4 offset:54272
	ds_read_b128 v[202:205], v4 offset:55296
	ds_read_b128 v[226:229], v4 offset:56320
	s_mov_b32 s2, m0
	s_mov_b32 m0, s9
	s_nop 2
	global_load_lds_dwordx4 v0, s[14:15]
	s_mov_b32 m0, s2
	s_nop 0
	s_mov_b32 s2, m0
	s_mov_b32 m0, s11
	s_nop 2
	global_load_lds_dwordx4 v1, s[14:15]
	s_mov_b32 m0, s2
	s_nop 0
	s_mov_b32 s2, m0
	s_mov_b32 m0, s3
	s_nop 2
	global_load_lds_dwordx4 v0, s[24:25]
	s_mov_b32 m0, s2
	s_nop 0
	s_mov_b32 s2, m0
	s_mov_b32 m0, s39
	s_nop 2
	global_load_lds_dwordx4 v1, s[24:25]
	s_mov_b32 m0, s2
	s_nop 0
	s_mov_b32 s2, m0
	s_mov_b32 m0, s33
	s_nop 2
	global_load_lds_dwordx4 v2, s[16:17]
	s_mov_b32 m0, s2
	s_nop 0
	s_mov_b32 s2, m0
	s_mov_b32 m0, s38
	s_nop 2
	global_load_lds_dwordx4 v3, s[16:17]
	s_mov_b32 m0, s2
	s_waitcnt vmcnt(8)
	s_waitcnt lgkmcnt(0)
	s_barrier
	s_setprio 1
	v_mfma_f32_16x16x32_bf16 v[0:3], v[10:13], v[40:43], v[134:137]
	v_mfma_f32_16x16x32_bf16 v[76:79], v[24:27], v[166:169], v[0:3]
	v_mfma_f32_16x16x32_bf16 v[0:3], v[64:67], v[40:43], v[138:141]
	v_mfma_f32_16x16x32_bf16 v[68:71], v[162:165], v[166:169], v[0:3]
	v_mfma_f32_16x16x32_bf16 v[0:3], v[10:13], v[170:173], v[142:145]
	v_mfma_f32_16x16x32_bf16 v[44:47], v[24:27], v[174:177], v[0:3]
	v_mfma_f32_16x16x32_bf16 v[0:3], v[64:67], v[170:173], v[146:149]
	v_mfma_f32_16x16x32_bf16 v[36:39], v[162:165], v[174:177], v[0:3]
	v_mfma_f32_16x16x32_bf16 v[0:3], v[10:13], v[178:181], v[150:153]
	v_mfma_f32_16x16x32_bf16 v[28:31], v[24:27], v[198:201], v[0:3]
	v_mfma_f32_16x16x32_bf16 v[0:3], v[64:67], v[178:181], v[154:157]
	v_mfma_f32_16x16x32_bf16 v[20:23], v[162:165], v[198:201], v[0:3]
	v_mfma_f32_16x16x32_bf16 v[0:3], v[10:13], v[202:205], v[6:9]
	v_mfma_f32_16x16x32_bf16 v[12:15], v[24:27], v[226:229], v[0:3]
	v_mfma_f32_16x16x32_bf16 v[0:3], v[64:67], v[202:205], v[206:209]
	v_mfma_f32_16x16x32_bf16 v[4:7], v[162:165], v[226:229], v[0:3]
	s_setprio 0
	s_setprio 1
	v_mfma_f32_16x16x32_bf16 v[0:3], v[186:189], v[40:43], v[210:213]
	v_mfma_f32_16x16x32_bf16 v[72:75], v[190:193], v[166:169], v[0:3]
	v_mfma_f32_16x16x32_bf16 v[0:3], v[194:197], v[40:43], v[16:19]
	v_mfma_f32_16x16x32_bf16 v[64:67], v[222:225], v[166:169], v[0:3]
	v_mfma_f32_16x16x32_bf16 v[0:3], v[186:189], v[170:173], v[214:217]
	v_mfma_f32_16x16x32_bf16 v[40:43], v[190:193], v[174:177], v[0:3]
	v_mfma_f32_16x16x32_bf16 v[0:3], v[194:197], v[170:173], v[32:35]
	v_mfma_f32_16x16x32_bf16 v[32:35], v[222:225], v[174:177], v[0:3]
	v_mfma_f32_16x16x32_bf16 v[0:3], v[186:189], v[178:181], v[218:221]
	v_mfma_f32_16x16x32_bf16 v[24:27], v[190:193], v[198:201], v[0:3]
	v_mfma_f32_16x16x32_bf16 v[0:3], v[194:197], v[178:181], v[182:185]
	v_mfma_f32_16x16x32_bf16 v[16:19], v[222:225], v[198:201], v[0:3]
	v_mfma_f32_16x16x32_bf16 v[0:3], v[186:189], v[202:205], v[128:131]
	v_mfma_f32_16x16x32_bf16 v[8:11], v[190:193], v[226:229], v[0:3]
	v_mfma_f32_16x16x32_bf16 v[0:3], v[194:197], v[202:205], v[158:161]
	v_mfma_f32_16x16x32_bf16 v[0:3], v[222:225], v[226:229], v[0:3]
	s_setprio 0
	s_barrier
	s_cbranch_scc1 .LBB0_1202
	s_barrier

.LBB0_1341:
	s_add_u32 s70, s0, s28
	s_addc_u32 s71, s1, s29
	s_add_u32 s36, s70, 0x100
	s_addc_u32 s37, s71, 0
	s_add_u32 s34, s8, s28
	s_addc_u32 s35, s9, s29
	s_add_u32 s34, s34, 0x100
	s_addc_u32 s35, s35, 0
	s_add_u32 s40, s10, s28
	v_add_u32_e32 v137, 0x10000, v134
	s_addc_u32 s41, s11, s29
	ds_read_b128 v[138:141], v137
	ds_read_b128 v[142:145], v137 offset:1024
	s_waitcnt vmcnt(0)
	ds_read_b128 v[146:149], v137 offset:2048
	ds_read_b128 v[150:153], v137 offset:3072
	v_add_u32_e32 v137, 0x14000, v134
	s_add_u32 s40, s40, 0x100
	ds_read_b128 v[154:157], v137
	ds_read_b128 v[158:161], v137 offset:1024
	ds_read_b128 v[162:165], v137 offset:2048
	ds_read_b128 v[166:169], v137 offset:3072
	s_addc_u32 s41, s41, 0
	s_cmp_eq_u32 s69, 12
	s_cselect_b32 s44, s66, s34
	s_cselect_b32 s45, s65, s35
	s_cselect_b32 s35, s67, s41
	s_cselect_b32 s34, s68, s40
	s_cselect_b32 s42, s19, s36
	s_cselect_b32 s43, s17, s37
	s_add_u32 s40, s44, 0x80
	s_addc_u32 s41, s45, 0
	s_add_u32 s36, s42, 0x80
	s_addc_u32 s37, s43, 0
	ds_read_b128 v[170:173], v135
	ds_read_b128 v[174:177], v135 offset:1024
	ds_read_b128 v[178:181], v135 offset:2048
	ds_read_b128 v[182:185], v135 offset:3072
	ds_read_b128 v[186:189], v135 offset:4096
	ds_read_b128 v[190:193], v135 offset:5120
	ds_read_b128 v[194:197], v135 offset:6144
	ds_read_b128 v[198:201], v135 offset:7168
	s_add_u32 s70, s70, 0x40080
	s_addc_u32 s71, s71, 0
	s_mov_b32 s72, m0
	s_mov_b32 m0, s62
	s_nop 2
	global_load_lds_dwordx4 v132, s[70:71]
	s_mov_b32 m0, s72
	s_nop 0
	s_mov_b32 s72, m0
	s_mov_b32 m0, s63
	s_nop 2
	global_load_lds_dwordx4 v133, s[70:71]
	s_mov_b32 m0, s72
	s_waitcnt vmcnt(8)
	s_waitcnt lgkmcnt(0)
	s_barrier
	s_setprio 1
	v_mfma_scale_f32_16x16x128_f8f6f4 v[96:99], v[146:153], v[178:185], v[96:99], v136, v136 op_sel_hi:[0,0,0]
	v_mfma_scale_f32_16x16x128_f8f6f4 v[120:123], v[138:145], v[186:193], v[120:123], v136, v136 op_sel_hi:[0,0,0]
	v_mfma_scale_f32_16x16x128_f8f6f4 v[124:127], v[146:153], v[186:193], v[124:127], v136, v136 op_sel_hi:[0,0,0]
	v_mfma_scale_f32_16x16x128_f8f6f4 v[100:103], v[138:145], v[194:201], v[100:103], v136, v136 op_sel_hi:[0,0,0]
	v_mfma_scale_f32_16x16x128_f8f6f4 v[202:205], v[138:145], v[170:177], v[64:67], v136, v136 op_sel_hi:[0,0,0]
	v_mfma_scale_f32_16x16x128_f8f6f4 v[206:209], v[146:153], v[170:177], v[72:75], v136, v136 op_sel_hi:[0,0,0]
	v_mfma_scale_f32_16x16x128_f8f6f4 v[210:213], v[138:145], v[178:185], v[88:91], v136, v136 op_sel_hi:[0,0,0]
	v_mfma_scale_f32_16x16x128_f8f6f4 v[214:217], v[146:153], v[194:201], v[92:95], v136, v136 op_sel_hi:[0,0,0]
	s_setprio 0
	s_setprio 1
	v_mfma_scale_f32_16x16x128_f8f6f4 v[108:111], v[154:161], v[178:185], v[108:111], v136, v136 op_sel_hi:[0,0,0]
	v_mfma_scale_f32_16x16x128_f8f6f4 v[112:115], v[162:169], v[178:185], v[112:115], v136, v136 op_sel_hi:[0,0,0]
	v_mfma_scale_f32_16x16x128_f8f6f4 v[116:119], v[154:161], v[186:193], v[116:119], v136, v136 op_sel_hi:[0,0,0]
	v_mfma_scale_f32_16x16x128_f8f6f4 v[104:107], v[162:169], v[186:193], v[104:107], v136, v136 op_sel_hi:[0,0,0]
	v_mfma_scale_f32_16x16x128_f8f6f4 v[218:221], v[154:161], v[170:177], v[80:83], v136, v136 op_sel_hi:[0,0,0]
	v_mfma_scale_f32_16x16x128_f8f6f4 v[170:173], v[162:169], v[170:177], v[84:87], v136, v136 op_sel_hi:[0,0,0]
	v_mfma_scale_f32_16x16x128_f8f6f4 v[174:177], v[154:161], v[194:201], v[76:79], v136, v136 op_sel_hi:[0,0,0]
	v_mfma_scale_f32_16x16x128_f8f6f4 v[178:181], v[162:169], v[194:201], v[68:71], v136, v136 op_sel_hi:[0,0,0]
	s_setprio 0
	s_barrier
	ds_read_b128 v[64:67], v135 offset:16384
	s_nop 3
	ds_read_b128 v[68:71], v135 offset:17408
	ds_read_b128 v[72:75], v135 offset:18432
	ds_read_b128 v[76:79], v135 offset:19456
	ds_read_b128 v[80:83], v135 offset:20480
	ds_read_b128 v[84:87], v135 offset:21504
	ds_read_b128 v[88:91], v135 offset:22528
	ds_read_b128 v[92:95], v135 offset:23552
	s_mov_b32 s70, m0
	s_mov_b32 m0, s49
	s_nop 2
	global_load_lds_dwordx4 v130, s[44:45]
	s_mov_b32 m0, s70
	s_nop 0
	s_mov_b32 s70, m0
	s_mov_b32 m0, s50
	s_nop 2
	global_load_lds_dwordx4 v131, s[44:45]
	s_mov_b32 m0, s70
	s_mov_b32 s44, m0
	s_mov_b32 m0, s51
	s_nop 2
	global_load_lds_dwordx4 v130, s[34:35]
	s_mov_b32 m0, s44
	s_nop 0
	s_mov_b32 s44, m0
	s_mov_b32 m0, s52
	s_nop 2
	global_load_lds_dwordx4 v131, s[34:35]
	s_mov_b32 m0, s44
	s_nop 0
	s_mov_b32 s44, m0
	s_mov_b32 m0, s47
	s_nop 2
	global_load_lds_dwordx4 v132, s[42:43]
	s_mov_b32 m0, s44
	s_nop 0
	s_mov_b32 s44, m0
	s_mov_b32 m0, s53
	s_nop 2
	global_load_lds_dwordx4 v133, s[42:43]
	s_mov_b32 m0, s44
	s_waitcnt vmcnt(8)
	s_waitcnt lgkmcnt(0)
	s_barrier
	s_setprio 1
	v_mfma_scale_f32_16x16x128_f8f6f4 v[60:63], v[138:145], v[64:71], v[60:63], v136, v136 op_sel_hi:[0,0,0]
	v_mfma_scale_f32_16x16x128_f8f6f4 v[56:59], v[146:153], v[64:71], v[56:59], v136, v136 op_sel_hi:[0,0,0]
	v_mfma_scale_f32_16x16x128_f8f6f4 v[182:185], v[138:145], v[72:79], v[44:47], v136, v136 op_sel_hi:[0,0,0]
	v_mfma_scale_f32_16x16x128_f8f6f4 v[186:189], v[146:153], v[72:79], v[40:43], v136, v136 op_sel_hi:[0,0,0]
	v_mfma_scale_f32_16x16x128_f8f6f4 v[190:193], v[138:145], v[80:87], v[24:27], v136, v136 op_sel_hi:[0,0,0]
	v_mfma_scale_f32_16x16x128_f8f6f4 v[194:197], v[146:153], v[80:87], v[16:19], v136, v136 op_sel_hi:[0,0,0]
	v_mfma_scale_f32_16x16x128_f8f6f4 v[198:201], v[138:145], v[88:95], v[4:7], v136, v136 op_sel_hi:[0,0,0]
	v_mfma_scale_f32_16x16x128_f8f6f4 v[222:225], v[146:153], v[88:95], v[0:3], v136, v136 op_sel_hi:[0,0,0]
	s_setprio 0
	s_setprio 1
	v_mfma_scale_f32_16x16x128_f8f6f4 v[52:55], v[154:161], v[64:71], v[52:55], v136, v136 op_sel_hi:[0,0,0]
	v_mfma_scale_f32_16x16x128_f8f6f4 v[48:51], v[162:169], v[64:71], v[48:51], v136, v136 op_sel_hi:[0,0,0]
	v_mfma_scale_f32_16x16x128_f8f6f4 v[226:229], v[154:161], v[72:79], v[36:39], v136, v136 op_sel_hi:[0,0,0]
	v_mfma_scale_f32_16x16x128_f8f6f4 v[230:233], v[162:169], v[72:79], v[20:23], v136, v136 op_sel_hi:[0,0,0]
	v_mfma_scale_f32_16x16x128_f8f6f4 v[234:237], v[154:161], v[80:87], v[32:35], v136, v136 op_sel_hi:[0,0,0]
	v_mfma_scale_f32_16x16x128_f8f6f4 v[238:241], v[162:169], v[80:87], v[28:31], v136, v136 op_sel_hi:[0,0,0]
	v_mfma_scale_f32_16x16x128_f8f6f4 v[242:245], v[154:161], v[88:95], v[12:15], v136, v136 op_sel_hi:[0,0,0]
	v_mfma_scale_f32_16x16x128_f8f6f4 v[246:249], v[162:169], v[88:95], v[8:11], v136, v136 op_sel_hi:[0,0,0]
	s_setprio 0
	s_barrier
	s_nop 3
	v_add_u32_e32 v12, 0x18000, v134
	v_add_u32_e32 v16, 0x1c000, v134
	ds_read_b128 v[0:3], v12
	ds_read_b128 v[4:7], v12 offset:1024
	ds_read_b128 v[8:11], v12 offset:2048
	ds_read_b128 v[12:15], v12 offset:3072
	ds_read_b128 v[138:141], v16
	ds_read_b128 v[142:145], v16 offset:1024
	ds_read_b128 v[146:149], v16 offset:2048
	ds_read_b128 v[150:153], v16 offset:3072
	ds_read_b128 v[16:19], v135 offset:32768
	ds_read_b128 v[20:23], v135 offset:33792
	ds_read_b128 v[24:27], v135 offset:34816
	ds_read_b128 v[28:31], v135 offset:35840
	ds_read_b128 v[32:35], v135 offset:36864
	ds_read_b128 v[36:39], v135 offset:37888
	ds_read_b128 v[40:43], v135 offset:38912
	ds_read_b128 v[44:47], v135 offset:39936
	s_add_u32 s42, s42, 0x40000
	s_addc_u32 s43, s43, 0
	s_mov_b32 s44, m0
	s_mov_b32 m0, s54
	s_nop 2
	global_load_lds_dwordx4 v132, s[42:43]
	s_mov_b32 m0, s44
	s_nop 0
	s_mov_b32 s44, m0
	s_mov_b32 m0, s55
	s_nop 2
	global_load_lds_dwordx4 v133, s[42:43]
	s_mov_b32 m0, s44
	s_waitcnt vmcnt(8)
	s_waitcnt lgkmcnt(0)
	s_barrier
	s_setprio 1
	v_mfma_scale_f32_16x16x128_f8f6f4 v[64:67], v[0:7], v[16:23], v[202:205], v136, v136 op_sel_hi:[0,0,0]
	v_mfma_scale_f32_16x16x128_f8f6f4 v[72:75], v[8:15], v[16:23], v[206:209], v136, v136 op_sel_hi:[0,0,0]
	v_mfma_scale_f32_16x16x128_f8f6f4 v[88:91], v[0:7], v[24:31], v[210:213], v136, v136 op_sel_hi:[0,0,0]
	v_mfma_scale_f32_16x16x128_f8f6f4 v[96:99], v[8:15], v[24:31], v[96:99], v136, v136 op_sel_hi:[0,0,0]
	v_mfma_scale_f32_16x16x128_f8f6f4 v[120:123], v[0:7], v[32:39], v[120:123], v136, v136 op_sel_hi:[0,0,0]
	v_mfma_scale_f32_16x16x128_f8f6f4 v[124:127], v[8:15], v[32:39], v[124:127], v136, v136 op_sel_hi:[0,0,0]
	v_mfma_scale_f32_16x16x128_f8f6f4 v[100:103], v[0:7], v[40:47], v[100:103], v136, v136 op_sel_hi:[0,0,0]
	v_mfma_scale_f32_16x16x128_f8f6f4 v[92:95], v[8:15], v[40:47], v[214:217], v136, v136 op_sel_hi:[0,0,0]
	s_setprio 0
	s_setprio 1
	v_mfma_scale_f32_16x16x128_f8f6f4 v[80:83], v[138:145], v[16:23], v[218:221], v136, v136 op_sel_hi:[0,0,0]
	v_mfma_scale_f32_16x16x128_f8f6f4 v[84:87], v[146:153], v[16:23], v[170:173], v136, v136 op_sel_hi:[0,0,0]
	v_mfma_scale_f32_16x16x128_f8f6f4 v[108:111], v[138:145], v[24:31], v[108:111], v136, v136 op_sel_hi:[0,0,0]
	v_mfma_scale_f32_16x16x128_f8f6f4 v[112:115], v[146:153], v[24:31], v[112:115], v136, v136 op_sel_hi:[0,0,0]
	v_mfma_scale_f32_16x16x128_f8f6f4 v[116:119], v[138:145], v[32:39], v[116:119], v136, v136 op_sel_hi:[0,0,0]
	v_mfma_scale_f32_16x16x128_f8f6f4 v[104:107], v[146:153], v[32:39], v[104:107], v136, v136 op_sel_hi:[0,0,0]
	v_mfma_scale_f32_16x16x128_f8f6f4 v[76:79], v[138:145], v[40:47], v[174:177], v136, v136 op_sel_hi:[0,0,0]
	v_mfma_scale_f32_16x16x128_f8f6f4 v[68:71], v[146:153], v[40:47], v[178:181], v136, v136 op_sel_hi:[0,0,0]
	s_setprio 0
	s_barrier
	ds_read_b128 v[28:31], v135 offset:49152
	ds_read_b128 v[32:35], v135 offset:50176
	ds_read_b128 v[154:157], v135 offset:51200
	ds_read_b128 v[158:161], v135 offset:52224
	ds_read_b128 v[162:165], v135 offset:53248
	ds_read_b128 v[166:169], v135 offset:54272
	ds_read_b128 v[170:173], v135 offset:55296
	ds_read_b128 v[174:177], v135 offset:56320
	s_mov_b32 s42, m0
	s_mov_b32 m0, s56
	s_nop 2
	global_load_lds_dwordx4 v130, s[40:41]
	s_mov_b32 m0, s42
	s_add_u32 s34, s34, 0x80
	s_mov_b32 s42, m0
	s_mov_b32 m0, s57
	s_nop 2
	global_load_lds_dwordx4 v131, s[40:41]
	s_mov_b32 m0, s42
	s_addc_u32 s35, s35, 0
	s_mov_b32 s40, m0
	s_mov_b32 m0, s60
	s_nop 2
	global_load_lds_dwordx4 v130, s[34:35]
	s_mov_b32 m0, s40
	s_nop 0
	s_mov_b32 s40, m0
	s_mov_b32 m0, s61
	s_nop 2
	global_load_lds_dwordx4 v131, s[34:35]
	s_mov_b32 m0, s40
	s_mov_b32 s34, m0
	s_mov_b32 m0, s58
	s_nop 2
	global_load_lds_dwordx4 v132, s[36:37]
	s_mov_b32 m0, s34
	s_nop 0
	s_mov_b32 s34, m0
	s_mov_b32 m0, s59
	s_nop 2
	global_load_lds_dwordx4 v133, s[36:37]
	s_mov_b32 m0, s34
	s_waitcnt vmcnt(8)
	s_waitcnt lgkmcnt(0)
	s_barrier
	s_setprio 1
	v_mfma_scale_f32_16x16x128_f8f6f4 v[60:63], v[0:7], v[28:35], v[60:63], v136, v136 op_sel_hi:[0,0,0]
	v_mfma_scale_f32_16x16x128_f8f6f4 v[56:59], v[8:15], v[28:35], v[56:59], v136, v136 op_sel_hi:[0,0,0]
	v_mfma_scale_f32_16x16x128_f8f6f4 v[44:47], v[0:7], v[154:161], v[182:185], v136, v136 op_sel_hi:[0,0,0]
	v_mfma_scale_f32_16x16x128_f8f6f4 v[40:43], v[8:15], v[154:161], v[186:189], v136, v136 op_sel_hi:[0,0,0]
	v_mfma_scale_f32_16x16x128_f8f6f4 v[24:27], v[0:7], v[162:169], v[190:193], v136, v136 op_sel_hi:[0,0,0]
	v_mfma_scale_f32_16x16x128_f8f6f4 v[16:19], v[8:15], v[162:169], v[194:197], v136, v136 op_sel_hi:[0,0,0]
	v_mfma_scale_f32_16x16x128_f8f6f4 v[4:7], v[0:7], v[170:177], v[198:201], v136, v136 op_sel_hi:[0,0,0]
	v_mfma_scale_f32_16x16x128_f8f6f4 v[0:3], v[8:15], v[170:177], v[222:225], v136, v136 op_sel_hi:[0,0,0]
	s_setprio 0
	s_setprio 1
	v_mfma_scale_f32_16x16x128_f8f6f4 v[52:55], v[138:145], v[28:35], v[52:55], v136, v136 op_sel_hi:[0,0,0]
	v_mfma_scale_f32_16x16x128_f8f6f4 v[48:51], v[146:153], v[28:35], v[48:51], v136, v136 op_sel_hi:[0,0,0]
	v_mfma_scale_f32_16x16x128_f8f6f4 v[36:39], v[138:145], v[154:161], v[226:229], v136, v136 op_sel_hi:[0,0,0]
	v_mfma_scale_f32_16x16x128_f8f6f4 v[20:23], v[146:153], v[154:161], v[230:233], v136, v136 op_sel_hi:[0,0,0]
	v_mfma_scale_f32_16x16x128_f8f6f4 v[32:35], v[138:145], v[162:169], v[234:237], v136, v136 op_sel_hi:[0,0,0]
	v_mfma_scale_f32_16x16x128_f8f6f4 v[28:31], v[146:153], v[162:169], v[238:241], v136, v136 op_sel_hi:[0,0,0]
	v_mfma_scale_f32_16x16x128_f8f6f4 v[12:15], v[138:145], v[170:177], v[242:245], v136, v136 op_sel_hi:[0,0,0]
	v_mfma_scale_f32_16x16x128_f8f6f4 v[8:11], v[146:153], v[170:177], v[246:249], v136, v136 op_sel_hi:[0,0,0]
	s_setprio 0
	s_barrier
	s_add_i32 s69, s69, 2
	s_add_u32 s28, s28, 0x100
	s_addc_u32 s29, s29, 0
	s_cmp_gt_u32 s69, 13
	s_cbranch_scc0 .LBB0_1341
	s_and_b64 vcc, exec, s[14:15]
	s_cbranch_vccnz .LBB0_1344
	s_andn2_b64 vcc, exec, s[30:31]
	s_cbranch_vccnz .LBB0_1331
	s_branch .LBB0_1345
